# MoE weight conversion reads (f32, read once) marked nt; GEMM K-loops DMA-first, no per-phase setprio
# speedup vs baseline: 1.0225x; 1.0159x over previous
; #define GM_STAGE(bufoff, gbase, voff) do { _Pragma("unroll") for (int _i = 0; _i < 2; ++_i) \
;         __builtin_amdgcn_global_load_lds((const unsigned*)((const char*)(gbase) + (voff)[_i]), (LAS unsigned*)(lds + (bufoff) + ldsw + _i * 8192), 16, 0, 0); } while (0)
; #define GM_LDA(dst, b, h) do { _Pragma("unroll") for (int m = 0; m < 4; ++m) _Pragma("unroll") for (int k = 0; k < 2; ++k) dst[m][k] = *(const LAS s16x8*)(lds + GM_SA(b, h) + aoff + m * 2048 + k * 1024); } while (0)
; #define GM_LDB(dst, b, h) do { _Pragma("unroll") for (int n = 0; n < 2; ++n) _Pragma("unroll") for (int k = 0; k < 2; ++k) dst[n][k] = *(const LAS s16x8*)(lds + GM_SB(b, h) + boff + n * 2048 + k * 1024); } while (0)
; #define GM_MMA(ai, bj, At, Bt) do { __builtin_amdgcn_s_setprio(1); _Pragma("unroll") for (int m = 0; m < 4; ++m) _Pragma("unroll") for (int n = 0; n < 2; ++n) _Pragma("unroll") for (int k = 0; k < 2; ++k) \
;         acc[ai][bj][m][n] = mma16<BF>(Bt[n][k], At[m][k], acc[ai][bj][m][n]); __builtin_amdgcn_s_setprio(0); } while (0)
; #define GM_WAIT_V(n) asm volatile("s_waitcnt vmcnt(" #n ")" ::: "memory")
; #define GM_WAIT_L(n) asm volatile("s_waitcnt lgkmcnt(" #n ")" ::: "memory")
; #define GM_BAR __builtin_amdgcn_s_barrier()
; template <bool BF, bool GATHER = false, class Epi, class Hook>
; __device__ __forceinline__ void gemm_phase(LAS unsigned char* lds, const Gemm g, const Order& S, const Epi& E, Hook& HK) {
;     ...
;             const char* a1 = cA + (size_t)(t + 1) * kstep;
;             const char* a2 = last ? nA : cA + (size_t)(t + 2) * kstep; const char* b2 = last ? nB : cB + (size_t)(t + 2) * kstep;
;             const char* a3 = a2 + kstep; const char* b3 = b2 + kstep;
;             unsigned s0[2], s1[2];
;             if constexpr (GATHER) { s0[0] = last ? nA0[0] : gA0[0]; s0[1] = last ? nA0[1] : gA0[1]; s1[0] = last ? nA1[0] : gA1[0]; s1[1] = last ? nA1[1] : gA1[1]; }
;             GM_LDB(B0, 0, 0); GM_LDB(B1, 0, 1); GM_SCHED; GM_LDA(At, 0, 0); GM_STA_H1(GM_SA(1, 1), a1, gA1);
;             GM_WAIT_V(8); GM_WAIT_L(0); GM_BAR; GM_MMA(0, 0, At, B0); GM_MMA(0, 1, At, B1); GM_BAR; GM_SCHED;
;             GM_LDA(At, 0, 1); GM_STAGE(GM_SB(0, 0), b2, voffB); GM_STAGE(GM_SB(0, 1), b2 + hstepB, voffB); GM_STA_H0(GM_SA(0, 0), a2, s0);
;             GM_WAIT_V(8); GM_WAIT_L(0); GM_BAR; GM_MMA(1, 0, At, B0); GM_MMA(1, 1, At, B1); GM_BAR; GM_SCHED;
.LBB0_380:
	s_add_u32 s28, s2, 0xfffc0080
	s_addc_u32 s29, s3, -1
	s_cmp_eq_u32 s51, 12
	s_cselect_b32 s31, s9, s29
	s_cselect_b32 s30, s19, s28
	s_cselect_b32 s29, s21, s50
	s_cselect_b32 s28, s48, s49
	v_lshl_add_u64 v[150:151], s[2:3], 0, v[138:139]
	s_add_i32 m0, s27, 0xc000
	global_load_lds_dwordx4 v[150:151], off
	v_lshl_add_u64 v[150:151], s[2:3], 0, v[140:141]
	s_add_i32 m0, s27, 0xe000
	s_nop 0
	global_load_lds_dwordx4 v[150:151], off
	ds_read_b128 v[146:149], v158
	ds_read_b128 v[162:165], v158 offset:1024
	ds_read_b128 v[166:169], v158 offset:2048
	ds_read_b128 v[170:173], v158 offset:3072
	ds_read_b128 v[174:177], v159
	ds_read_b128 v[178:181], v159 offset:1024
	ds_read_b128 v[182:185], v159 offset:2048
	ds_read_b128 v[186:189], v159 offset:3072
	ds_read_b128 v[190:193], v160
	ds_read_b128 v[194:197], v160 offset:1024
	ds_read_b128 v[198:201], v160 offset:2048
	ds_read_b128 v[202:205], v160 offset:3072
	ds_read_b128 v[206:209], v160 offset:4096
	ds_read_b128 v[210:213], v160 offset:5120
	ds_read_b128 v[214:217], v160 offset:6144
	ds_read_b128 v[218:221], v160 offset:7168
	s_waitcnt vmcnt(8)
	s_waitcnt lgkmcnt(0)
	s_barrier
	s_waitcnt lgkmcnt(0)
	v_mfma_f32_16x16x32_f16 v[126:129], v[146:149], v[190:193], v[126:129]
	v_mfma_f32_16x16x32_f16 v[122:125], v[166:169], v[190:193], v[122:125]
	v_mfma_f32_16x16x32_f16 v[110:113], v[146:149], v[198:201], v[110:113]
	v_mfma_f32_16x16x32_f16 v[106:109], v[166:169], v[198:201], v[106:109]
	v_mfma_f32_16x16x32_f16 v[94:97], v[146:149], v[206:209], v[94:97]
	v_mfma_f32_16x16x32_f16 v[90:93], v[166:169], v[206:209], v[90:93]
	v_mfma_f32_16x16x32_f16 v[78:81], v[146:149], v[214:217], v[78:81]
	v_mfma_f32_16x16x32_f16 v[74:77], v[166:169], v[214:217], v[74:77]
	v_mfma_f32_16x16x32_f16 v[126:129], v[162:165], v[194:197], v[126:129]
	v_mfma_f32_16x16x32_f16 v[122:125], v[170:173], v[194:197], v[122:125]
	v_mfma_f32_16x16x32_f16 v[110:113], v[162:165], v[202:205], v[110:113]
	v_mfma_f32_16x16x32_f16 v[106:109], v[170:173], v[202:205], v[106:109]
	v_mfma_f32_16x16x32_f16 v[94:97], v[162:165], v[210:213], v[94:97]
	v_mfma_f32_16x16x32_f16 v[90:93], v[170:173], v[210:213], v[90:93]
	v_mfma_f32_16x16x32_f16 v[78:81], v[162:165], v[218:221], v[78:81]
	v_mfma_f32_16x16x32_f16 v[74:77], v[170:173], v[218:221], v[74:77]
	v_mfma_f32_16x16x32_f16 v[118:121], v[174:177], v[190:193], v[118:121]
	v_mfma_f32_16x16x32_f16 v[114:117], v[182:185], v[190:193], v[114:117]
	v_mfma_f32_16x16x32_f16 v[102:105], v[174:177], v[198:201], v[102:105]
	v_mfma_f32_16x16x32_f16 v[98:101], v[182:185], v[198:201], v[98:101]
	v_mfma_f32_16x16x32_f16 v[86:89], v[174:177], v[206:209], v[86:89]
	v_mfma_f32_16x16x32_f16 v[82:85], v[182:185], v[206:209], v[82:85]
	v_mfma_f32_16x16x32_f16 v[70:73], v[174:177], v[214:217], v[70:73]
	v_mfma_f32_16x16x32_f16 v[66:69], v[182:185], v[214:217], v[66:69]
	v_mfma_f32_16x16x32_f16 v[118:121], v[178:181], v[194:197], v[118:121]
	v_mfma_f32_16x16x32_f16 v[114:117], v[186:189], v[194:197], v[114:117]
	v_mfma_f32_16x16x32_f16 v[102:105], v[178:181], v[202:205], v[102:105]
	v_mfma_f32_16x16x32_f16 v[98:101], v[186:189], v[202:205], v[98:101]
	v_mfma_f32_16x16x32_f16 v[86:89], v[178:181], v[210:213], v[86:89]
	v_mfma_f32_16x16x32_f16 v[82:85], v[186:189], v[210:213], v[82:85]
	v_mfma_f32_16x16x32_f16 v[70:73], v[178:181], v[218:221], v[70:73]
	v_mfma_f32_16x16x32_f16 v[66:69], v[186:189], v[218:221], v[66:69]
	s_barrier
	s_add_i32 s52, s45, s35
	v_lshl_add_u64 v[150:151], s[28:29], 0, v[132:133]
	s_mov_b32 m0, s52
	global_load_lds_dwordx4 v[150:151], off
	s_add_i32 m0, s52, 0x2000
	s_add_u32 s52, s28, 0x40000
	v_lshl_add_u64 v[222:223], s[28:29], 0, v[136:137]
	s_addc_u32 s53, s29, 0
	s_add_i32 s54, s46, s35
	global_load_lds_dwordx4 v[222:223], off
	v_lshl_add_u64 v[224:225], s[52:53], 0, v[132:133]
	s_mov_b32 m0, s54
	v_lshl_add_u64 v[226:227], s[30:31], 0, v[134:135]
	global_load_lds_dwordx4 v[224:225], off
	v_lshl_add_u64 v[224:225], s[52:53], 0, v[136:137]
	s_add_i32 m0, s54, 0x2000
	s_nop 0
	global_load_lds_dwordx4 v[224:225], off
	v_lshl_add_u64 v[224:225], s[30:31], 0, v[130:131]
	s_mov_b32 m0, s27
	s_nop 0
	global_load_lds_dwordx4 v[224:225], off
	s_mov_b32 m0, s36
	s_nop 0
	global_load_lds_dwordx4 v[226:227], off
	ds_read_b128 v[190:193], v160 offset:16384
	ds_read_b128 v[194:197], v160 offset:17408
	ds_read_b128 v[198:201], v160 offset:18432
	ds_read_b128 v[202:205], v160 offset:19456
	ds_read_b128 v[206:209], v160 offset:20480
	ds_read_b128 v[210:213], v160 offset:21504
	ds_read_b128 v[214:217], v160 offset:22528
	ds_read_b128 v[218:221], v160 offset:23552
	s_waitcnt vmcnt(8)
	s_waitcnt lgkmcnt(0)
	s_barrier
; #define GM_STAGE(bufoff, gbase, voff) do { _Pragma("unroll") for (int _i = 0; _i < 2; ++_i) \
;         __builtin_amdgcn_global_load_lds((const unsigned*)((const char*)(gbase) + (voff)[_i]), (LAS unsigned*)(lds + (bufoff) + ldsw + _i * 8192), 16, 0, 0); } while (0)
; #define GM_LDA(dst, b, h) do { _Pragma("unroll") for (int m = 0; m < 4; ++m) _Pragma("unroll") for (int k = 0; k < 2; ++k) dst[m][k] = *(const LAS s16x8*)(lds + GM_SA(b, h) + aoff + m * 2048 + k * 1024); } while (0)
; #define GM_LDB(dst, b, h) do { _Pragma("unroll") for (int n = 0; n < 2; ++n) _Pragma("unroll") for (int k = 0; k < 2; ++k) dst[n][k] = *(const LAS s16x8*)(lds + GM_SB(b, h) + boff + n * 2048 + k * 1024); } while (0)
; #define GM_MMA(ai, bj, At, Bt) do { __builtin_amdgcn_s_setprio(1); _Pragma("unroll") for (int m = 0; m < 4; ++m) _Pragma("unroll") for (int n = 0; n < 2; ++n) _Pragma("unroll") for (int k = 0; k < 2; ++k) \
;         acc[ai][bj][m][n] = mma16<BF>(Bt[n][k], At[m][k], acc[ai][bj][m][n]); __builtin_amdgcn_s_setprio(0); } while (0)
; #define GM_WAIT_V(n) asm volatile("s_waitcnt vmcnt(" #n ")" ::: "memory")
; #define GM_WAIT_L(n) asm volatile("s_waitcnt lgkmcnt(" #n ")" ::: "memory")
; #define GM_BAR __builtin_amdgcn_s_barrier()
; #define GM_SCHED __builtin_amdgcn_sched_barrier(0)
; #define GM_STA_H0(buf, p, o0) do { if constexpr (GATHER) GM_STAGE(buf, p, o0); else GM_STAGE(buf, p, voffA); } while (0)
; #define GM_STA_H1(buf, p, o1) do { if constexpr (GATHER) GM_STAGE(buf, p, o1); else GM_STAGE(buf, (p) + hstepB, voffA); } while (0)
; template <bool BF, bool GATHER = false, class Epi, class Hook>
; __device__ __forceinline__ void gemm_phase(LAS unsigned char* lds, const Gemm g, const Order& S, const Epi& E, Hook& HK) {
;     ...
;             GM_WAIT_V(8); GM_WAIT_L(0); GM_BAR; GM_MMA(1, 0, At, B0); GM_MMA(1, 1, At, B1); GM_BAR; GM_SCHED;
;             GM_LDB(B0, 1, 0); GM_LDB(B1, 1, 1); GM_SCHED; GM_LDA(At, 1, 0); GM_STA_H1(GM_SA(0, 1), a2, s1);
;             GM_WAIT_V(8); GM_WAIT_L(0); GM_BAR; GM_MMA(0, 0, At, B0); GM_MMA(0, 1, At, B1); GM_BAR; GM_SCHED;
;             GM_LDA(At, 1, 1); GM_STAGE(GM_SB(1, 0), b3, voffB); GM_STAGE(GM_SB(1, 1), b3 + hstepB, voffB); GM_STA_H0(GM_SA(1, 0), a3, s0);
;             GM_WAIT_V(8); GM_WAIT_L(0); GM_BAR; GM_MMA(1, 0, At, B0); GM_MMA(1, 1, At, B1); GM_BAR; GM_SCHED;
	s_waitcnt lgkmcnt(0)
	v_mfma_f32_16x16x32_f16 v[62:65], v[146:149], v[190:193], v[62:65]
	v_mfma_f32_16x16x32_f16 v[58:61], v[166:169], v[190:193], v[58:61]
	v_mfma_f32_16x16x32_f16 v[46:49], v[146:149], v[198:201], v[46:49]
	v_mfma_f32_16x16x32_f16 v[42:45], v[166:169], v[198:201], v[42:45]
	v_mfma_f32_16x16x32_f16 v[30:33], v[146:149], v[206:209], v[30:33]
	v_mfma_f32_16x16x32_f16 v[26:29], v[166:169], v[206:209], v[26:29]
	v_mfma_f32_16x16x32_f16 v[14:17], v[146:149], v[214:217], v[14:17]
	v_mfma_f32_16x16x32_f16 v[10:13], v[166:169], v[214:217], v[10:13]
	v_mfma_f32_16x16x32_f16 v[62:65], v[162:165], v[194:197], v[62:65]
	v_mfma_f32_16x16x32_f16 v[58:61], v[170:173], v[194:197], v[58:61]
	v_mfma_f32_16x16x32_f16 v[46:49], v[162:165], v[202:205], v[46:49]
	v_mfma_f32_16x16x32_f16 v[42:45], v[170:173], v[202:205], v[42:45]
	v_mfma_f32_16x16x32_f16 v[30:33], v[162:165], v[210:213], v[30:33]
	v_mfma_f32_16x16x32_f16 v[26:29], v[170:173], v[210:213], v[26:29]
	v_mfma_f32_16x16x32_f16 v[14:17], v[162:165], v[218:221], v[14:17]
	v_mfma_f32_16x16x32_f16 v[10:13], v[170:173], v[218:221], v[10:13]
	v_mfma_f32_16x16x32_f16 v[54:57], v[174:177], v[190:193], v[54:57]
	v_mfma_f32_16x16x32_f16 v[50:53], v[182:185], v[190:193], v[50:53]
	v_mfma_f32_16x16x32_f16 v[38:41], v[174:177], v[198:201], v[38:41]
	v_mfma_f32_16x16x32_f16 v[34:37], v[182:185], v[198:201], v[34:37]
	v_mfma_f32_16x16x32_f16 v[22:25], v[174:177], v[206:209], v[22:25]
	v_mfma_f32_16x16x32_f16 v[18:21], v[182:185], v[206:209], v[18:21]
	v_mfma_f32_16x16x32_f16 v[6:9], v[174:177], v[214:217], v[6:9]
	v_mfma_f32_16x16x32_f16 v[2:5], v[182:185], v[214:217], v[2:5]
	v_mfma_f32_16x16x32_f16 v[54:57], v[178:181], v[194:197], v[54:57]
	v_mfma_f32_16x16x32_f16 v[50:53], v[186:189], v[194:197], v[50:53]
	v_mfma_f32_16x16x32_f16 v[38:41], v[178:181], v[202:205], v[38:41]
	v_mfma_f32_16x16x32_f16 v[34:37], v[186:189], v[202:205], v[34:37]
	v_mfma_f32_16x16x32_f16 v[22:25], v[178:181], v[210:213], v[22:25]
	v_mfma_f32_16x16x32_f16 v[18:21], v[186:189], v[210:213], v[18:21]
	v_mfma_f32_16x16x32_f16 v[6:9], v[178:181], v[218:221], v[6:9]
	v_mfma_f32_16x16x32_f16 v[2:5], v[186:189], v[218:221], v[2:5]
	s_barrier
	s_add_u32 s30, s30, 0x40000
	s_addc_u32 s31, s31, 0
	s_mov_b32 m0, s37
	v_lshl_add_u64 v[228:229], s[30:31], 0, v[130:131]
	global_load_lds_dwordx4 v[228:229], off
	v_lshl_add_u64 v[228:229], s[30:31], 0, v[134:135]
	s_mov_b32 m0, s38
	s_nop 0
	global_load_lds_dwordx4 v[228:229], off
	s_mov_b32 s53, 0x1c000
	s_mov_b32 s52, 0x18000
	v_add_u32_e32 v244, s52, v153
	v_add_u32_e32 v245, s53, v153
	ds_read_b128 v[146:149], v244
	ds_read_b128 v[162:165], v244 offset:1024
	ds_read_b128 v[166:169], v244 offset:2048
	ds_read_b128 v[170:173], v244 offset:3072
	ds_read_b128 v[174:177], v245
	ds_read_b128 v[178:181], v245 offset:1024
	ds_read_b128 v[182:185], v245 offset:2048
	ds_read_b128 v[186:189], v245 offset:3072
	ds_read_b128 v[190:193], v160 offset:32768
	ds_read_b128 v[194:197], v160 offset:33792
	ds_read_b128 v[198:201], v160 offset:34816
	ds_read_b128 v[202:205], v160 offset:35840
	ds_read_b128 v[206:209], v160 offset:36864
	ds_read_b128 v[210:213], v160 offset:37888
	ds_read_b128 v[214:217], v160 offset:38912
	ds_read_b128 v[218:221], v160 offset:39936
	s_waitcnt vmcnt(8)
	s_waitcnt lgkmcnt(0)
	s_barrier
	s_waitcnt lgkmcnt(0)
	v_mfma_f32_16x16x32_f16 v[126:129], v[146:149], v[190:193], v[126:129]
	v_mfma_f32_16x16x32_f16 v[122:125], v[166:169], v[190:193], v[122:125]
	v_mfma_f32_16x16x32_f16 v[110:113], v[146:149], v[198:201], v[110:113]
	v_mfma_f32_16x16x32_f16 v[106:109], v[166:169], v[198:201], v[106:109]
	v_mfma_f32_16x16x32_f16 v[94:97], v[146:149], v[206:209], v[94:97]
	v_mfma_f32_16x16x32_f16 v[90:93], v[166:169], v[206:209], v[90:93]
	v_mfma_f32_16x16x32_f16 v[78:81], v[146:149], v[214:217], v[78:81]
	v_mfma_f32_16x16x32_f16 v[74:77], v[166:169], v[214:217], v[74:77]
	v_mfma_f32_16x16x32_f16 v[126:129], v[162:165], v[194:197], v[126:129]
	v_mfma_f32_16x16x32_f16 v[122:125], v[170:173], v[194:197], v[122:125]
	v_mfma_f32_16x16x32_f16 v[110:113], v[162:165], v[202:205], v[110:113]
	v_mfma_f32_16x16x32_f16 v[106:109], v[170:173], v[202:205], v[106:109]
	v_mfma_f32_16x16x32_f16 v[94:97], v[162:165], v[210:213], v[94:97]
	v_mfma_f32_16x16x32_f16 v[90:93], v[170:173], v[210:213], v[90:93]
	v_mfma_f32_16x16x32_f16 v[78:81], v[162:165], v[218:221], v[78:81]
	v_mfma_f32_16x16x32_f16 v[74:77], v[170:173], v[218:221], v[74:77]
	v_mfma_f32_16x16x32_f16 v[118:121], v[174:177], v[190:193], v[118:121]
	v_mfma_f32_16x16x32_f16 v[114:117], v[182:185], v[190:193], v[114:117]
	v_mfma_f32_16x16x32_f16 v[102:105], v[174:177], v[198:201], v[102:105]
	v_mfma_f32_16x16x32_f16 v[98:101], v[182:185], v[198:201], v[98:101]
	v_mfma_f32_16x16x32_f16 v[86:89], v[174:177], v[206:209], v[86:89]
	v_mfma_f32_16x16x32_f16 v[82:85], v[182:185], v[206:209], v[82:85]
	v_mfma_f32_16x16x32_f16 v[70:73], v[174:177], v[214:217], v[70:73]
	v_mfma_f32_16x16x32_f16 v[66:69], v[182:185], v[214:217], v[66:69]
	v_mfma_f32_16x16x32_f16 v[118:121], v[178:181], v[194:197], v[118:121]
	v_mfma_f32_16x16x32_f16 v[114:117], v[186:189], v[194:197], v[114:117]
	v_mfma_f32_16x16x32_f16 v[102:105], v[178:181], v[202:205], v[102:105]
	v_mfma_f32_16x16x32_f16 v[98:101], v[186:189], v[202:205], v[98:101]
	v_mfma_f32_16x16x32_f16 v[86:89], v[178:181], v[210:213], v[86:89]
	v_mfma_f32_16x16x32_f16 v[82:85], v[186:189], v[210:213], v[82:85]
	v_mfma_f32_16x16x32_f16 v[70:73], v[178:181], v[218:221], v[70:73]
	v_mfma_f32_16x16x32_f16 v[66:69], v[186:189], v[218:221], v[66:69]
	s_barrier
; #define GM_STAGE(bufoff, gbase, voff) do { _Pragma("unroll") for (int _i = 0; _i < 2; ++_i) \
;         __builtin_amdgcn_global_load_lds((const unsigned*)((const char*)(gbase) + (voff)[_i]), (LAS unsigned*)(lds + (bufoff) + ldsw + _i * 8192), 16, 0, 0); } while (0)
; #define GM_LDA(dst, b, h) do { _Pragma("unroll") for (int m = 0; m < 4; ++m) _Pragma("unroll") for (int k = 0; k < 2; ++k) dst[m][k] = *(const LAS s16x8*)(lds + GM_SA(b, h) + aoff + m * 2048 + k * 1024); } while (0)
; #define GM_MMA(ai, bj, At, Bt) do { __builtin_amdgcn_s_setprio(1); _Pragma("unroll") for (int m = 0; m < 4; ++m) _Pragma("unroll") for (int n = 0; n < 2; ++n) _Pragma("unroll") for (int k = 0; k < 2; ++k) \
;         acc[ai][bj][m][n] = mma16<BF>(Bt[n][k], At[m][k], acc[ai][bj][m][n]); __builtin_amdgcn_s_setprio(0); } while (0)
; #define GM_WAIT_V(n) asm volatile("s_waitcnt vmcnt(" #n ")" ::: "memory")
; #define GM_WAIT_L(n) asm volatile("s_waitcnt lgkmcnt(" #n ")" ::: "memory")
; #define GM_BAR __builtin_amdgcn_s_barrier()
; #define GM_SCHED __builtin_amdgcn_sched_barrier(0)
; #define GM_STA_H0(buf, p, o0) do { if constexpr (GATHER) GM_STAGE(buf, p, o0); else GM_STAGE(buf, p, voffA); } while (0)
; template <bool BF, bool GATHER = false, class Epi, class Hook>
; __device__ __forceinline__ void gemm_phase(LAS unsigned char* lds, const Gemm g, const Order& S, const Epi& E, Hook& HK) {
;     ...
;             GM_WAIT_V(8); GM_WAIT_L(0); GM_BAR; GM_MMA(0, 0, At, B0); GM_MMA(0, 1, At, B1); GM_BAR; GM_SCHED;
;             GM_LDA(At, 1, 1); GM_STAGE(GM_SB(1, 0), b3, voffB); GM_STAGE(GM_SB(1, 1), b3 + hstepB, voffB); GM_STA_H0(GM_SA(1, 0), a3, s0);
;             GM_WAIT_V(8); GM_WAIT_L(0); GM_BAR; GM_MMA(1, 0, At, B0); GM_MMA(1, 1, At, B1); GM_BAR; GM_SCHED;
;         }
	s_add_i32 s30, s52, s35
	v_lshl_add_u64 v[150:151], v[150:151], 0, s[14:15]
	s_mov_b32 m0, s30
	global_load_lds_dwordx4 v[150:151], off
	s_add_i32 m0, s30, 0x2000
	s_add_u32 s28, s28, 0x40080
	v_lshl_add_u64 v[150:151], v[222:223], 0, s[14:15]
	s_addc_u32 s29, s29, 0
	s_add_i32 s30, s53, s35
	global_load_lds_dwordx4 v[150:151], off
	v_lshl_add_u64 v[150:151], s[28:29], 0, v[132:133]
	s_mov_b32 m0, s30
	s_nop 0
	global_load_lds_dwordx4 v[150:151], off
	v_lshl_add_u64 v[150:151], s[28:29], 0, v[136:137]
	s_add_i32 m0, s30, 0x2000
	s_nop 0
	global_load_lds_dwordx4 v[150:151], off
	v_lshl_add_u64 v[150:151], v[224:225], 0, s[14:15]
	s_mov_b32 m0, s42
	s_nop 0
	global_load_lds_dwordx4 v[150:151], off
	v_lshl_add_u64 v[150:151], v[226:227], 0, s[14:15]
	s_mov_b32 m0, s43
	s_nop 0
	global_load_lds_dwordx4 v[150:151], off
	ds_read_b128 v[190:193], v160 offset:49152
	ds_read_b128 v[194:197], v160 offset:50176
	ds_read_b128 v[198:201], v160 offset:51200
	ds_read_b128 v[202:205], v160 offset:52224
	ds_read_b128 v[206:209], v160 offset:53248
	ds_read_b128 v[210:213], v160 offset:54272
	ds_read_b128 v[214:217], v160 offset:55296
	ds_read_b128 v[218:221], v160 offset:56320
	s_waitcnt vmcnt(8)
	s_waitcnt lgkmcnt(0)
	s_barrier
	s_waitcnt lgkmcnt(0)
	v_mfma_f32_16x16x32_f16 v[62:65], v[146:149], v[190:193], v[62:65]
	v_mfma_f32_16x16x32_f16 v[58:61], v[166:169], v[190:193], v[58:61]
	v_mfma_f32_16x16x32_f16 v[46:49], v[146:149], v[198:201], v[46:49]
	v_mfma_f32_16x16x32_f16 v[42:45], v[166:169], v[198:201], v[42:45]
	v_mfma_f32_16x16x32_f16 v[30:33], v[146:149], v[206:209], v[30:33]
	v_mfma_f32_16x16x32_f16 v[26:29], v[166:169], v[206:209], v[26:29]
	v_mfma_f32_16x16x32_f16 v[14:17], v[146:149], v[214:217], v[14:17]
	v_mfma_f32_16x16x32_f16 v[10:13], v[166:169], v[214:217], v[10:13]
	v_mfma_f32_16x16x32_f16 v[62:65], v[162:165], v[194:197], v[62:65]
	v_mfma_f32_16x16x32_f16 v[58:61], v[170:173], v[194:197], v[58:61]
	v_mfma_f32_16x16x32_f16 v[46:49], v[162:165], v[202:205], v[46:49]
	v_mfma_f32_16x16x32_f16 v[42:45], v[170:173], v[202:205], v[42:45]
	v_mfma_f32_16x16x32_f16 v[30:33], v[162:165], v[210:213], v[30:33]
	v_mfma_f32_16x16x32_f16 v[26:29], v[170:173], v[210:213], v[26:29]
	v_mfma_f32_16x16x32_f16 v[14:17], v[162:165], v[218:221], v[14:17]
	v_mfma_f32_16x16x32_f16 v[10:13], v[170:173], v[218:221], v[10:13]
	v_mfma_f32_16x16x32_f16 v[54:57], v[174:177], v[190:193], v[54:57]
	v_mfma_f32_16x16x32_f16 v[50:53], v[182:185], v[190:193], v[50:53]
	v_mfma_f32_16x16x32_f16 v[38:41], v[174:177], v[198:201], v[38:41]
	v_mfma_f32_16x16x32_f16 v[34:37], v[182:185], v[198:201], v[34:37]
	v_mfma_f32_16x16x32_f16 v[22:25], v[174:177], v[206:209], v[22:25]
	v_mfma_f32_16x16x32_f16 v[18:21], v[182:185], v[206:209], v[18:21]
	v_mfma_f32_16x16x32_f16 v[6:9], v[174:177], v[214:217], v[6:9]
	v_mfma_f32_16x16x32_f16 v[2:5], v[182:185], v[214:217], v[2:5]
	v_mfma_f32_16x16x32_f16 v[54:57], v[178:181], v[194:197], v[54:57]
	v_mfma_f32_16x16x32_f16 v[50:53], v[186:189], v[194:197], v[50:53]
	v_mfma_f32_16x16x32_f16 v[38:41], v[178:181], v[202:205], v[38:41]
	v_mfma_f32_16x16x32_f16 v[34:37], v[186:189], v[202:205], v[34:37]
	v_mfma_f32_16x16x32_f16 v[22:25], v[178:181], v[210:213], v[22:25]
	v_mfma_f32_16x16x32_f16 v[18:21], v[186:189], v[210:213], v[18:21]
	v_mfma_f32_16x16x32_f16 v[6:9], v[178:181], v[218:221], v[6:9]
	v_mfma_f32_16x16x32_f16 v[2:5], v[186:189], v[218:221], v[2:5]
	s_barrier
	s_add_i32 s51, s51, 2
	s_add_u32 s2, s2, 0x100
	s_addc_u32 s3, s3, 0
	s_add_u32 s49, s49, 0x100
	s_addc_u32 s50, s50, 0
	s_cmp_gt_u32 s51, 13
	s_cbranch_scc0 .LBB0_380
	s_and_b64 vcc, exec, s[16:17]
	s_cbranch_vccz .LBB0_383
	s_barrier

;     __device__ __forceinline__ CvItem decode(int it) const {
;         constexpr int I13 = (DM / 256) * (DE / 128), I2 = (DE / 256) * (DM / 128);
;         const int per_e = mode == 0 ? 2 * I13 + I2 : (mode == 1 ? 2 * I13 : I2);
;         const int e = it / per_e; int r = it % per_e; if (mode == 2) r += 2 * I13;
;         CvItem d;
;         if (r < I13) { d.W = w1 + (size_t)e * DM * DE; d.WT = W13 + (size_t)e * 2 * DE * DM; d.K = DM; d.N = DE; d.add = 0; d.r = r; }
;         else if (r < 2 * I13) { d.W = w3 + (size_t)e * DM * DE; d.WT = W13 + (size_t)e * 2 * DE * DM; d.K = DM; d.N = DE; d.add = 128; d.r = r - I13; }
;         else { d.W = w2 + (size_t)e * DE * DM; d.WT = W2T + (size_t)e * DM * DE; d.K = DE; d.N = DM; d.add = -1; d.r = r - 2 * I13; }
;         return d; }
;     static __device__ __forceinline__ void load(const CvItem& d, int tid, f32x4 (&v)[2][8]) {
;         const int lane = tid & 63, wave = tid >> 6, kg = lane >> 3, ng = lane & 7; const int nblk = d.N / 128, kb = d.r / nblk, nb = d.r % nblk;
; #pragma unroll
;         for (int t = 0; t < 2; ++t) { const int sb = 2 * wave + t, k0 = 256 * kb + 64 * (sb >> 2) + 8 * kg, n0 = 128 * nb + 32 * (sb & 3) + 4 * ng;
; #pragma unroll
;             for (int i = 0; i < 8; ++i) v[t][i] = *(const f32x4*)(d.W + (size_t)(k0 + i) * d.N + n0); } }
;     __device__ __forceinline__ void run_all(int tid) const {
;     ...
;         for (int it = it_lo; it < it_hi; it += 2) {
;             f32x4 va[2][8], vb[2][8];
;             const CvItem d0 = decode(it); load(d0, tid, va);
;             const bool two = it + 1 < it_hi; const CvItem d1 = decode(two ? it + 1 : it);
;             if (two) load(d1, tid, vb);
.LBB0_597:
	s_lshr_b32 s14, s3, 7
	v_cvt_f32_i32_e32 v2, s14
	s_sext_i32_i16 s12, s17
	v_cvt_f32_i32_e32 v68, s12
	s_ashr_i32 s12, s12, 30
	v_rcp_iflag_f32_e32 v69, v2
	s_or_b32 s15, s12, 1
	v_mul_f32_e32 v69, v68, v69
	v_trunc_f32_e32 v69, v69
	v_fma_f32 v68, -v69, v2, v68
	v_cvt_i32_f32_e32 v69, v69
	v_cmp_ge_f32_e64 s[12:13], |v68|, v2
	s_and_b64 s[12:13], s[12:13], exec
	s_cselect_b32 s12, s15, 0
	v_readfirstlane_b32 s13, v69
	s_add_i32 s12, s13, s12
	s_sext_i32_i16 s13, s12
	s_mul_i32 s12, s12, s14
	s_sub_i32 s12, s17, s12
	v_lshl_or_b32 v134, s13, 8, v213
	s_sext_i32_i16 s25, s12
	v_ashrrev_i32_e32 v135, 31, v134
	v_or_b32_e32 v74, 2, v134
	v_lshl_or_b32 v132, s25, 7, v214
	v_mul_lo_u32 v2, v135, s3
	v_mad_u64_u32 v[74:75], s[12:13], v74, s3, 0
	v_ashrrev_i32_e32 v133, 31, v132
	v_add_u32_e32 v75, v75, v2
	v_lshlrev_b64 v[70:71], 2, v[132:133]
	v_lshl_add_u64 v[74:75], v[74:75], 2, s[4:5]
	v_lshl_add_u64 v[76:77], v[74:75], 0, v[70:71]
	v_or_b32_e32 v74, 3, v134
	v_mad_u64_u32 v[74:75], s[12:13], v74, s3, 0
	v_add_u32_e32 v75, v75, v2
	v_lshl_add_u64 v[74:75], v[74:75], 2, s[4:5]
	v_lshl_add_u64 v[80:81], v[74:75], 0, v[70:71]
	v_or_b32_e32 v74, 4, v134
	v_mad_u64_u32 v[74:75], s[12:13], v74, s3, 0
	v_add_u32_e32 v75, v75, v2
	v_lshl_add_u64 v[74:75], v[74:75], 2, s[4:5]
	v_lshl_add_u64 v[84:85], v[74:75], 0, v[70:71]
	v_or_b32_e32 v74, 5, v134
	v_mad_u64_u32 v[74:75], s[12:13], v74, s3, 0
	v_add_u32_e32 v75, v75, v2
	v_lshl_add_u64 v[74:75], v[74:75], 2, s[4:5]
	v_lshl_add_u64 v[88:89], v[74:75], 0, v[70:71]
	v_or_b32_e32 v74, 6, v134
	v_mad_u64_u32 v[74:75], s[12:13], v74, s3, 0
	v_add_u32_e32 v75, v75, v2
	v_lshl_add_u64 v[74:75], v[74:75], 2, s[4:5]
	v_or_b32_e32 v72, 1, v134
	v_lshl_add_u64 v[92:93], v[74:75], 0, v[70:71]
	v_or_b32_e32 v74, 7, v134
	v_mad_u64_u32 v[68:69], s[12:13], v134, s3, 0
	v_mad_u64_u32 v[72:73], s[12:13], v72, s3, 0
	v_mad_u64_u32 v[74:75], s[12:13], v74, s3, 0
	v_add_u32_e32 v69, v69, v2
	v_add_u32_e32 v73, v73, v2
	v_add_u32_e32 v75, v75, v2
	v_lshl_add_u64 v[68:69], v[68:69], 2, s[4:5]
	v_lshl_add_u64 v[72:73], v[72:73], 2, s[4:5]
	v_lshl_add_u64 v[74:75], v[74:75], 2, s[4:5]
	v_lshl_add_u64 v[68:69], v[68:69], 0, v[70:71]
	v_lshl_add_u64 v[72:73], v[72:73], 0, v[70:71]
	v_lshl_add_u64 v[96:97], v[74:75], 0, v[70:71]
	global_load_dwordx4 v[100:103], v[68:69], off nt
	s_nop 0
	global_load_dwordx4 v[68:71], v[68:69], off offset:128 nt
	s_nop 0
	global_load_dwordx4 v[104:107], v[72:73], off nt
	s_nop 0
	global_load_dwordx4 v[72:75], v[72:73], off offset:128 nt
	s_nop 0
	global_load_dwordx4 v[108:111], v[76:77], off nt
	s_nop 0
	global_load_dwordx4 v[76:79], v[76:77], off offset:128 nt
	s_nop 0
	global_load_dwordx4 v[112:115], v[80:81], off nt
	s_nop 0
	global_load_dwordx4 v[80:83], v[80:81], off offset:128 nt
	s_nop 0
	global_load_dwordx4 v[116:119], v[84:85], off nt
	s_nop 0
	global_load_dwordx4 v[84:87], v[84:85], off offset:128 nt
	s_nop 0
	global_load_dwordx4 v[120:123], v[88:89], off nt
	s_nop 0
	global_load_dwordx4 v[88:91], v[88:89], off offset:128 nt
	s_nop 0
	global_load_dwordx4 v[124:127], v[92:93], off nt
	s_nop 0
	global_load_dwordx4 v[92:95], v[92:93], off offset:128 nt
	s_nop 0
	global_load_dwordx4 v[128:131], v[96:97], off nt
	s_nop 0
	global_load_dwordx4 v[96:99], v[96:97], off offset:128 nt
	s_add_i32 s3, s0, 1
	s_cmp_lt_i32 s3, s2
	s_cselect_b64 s[20:21], -1, 0
	s_and_b64 s[4:5], s[20:21], exec
	s_cselect_b32 s3, s3, s0
	s_mul_hi_i32 s4, s3, 0x3e0f83e1
	s_lshr_b32 s5, s4, 31
	s_ashr_i32 s29, s4, 6
	s_add_i32 s29, s29, s5
	s_mul_i32 s4, s29, 0x108
	s_sub_i32 s26, s3, s4
	s_cmpk_gt_i32 s26, 0x57
	s_mul_hi_i32 s27, s29, 0xb00000
	s_mul_i32 s28, s29, 0xb00000
	s_mov_b64 s[4:5], -1
	s_cbranch_scc0 .LBB0_602
	s_mov_b64 s[14:15], -1
	s_cmpk_gt_u32 s26, 0xaf
	s_cbranch_scc0 .LBB0_600
	v_readlane_b32 s36, v251, 28
	v_readlane_b32 s42, v251, 34
	v_readlane_b32 s43, v251, 35
	s_add_u32 s18, s42, s28
	s_addc_u32 s19, s43, s27
	s_mul_hi_i32 s3, s29, 0x580000
	s_mul_i32 s29, s29, 0x580000
	s_add_u32 s12, s78, s29
	v_readlane_b32 s4, v250, 16
	v_readlane_b32 s37, v251, 29
	v_readlane_b32 s38, v251, 30
	v_readlane_b32 s39, v251, 31
	v_readlane_b32 s40, v251, 32
	v_readlane_b32 s41, v251, 33
	v_readlane_b32 s44, v251, 36
	v_readlane_b32 s45, v251, 37
	v_readlane_b32 s46, v251, 38
	v_readlane_b32 s47, v251, 39
	v_readlane_b32 s48, v251, 40
	v_readlane_b32 s49, v251, 41
	v_readlane_b32 s50, v251, 42
	v_readlane_b32 s51, v251, 43
	s_addc_u32 s13, s4, s3
	s_add_i32 s3, s26, 0xffffff50
	s_mov_b64 s[4:5], 0

;     static __device__ __forceinline__ void load(const CvItem& d, int tid, f32x4 (&v)[2][8]) {
;         const int lane = tid & 63, wave = tid >> 6, kg = lane >> 3, ng = lane & 7; const int nblk = d.N / 128, kb = d.r / nblk, nb = d.r % nblk;
; #pragma unroll
;         for (int t = 0; t < 2; ++t) { const int sb = 2 * wave + t, k0 = 256 * kb + 64 * (sb >> 2) + 8 * kg, n0 = 128 * nb + 32 * (sb & 3) + 4 * ng;
; #pragma unroll
;             for (int i = 0; i < 8; ++i) v[t][i] = *(const f32x4*)(d.W + (size_t)(k0 + i) * d.N + n0); } }
;     __device__ __forceinline__ void run_all(int tid) const {
;     ...
;             const bool two = it + 1 < it_hi; const CvItem d1 = decode(two ? it + 1 : it);
;             if (two) load(d1, tid, vb);
.LBB0_604:
	v_cndmask_b32_e64 v2, 0, 1, s[20:21]
	s_andn2_b64 vcc, exec, s[20:21]
	s_sext_i32_i16 s20, s3
	v_cmp_ne_u32_e64 s[4:5], 1, v2
	v_cvt_f32_i32_e32 v2, s20
	s_cbranch_vccnz .LBB0_606
	s_lshr_b32 s21, s24, 7
	v_cvt_f32_i32_e32 v4, s21
	s_ashr_i32 s26, s20, 30
	s_or_b32 s28, s26, 1
	v_rcp_iflag_f32_e32 v5, v4
	s_nop 0
	v_mul_f32_e32 v5, v2, v5
	v_trunc_f32_e32 v5, v5
	v_fma_f32 v6, -v5, v4, v2
	v_cvt_i32_f32_e32 v5, v5
	v_cmp_ge_f32_e64 s[26:27], |v6|, v4
	s_and_b64 s[26:27], s[26:27], exec
	s_cselect_b32 s26, s28, 0
	v_add_u32_e32 v4, s26, v5
	v_bfe_i32 v5, v4, 0, 16
	v_mul_lo_u32 v4, v4, s21
	v_sub_u32_e32 v4, s3, v4
	v_lshl_or_b32 v14, v5, 8, v213
	v_ashrrev_i32_e32 v6, 31, v5
	v_bfe_i32 v4, v4, 0, 16
	v_or_b32_e32 v10, 2, v14
	v_lshl_or_b32 v4, v4, 7, v214
	v_mul_lo_u32 v15, v6, s24
	v_mad_u64_u32 v[10:11], s[26:27], v10, s24, 0
	v_ashrrev_i32_e32 v5, 31, v4
	v_add_u32_e32 v11, v11, v15
	v_lshlrev_b64 v[4:5], 2, v[4:5]
	v_lshl_add_u64 v[10:11], v[10:11], 2, s[18:19]
	v_lshl_add_u64 v[12:13], v[10:11], 0, v[4:5]
	v_or_b32_e32 v10, 3, v14
	v_mad_u64_u32 v[10:11], s[26:27], v10, s24, 0
	v_add_u32_e32 v11, v11, v15
	v_lshl_add_u64 v[10:11], v[10:11], 2, s[18:19]
	v_lshl_add_u64 v[20:21], v[10:11], 0, v[4:5]
	v_or_b32_e32 v10, 4, v14
	v_mad_u64_u32 v[10:11], s[26:27], v10, s24, 0
	v_add_u32_e32 v11, v11, v15
	v_lshl_add_u64 v[10:11], v[10:11], 2, s[18:19]
	v_lshl_add_u64 v[24:25], v[10:11], 0, v[4:5]
	v_or_b32_e32 v10, 5, v14
	v_mad_u64_u32 v[10:11], s[26:27], v10, s24, 0
	v_add_u32_e32 v11, v11, v15
	v_lshl_add_u64 v[10:11], v[10:11], 2, s[18:19]
	v_lshl_add_u64 v[28:29], v[10:11], 0, v[4:5]
	v_or_b32_e32 v10, 6, v14
	v_mad_u64_u32 v[10:11], s[26:27], v10, s24, 0
	v_add_u32_e32 v11, v11, v15
	v_lshl_add_u64 v[10:11], v[10:11], 2, s[18:19]
	v_or_b32_e32 v8, 1, v14
	v_lshl_add_u64 v[32:33], v[10:11], 0, v[4:5]
	v_or_b32_e32 v10, 7, v14
	v_mad_u64_u32 v[6:7], s[26:27], v14, s24, 0
	v_mad_u64_u32 v[8:9], s[26:27], v8, s24, 0
	v_mad_u64_u32 v[10:11], s[26:27], v10, s24, 0
	v_add_u32_e32 v7, v7, v15
	v_add_u32_e32 v9, v9, v15
	v_add_u32_e32 v11, v11, v15
	v_lshl_add_u64 v[6:7], v[6:7], 2, s[18:19]
	v_lshl_add_u64 v[8:9], v[8:9], 2, s[18:19]
	v_lshl_add_u64 v[10:11], v[10:11], 2, s[18:19]
	v_lshl_add_u64 v[6:7], v[6:7], 0, v[4:5]
	v_lshl_add_u64 v[8:9], v[8:9], 0, v[4:5]
	v_lshl_add_u64 v[40:41], v[10:11], 0, v[4:5]
	global_load_dwordx4 v[16:19], v[6:7], off nt
	s_nop 0
	global_load_dwordx4 v[4:7], v[6:7], off offset:128 nt
	s_nop 0
	global_load_dwordx4 v[36:39], v[8:9], off nt
	s_nop 0
	global_load_dwordx4 v[8:11], v[8:9], off offset:128 nt
	s_nop 0
	global_load_dwordx4 v[44:47], v[12:13], off nt
	s_nop 0
	global_load_dwordx4 v[12:15], v[12:13], off offset:128 nt
	s_nop 0
	global_load_dwordx4 v[56:59], v[20:21], off nt
	s_nop 0
	global_load_dwordx4 v[20:23], v[20:21], off offset:128 nt
	s_nop 0
	global_load_dwordx4 v[48:51], v[24:25], off nt
	s_nop 0
	global_load_dwordx4 v[24:27], v[24:25], off offset:128 nt
	s_nop 0
	global_load_dwordx4 v[52:55], v[28:29], off nt
	s_nop 0
	global_load_dwordx4 v[28:31], v[28:29], off offset:128 nt
	s_nop 0
	global_load_dwordx4 v[60:63], v[32:33], off nt
	s_nop 0
	global_load_dwordx4 v[32:35], v[32:33], off offset:128 nt
	s_nop 0
	global_load_dwordx4 v[64:67], v[40:41], off nt
	s_nop 0
	global_load_dwordx4 v[40:43], v[40:41], off offset:128 nt

; #define GM_STAGE(bufoff, gbase, voff) do { _Pragma("unroll") for (int _i = 0; _i < 2; ++_i) \
;         __builtin_amdgcn_global_load_lds((const unsigned*)((const char*)(gbase) + (voff)[_i]), (LAS unsigned*)(lds + (bufoff) + ldsw + _i * 8192), 16, 0, 0); } while (0)
; #define GM_LDA(dst, b, h) do { _Pragma("unroll") for (int m = 0; m < 4; ++m) _Pragma("unroll") for (int k = 0; k < 2; ++k) dst[m][k] = *(const LAS s16x8*)(lds + GM_SA(b, h) + aoff + m * 2048 + k * 1024); } while (0)
; #define GM_LDB(dst, b, h) do { _Pragma("unroll") for (int n = 0; n < 2; ++n) _Pragma("unroll") for (int k = 0; k < 2; ++k) dst[n][k] = *(const LAS s16x8*)(lds + GM_SB(b, h) + boff + n * 2048 + k * 1024); } while (0)
; #define GM_MMA(ai, bj, At, Bt) do { __builtin_amdgcn_s_setprio(1); _Pragma("unroll") for (int m = 0; m < 4; ++m) _Pragma("unroll") for (int n = 0; n < 2; ++n) _Pragma("unroll") for (int k = 0; k < 2; ++k) \
;         acc[ai][bj][m][n] = mma16<BF>(Bt[n][k], At[m][k], acc[ai][bj][m][n]); __builtin_amdgcn_s_setprio(0); } while (0)
; #define GM_WAIT_V(n) asm volatile("s_waitcnt vmcnt(" #n ")" ::: "memory")
; #define GM_WAIT_L(n) asm volatile("s_waitcnt lgkmcnt(" #n ")" ::: "memory")
; #define GM_BAR __builtin_amdgcn_s_barrier()
; template <bool BF, bool GATHER = false, class Epi, class Hook>
; __device__ __forceinline__ void gemm_phase(LAS unsigned char* lds, const Gemm g, const Order& S, const Epi& E, Hook& HK) {
;     ...
;             const char* a1 = cA + (size_t)(t + 1) * kstep;
;             const char* a2 = last ? nA : cA + (size_t)(t + 2) * kstep; const char* b2 = last ? nB : cB + (size_t)(t + 2) * kstep;
;             const char* a3 = a2 + kstep; const char* b3 = b2 + kstep;
;             unsigned s0[2], s1[2];
;             if constexpr (GATHER) { s0[0] = last ? nA0[0] : gA0[0]; s0[1] = last ? nA0[1] : gA0[1]; s1[0] = last ? nA1[0] : gA1[0]; s1[1] = last ? nA1[1] : gA1[1]; }
;             GM_LDB(B0, 0, 0); GM_LDB(B1, 0, 1); GM_SCHED; GM_LDA(At, 0, 0); GM_STA_H1(GM_SA(1, 1), a1, gA1);
;             GM_WAIT_V(8); GM_WAIT_L(0); GM_BAR; GM_MMA(0, 0, At, B0); GM_MMA(0, 1, At, B1); GM_BAR; GM_SCHED;
;             GM_LDA(At, 0, 1); GM_STAGE(GM_SB(0, 0), b2, voffB); GM_STAGE(GM_SB(0, 1), b2 + hstepB, voffB); GM_STA_H0(GM_SA(0, 0), a2, s0);
;             GM_WAIT_V(8); GM_WAIT_L(0); GM_BAR; GM_MMA(1, 0, At, B0); GM_MMA(1, 1, At, B1); GM_BAR; GM_SCHED;
.LBB0_715:
	s_add_u32 s22, s20, 0xfffc0080
	s_addc_u32 s23, s21, -1
	s_cmp_eq_u32 s47, 12
	s_cselect_b32 s25, s13, s23
	s_cselect_b32 s24, s43, s22
	s_cselect_b32 s23, s15, s46
	s_cselect_b32 s22, s44, s45
	v_lshl_add_u64 v[216:217], s[20:21], 0, v[154:155]
	s_add_i32 m0, s30, 0xc000
	global_load_lds_dwordx4 v[216:217], off
	v_lshl_add_u64 v[216:217], s[20:21], 0, v[156:157]
	s_add_i32 m0, s30, 0xe000
	s_nop 0
	global_load_lds_dwordx4 v[216:217], off
	ds_read_b128 v[130:133], v168
	ds_read_b128 v[134:137], v168 offset:1024
	ds_read_b128 v[138:141], v168 offset:2048
	ds_read_b128 v[142:145], v168 offset:3072
	ds_read_b128 v[162:165], v169
	ds_read_b128 v[172:175], v169 offset:1024
	ds_read_b128 v[176:179], v169 offset:2048
	ds_read_b128 v[180:183], v169 offset:3072
	ds_read_b128 v[184:187], v170
	ds_read_b128 v[188:191], v170 offset:1024
	ds_read_b128 v[192:195], v170 offset:2048
	ds_read_b128 v[196:199], v170 offset:3072
	ds_read_b128 v[200:203], v170 offset:4096
	ds_read_b128 v[204:207], v170 offset:5120
	ds_read_b128 v[208:211], v170 offset:6144
	ds_read_b128 v[212:215], v170 offset:7168
	s_waitcnt vmcnt(8)
	s_waitcnt lgkmcnt(0)
	s_barrier
	s_waitcnt lgkmcnt(0)
	v_mfma_f32_16x16x32_f16 v[126:129], v[130:133], v[184:187], v[126:129]
	v_mfma_f32_16x16x32_f16 v[122:125], v[138:141], v[184:187], v[122:125]
	v_mfma_f32_16x16x32_f16 v[110:113], v[130:133], v[192:195], v[110:113]
	v_mfma_f32_16x16x32_f16 v[106:109], v[138:141], v[192:195], v[106:109]
	v_mfma_f32_16x16x32_f16 v[94:97], v[130:133], v[200:203], v[94:97]
	v_mfma_f32_16x16x32_f16 v[90:93], v[138:141], v[200:203], v[90:93]
	v_mfma_f32_16x16x32_f16 v[78:81], v[130:133], v[208:211], v[78:81]
	v_mfma_f32_16x16x32_f16 v[74:77], v[138:141], v[208:211], v[74:77]
	v_mfma_f32_16x16x32_f16 v[126:129], v[134:137], v[188:191], v[126:129]
	v_mfma_f32_16x16x32_f16 v[122:125], v[142:145], v[188:191], v[122:125]
	v_mfma_f32_16x16x32_f16 v[110:113], v[134:137], v[196:199], v[110:113]
	v_mfma_f32_16x16x32_f16 v[106:109], v[142:145], v[196:199], v[106:109]
	v_mfma_f32_16x16x32_f16 v[94:97], v[134:137], v[204:207], v[94:97]
	v_mfma_f32_16x16x32_f16 v[90:93], v[142:145], v[204:207], v[90:93]
	v_mfma_f32_16x16x32_f16 v[78:81], v[134:137], v[212:215], v[78:81]
	v_mfma_f32_16x16x32_f16 v[74:77], v[142:145], v[212:215], v[74:77]
	v_mfma_f32_16x16x32_f16 v[118:121], v[162:165], v[184:187], v[118:121]
	v_mfma_f32_16x16x32_f16 v[114:117], v[176:179], v[184:187], v[114:117]
	v_mfma_f32_16x16x32_f16 v[102:105], v[162:165], v[192:195], v[102:105]
	v_mfma_f32_16x16x32_f16 v[98:101], v[176:179], v[192:195], v[98:101]
	v_mfma_f32_16x16x32_f16 v[86:89], v[162:165], v[200:203], v[86:89]
	v_mfma_f32_16x16x32_f16 v[82:85], v[176:179], v[200:203], v[82:85]
	v_mfma_f32_16x16x32_f16 v[70:73], v[162:165], v[208:211], v[70:73]
	v_mfma_f32_16x16x32_f16 v[66:69], v[176:179], v[208:211], v[66:69]
	v_mfma_f32_16x16x32_f16 v[118:121], v[172:175], v[188:191], v[118:121]
	v_mfma_f32_16x16x32_f16 v[114:117], v[180:183], v[188:191], v[114:117]
	v_mfma_f32_16x16x32_f16 v[102:105], v[172:175], v[196:199], v[102:105]
	v_mfma_f32_16x16x32_f16 v[98:101], v[180:183], v[196:199], v[98:101]
	v_mfma_f32_16x16x32_f16 v[86:89], v[172:175], v[204:207], v[86:89]
	v_mfma_f32_16x16x32_f16 v[82:85], v[180:183], v[204:207], v[82:85]
	v_mfma_f32_16x16x32_f16 v[70:73], v[172:175], v[212:215], v[70:73]
	v_mfma_f32_16x16x32_f16 v[66:69], v[180:183], v[212:215], v[66:69]
	s_barrier
	s_add_i32 s48, s41, s29
	v_lshl_add_u64 v[216:217], s[22:23], 0, v[148:149]
	s_mov_b32 m0, s48
	global_load_lds_dwordx4 v[216:217], off
	s_add_i32 m0, s48, 0x2000
	s_add_u32 s48, s22, 0x40000
	v_lshl_add_u64 v[218:219], s[22:23], 0, v[152:153]
	s_addc_u32 s49, s23, 0
	s_add_i32 s50, s42, s29
	global_load_lds_dwordx4 v[218:219], off
	v_lshl_add_u64 v[220:221], s[48:49], 0, v[148:149]
	s_mov_b32 m0, s50
	v_lshl_add_u64 v[222:223], s[24:25], 0, v[150:151]
	global_load_lds_dwordx4 v[220:221], off
	v_lshl_add_u64 v[220:221], s[48:49], 0, v[152:153]
	s_add_i32 m0, s50, 0x2000
	s_nop 0
	global_load_lds_dwordx4 v[220:221], off
	v_lshl_add_u64 v[220:221], s[24:25], 0, v[146:147]
	s_mov_b32 m0, s30
	s_nop 0
	global_load_lds_dwordx4 v[220:221], off
	s_mov_b32 m0, s31
	s_nop 0
	global_load_lds_dwordx4 v[222:223], off
	ds_read_b128 v[184:187], v170 offset:16384
	ds_read_b128 v[188:191], v170 offset:17408
	ds_read_b128 v[192:195], v170 offset:18432
	ds_read_b128 v[196:199], v170 offset:19456
	ds_read_b128 v[200:203], v170 offset:20480
	ds_read_b128 v[204:207], v170 offset:21504
	ds_read_b128 v[208:211], v170 offset:22528
	ds_read_b128 v[212:215], v170 offset:23552
	s_waitcnt vmcnt(8)
	s_waitcnt lgkmcnt(0)
	s_barrier
; #define GM_STAGE(bufoff, gbase, voff) do { _Pragma("unroll") for (int _i = 0; _i < 2; ++_i) \
;         __builtin_amdgcn_global_load_lds((const unsigned*)((const char*)(gbase) + (voff)[_i]), (LAS unsigned*)(lds + (bufoff) + ldsw + _i * 8192), 16, 0, 0); } while (0)
; #define GM_LDA(dst, b, h) do { _Pragma("unroll") for (int m = 0; m < 4; ++m) _Pragma("unroll") for (int k = 0; k < 2; ++k) dst[m][k] = *(const LAS s16x8*)(lds + GM_SA(b, h) + aoff + m * 2048 + k * 1024); } while (0)
; #define GM_LDB(dst, b, h) do { _Pragma("unroll") for (int n = 0; n < 2; ++n) _Pragma("unroll") for (int k = 0; k < 2; ++k) dst[n][k] = *(const LAS s16x8*)(lds + GM_SB(b, h) + boff + n * 2048 + k * 1024); } while (0)
; #define GM_MMA(ai, bj, At, Bt) do { __builtin_amdgcn_s_setprio(1); _Pragma("unroll") for (int m = 0; m < 4; ++m) _Pragma("unroll") for (int n = 0; n < 2; ++n) _Pragma("unroll") for (int k = 0; k < 2; ++k) \
;         acc[ai][bj][m][n] = mma16<BF>(Bt[n][k], At[m][k], acc[ai][bj][m][n]); __builtin_amdgcn_s_setprio(0); } while (0)
; #define GM_WAIT_V(n) asm volatile("s_waitcnt vmcnt(" #n ")" ::: "memory")
; #define GM_WAIT_L(n) asm volatile("s_waitcnt lgkmcnt(" #n ")" ::: "memory")
; #define GM_BAR __builtin_amdgcn_s_barrier()
; #define GM_SCHED __builtin_amdgcn_sched_barrier(0)
; #define GM_STA_H0(buf, p, o0) do { if constexpr (GATHER) GM_STAGE(buf, p, o0); else GM_STAGE(buf, p, voffA); } while (0)
; #define GM_STA_H1(buf, p, o1) do { if constexpr (GATHER) GM_STAGE(buf, p, o1); else GM_STAGE(buf, (p) + hstepB, voffA); } while (0)
; template <bool BF, bool GATHER = false, class Epi, class Hook>
; __device__ __forceinline__ void gemm_phase(LAS unsigned char* lds, const Gemm g, const Order& S, const Epi& E, Hook& HK) {
;     ...
;             GM_WAIT_V(8); GM_WAIT_L(0); GM_BAR; GM_MMA(1, 0, At, B0); GM_MMA(1, 1, At, B1); GM_BAR; GM_SCHED;
;             GM_LDB(B0, 1, 0); GM_LDB(B1, 1, 1); GM_SCHED; GM_LDA(At, 1, 0); GM_STA_H1(GM_SA(0, 1), a2, s1);
;             GM_WAIT_V(8); GM_WAIT_L(0); GM_BAR; GM_MMA(0, 0, At, B0); GM_MMA(0, 1, At, B1); GM_BAR; GM_SCHED;
;             GM_LDA(At, 1, 1); GM_STAGE(GM_SB(1, 0), b3, voffB); GM_STAGE(GM_SB(1, 1), b3 + hstepB, voffB); GM_STA_H0(GM_SA(1, 0), a3, s0);
;             GM_WAIT_V(8); GM_WAIT_L(0); GM_BAR; GM_MMA(1, 0, At, B0); GM_MMA(1, 1, At, B1); GM_BAR; GM_SCHED;
	s_waitcnt lgkmcnt(0)
	v_mfma_f32_16x16x32_f16 v[62:65], v[130:133], v[184:187], v[62:65]
	v_mfma_f32_16x16x32_f16 v[58:61], v[138:141], v[184:187], v[58:61]
	v_mfma_f32_16x16x32_f16 v[46:49], v[130:133], v[192:195], v[46:49]
	v_mfma_f32_16x16x32_f16 v[42:45], v[138:141], v[192:195], v[42:45]
	v_mfma_f32_16x16x32_f16 v[30:33], v[130:133], v[200:203], v[30:33]
	v_mfma_f32_16x16x32_f16 v[26:29], v[138:141], v[200:203], v[26:29]
	v_mfma_f32_16x16x32_f16 v[14:17], v[130:133], v[208:211], v[14:17]
	v_mfma_f32_16x16x32_f16 v[10:13], v[138:141], v[208:211], v[10:13]
	v_mfma_f32_16x16x32_f16 v[62:65], v[134:137], v[188:191], v[62:65]
	v_mfma_f32_16x16x32_f16 v[58:61], v[142:145], v[188:191], v[58:61]
	v_mfma_f32_16x16x32_f16 v[46:49], v[134:137], v[196:199], v[46:49]
	v_mfma_f32_16x16x32_f16 v[42:45], v[142:145], v[196:199], v[42:45]
	v_mfma_f32_16x16x32_f16 v[30:33], v[134:137], v[204:207], v[30:33]
	v_mfma_f32_16x16x32_f16 v[26:29], v[142:145], v[204:207], v[26:29]
	v_mfma_f32_16x16x32_f16 v[14:17], v[134:137], v[212:215], v[14:17]
	v_mfma_f32_16x16x32_f16 v[10:13], v[142:145], v[212:215], v[10:13]
	v_mfma_f32_16x16x32_f16 v[54:57], v[162:165], v[184:187], v[54:57]
	v_mfma_f32_16x16x32_f16 v[50:53], v[176:179], v[184:187], v[50:53]
	v_mfma_f32_16x16x32_f16 v[38:41], v[162:165], v[192:195], v[38:41]
	v_mfma_f32_16x16x32_f16 v[34:37], v[176:179], v[192:195], v[34:37]
	v_mfma_f32_16x16x32_f16 v[22:25], v[162:165], v[200:203], v[22:25]
	v_mfma_f32_16x16x32_f16 v[18:21], v[176:179], v[200:203], v[18:21]
	v_mfma_f32_16x16x32_f16 v[6:9], v[162:165], v[208:211], v[6:9]
	v_mfma_f32_16x16x32_f16 v[2:5], v[176:179], v[208:211], v[2:5]
	v_mfma_f32_16x16x32_f16 v[54:57], v[172:175], v[188:191], v[54:57]
	v_mfma_f32_16x16x32_f16 v[50:53], v[180:183], v[188:191], v[50:53]
	v_mfma_f32_16x16x32_f16 v[38:41], v[172:175], v[196:199], v[38:41]
	v_mfma_f32_16x16x32_f16 v[34:37], v[180:183], v[196:199], v[34:37]
	v_mfma_f32_16x16x32_f16 v[22:25], v[172:175], v[204:207], v[22:25]
	v_mfma_f32_16x16x32_f16 v[18:21], v[180:183], v[204:207], v[18:21]
	v_mfma_f32_16x16x32_f16 v[6:9], v[172:175], v[212:215], v[6:9]
	v_mfma_f32_16x16x32_f16 v[2:5], v[180:183], v[212:215], v[2:5]
	s_barrier
	s_add_u32 s24, s24, 0x40000
	s_addc_u32 s25, s25, 0
	s_mov_b32 m0, s33
	v_lshl_add_u64 v[224:225], s[24:25], 0, v[146:147]
	global_load_lds_dwordx4 v[224:225], off
	v_lshl_add_u64 v[224:225], s[24:25], 0, v[150:151]
	s_mov_b32 m0, s34
	s_nop 0
	global_load_lds_dwordx4 v[224:225], off
	s_mov_b32 s49, 0x1c000
	s_mov_b32 s48, 0x18000
	v_add_u32_e32 v244, s48, v166
	v_add_u32_e32 v245, s49, v166
	ds_read_b128 v[130:133], v244
	ds_read_b128 v[134:137], v244 offset:1024
	ds_read_b128 v[138:141], v244 offset:2048
	ds_read_b128 v[142:145], v244 offset:3072
	ds_read_b128 v[162:165], v245
	ds_read_b128 v[172:175], v245 offset:1024
	ds_read_b128 v[176:179], v245 offset:2048
	ds_read_b128 v[180:183], v245 offset:3072
	ds_read_b128 v[184:187], v170 offset:32768
	ds_read_b128 v[188:191], v170 offset:33792
	ds_read_b128 v[192:195], v170 offset:34816
	ds_read_b128 v[196:199], v170 offset:35840
	ds_read_b128 v[200:203], v170 offset:36864
	ds_read_b128 v[204:207], v170 offset:37888
	ds_read_b128 v[208:211], v170 offset:38912
	ds_read_b128 v[212:215], v170 offset:39936
	s_waitcnt vmcnt(8)
	s_waitcnt lgkmcnt(0)
	s_barrier
	s_waitcnt lgkmcnt(0)
	v_mfma_f32_16x16x32_f16 v[126:129], v[130:133], v[184:187], v[126:129]
	v_mfma_f32_16x16x32_f16 v[122:125], v[138:141], v[184:187], v[122:125]
	v_mfma_f32_16x16x32_f16 v[110:113], v[130:133], v[192:195], v[110:113]
	v_mfma_f32_16x16x32_f16 v[106:109], v[138:141], v[192:195], v[106:109]
	v_mfma_f32_16x16x32_f16 v[94:97], v[130:133], v[200:203], v[94:97]
	v_mfma_f32_16x16x32_f16 v[90:93], v[138:141], v[200:203], v[90:93]
	v_mfma_f32_16x16x32_f16 v[78:81], v[130:133], v[208:211], v[78:81]
	v_mfma_f32_16x16x32_f16 v[74:77], v[138:141], v[208:211], v[74:77]
	v_mfma_f32_16x16x32_f16 v[126:129], v[134:137], v[188:191], v[126:129]
	v_mfma_f32_16x16x32_f16 v[122:125], v[142:145], v[188:191], v[122:125]
	v_mfma_f32_16x16x32_f16 v[110:113], v[134:137], v[196:199], v[110:113]
	v_mfma_f32_16x16x32_f16 v[106:109], v[142:145], v[196:199], v[106:109]
	v_mfma_f32_16x16x32_f16 v[94:97], v[134:137], v[204:207], v[94:97]
	v_mfma_f32_16x16x32_f16 v[90:93], v[142:145], v[204:207], v[90:93]
	v_mfma_f32_16x16x32_f16 v[78:81], v[134:137], v[212:215], v[78:81]
	v_mfma_f32_16x16x32_f16 v[74:77], v[142:145], v[212:215], v[74:77]
	v_mfma_f32_16x16x32_f16 v[118:121], v[162:165], v[184:187], v[118:121]
	v_mfma_f32_16x16x32_f16 v[114:117], v[176:179], v[184:187], v[114:117]
	v_mfma_f32_16x16x32_f16 v[102:105], v[162:165], v[192:195], v[102:105]
	v_mfma_f32_16x16x32_f16 v[98:101], v[176:179], v[192:195], v[98:101]
	v_mfma_f32_16x16x32_f16 v[86:89], v[162:165], v[200:203], v[86:89]
	v_mfma_f32_16x16x32_f16 v[82:85], v[176:179], v[200:203], v[82:85]
	v_mfma_f32_16x16x32_f16 v[70:73], v[162:165], v[208:211], v[70:73]
	v_mfma_f32_16x16x32_f16 v[66:69], v[176:179], v[208:211], v[66:69]
	v_mfma_f32_16x16x32_f16 v[118:121], v[172:175], v[188:191], v[118:121]
	v_mfma_f32_16x16x32_f16 v[114:117], v[180:183], v[188:191], v[114:117]
	v_mfma_f32_16x16x32_f16 v[102:105], v[172:175], v[196:199], v[102:105]
	v_mfma_f32_16x16x32_f16 v[98:101], v[180:183], v[196:199], v[98:101]
	v_mfma_f32_16x16x32_f16 v[86:89], v[172:175], v[204:207], v[86:89]
	v_mfma_f32_16x16x32_f16 v[82:85], v[180:183], v[204:207], v[82:85]
	v_mfma_f32_16x16x32_f16 v[70:73], v[172:175], v[212:215], v[70:73]
	v_mfma_f32_16x16x32_f16 v[66:69], v[180:183], v[212:215], v[66:69]
	s_barrier
; #define GM_STAGE(bufoff, gbase, voff) do { _Pragma("unroll") for (int _i = 0; _i < 2; ++_i) \
;         __builtin_amdgcn_global_load_lds((const unsigned*)((const char*)(gbase) + (voff)[_i]), (LAS unsigned*)(lds + (bufoff) + ldsw + _i * 8192), 16, 0, 0); } while (0)
; #define GM_LDA(dst, b, h) do { _Pragma("unroll") for (int m = 0; m < 4; ++m) _Pragma("unroll") for (int k = 0; k < 2; ++k) dst[m][k] = *(const LAS s16x8*)(lds + GM_SA(b, h) + aoff + m * 2048 + k * 1024); } while (0)
; #define GM_MMA(ai, bj, At, Bt) do { __builtin_amdgcn_s_setprio(1); _Pragma("unroll") for (int m = 0; m < 4; ++m) _Pragma("unroll") for (int n = 0; n < 2; ++n) _Pragma("unroll") for (int k = 0; k < 2; ++k) \
;         acc[ai][bj][m][n] = mma16<BF>(Bt[n][k], At[m][k], acc[ai][bj][m][n]); __builtin_amdgcn_s_setprio(0); } while (0)
; #define GM_WAIT_V(n) asm volatile("s_waitcnt vmcnt(" #n ")" ::: "memory")
; #define GM_WAIT_L(n) asm volatile("s_waitcnt lgkmcnt(" #n ")" ::: "memory")
; #define GM_BAR __builtin_amdgcn_s_barrier()
; #define GM_SCHED __builtin_amdgcn_sched_barrier(0)
; #define GM_STA_H0(buf, p, o0) do { if constexpr (GATHER) GM_STAGE(buf, p, o0); else GM_STAGE(buf, p, voffA); } while (0)
; template <bool BF, bool GATHER = false, class Epi, class Hook>
; __device__ __forceinline__ void gemm_phase(LAS unsigned char* lds, const Gemm g, const Order& S, const Epi& E, Hook& HK) {
;     ...
;             GM_WAIT_V(8); GM_WAIT_L(0); GM_BAR; GM_MMA(0, 0, At, B0); GM_MMA(0, 1, At, B1); GM_BAR; GM_SCHED;
;             GM_LDA(At, 1, 1); GM_STAGE(GM_SB(1, 0), b3, voffB); GM_STAGE(GM_SB(1, 1), b3 + hstepB, voffB); GM_STA_H0(GM_SA(1, 0), a3, s0);
;             GM_WAIT_V(8); GM_WAIT_L(0); GM_BAR; GM_MMA(1, 0, At, B0); GM_MMA(1, 1, At, B1); GM_BAR; GM_SCHED;
;         }
	s_add_i32 s24, s48, s29
	v_lshl_add_u64 v[216:217], v[216:217], 0, s[8:9]
	s_mov_b32 m0, s24
	global_load_lds_dwordx4 v[216:217], off
	s_add_i32 m0, s24, 0x2000
	s_add_u32 s22, s22, 0x40080
	v_lshl_add_u64 v[216:217], v[218:219], 0, s[8:9]
	s_addc_u32 s23, s23, 0
	s_add_i32 s24, s49, s29
	global_load_lds_dwordx4 v[216:217], off
	v_lshl_add_u64 v[216:217], s[22:23], 0, v[148:149]
	s_mov_b32 m0, s24
	s_nop 0
	global_load_lds_dwordx4 v[216:217], off
	v_lshl_add_u64 v[216:217], s[22:23], 0, v[152:153]
	s_add_i32 m0, s24, 0x2000
	s_nop 0
	global_load_lds_dwordx4 v[216:217], off
	v_lshl_add_u64 v[216:217], v[220:221], 0, s[8:9]
	s_mov_b32 m0, s38
	s_nop 0
	global_load_lds_dwordx4 v[216:217], off
	v_lshl_add_u64 v[216:217], v[222:223], 0, s[8:9]
	s_mov_b32 m0, s39
	s_nop 0
	global_load_lds_dwordx4 v[216:217], off
	ds_read_b128 v[184:187], v170 offset:49152
	ds_read_b128 v[188:191], v170 offset:50176
	ds_read_b128 v[192:195], v170 offset:51200
	ds_read_b128 v[196:199], v170 offset:52224
	ds_read_b128 v[200:203], v170 offset:53248
	ds_read_b128 v[204:207], v170 offset:54272
	ds_read_b128 v[208:211], v170 offset:55296
	ds_read_b128 v[212:215], v170 offset:56320
	s_waitcnt vmcnt(8)
	s_waitcnt lgkmcnt(0)
	s_barrier
	s_waitcnt lgkmcnt(0)
	v_mfma_f32_16x16x32_f16 v[62:65], v[130:133], v[184:187], v[62:65]
	v_mfma_f32_16x16x32_f16 v[58:61], v[138:141], v[184:187], v[58:61]
	v_mfma_f32_16x16x32_f16 v[46:49], v[130:133], v[192:195], v[46:49]
	v_mfma_f32_16x16x32_f16 v[42:45], v[138:141], v[192:195], v[42:45]
	v_mfma_f32_16x16x32_f16 v[30:33], v[130:133], v[200:203], v[30:33]
	v_mfma_f32_16x16x32_f16 v[26:29], v[138:141], v[200:203], v[26:29]
	v_mfma_f32_16x16x32_f16 v[14:17], v[130:133], v[208:211], v[14:17]
	v_mfma_f32_16x16x32_f16 v[10:13], v[138:141], v[208:211], v[10:13]
	v_mfma_f32_16x16x32_f16 v[62:65], v[134:137], v[188:191], v[62:65]
	v_mfma_f32_16x16x32_f16 v[58:61], v[142:145], v[188:191], v[58:61]
	v_mfma_f32_16x16x32_f16 v[46:49], v[134:137], v[196:199], v[46:49]
	v_mfma_f32_16x16x32_f16 v[42:45], v[142:145], v[196:199], v[42:45]
	v_mfma_f32_16x16x32_f16 v[30:33], v[134:137], v[204:207], v[30:33]
	v_mfma_f32_16x16x32_f16 v[26:29], v[142:145], v[204:207], v[26:29]
	v_mfma_f32_16x16x32_f16 v[14:17], v[134:137], v[212:215], v[14:17]
	v_mfma_f32_16x16x32_f16 v[10:13], v[142:145], v[212:215], v[10:13]
	v_mfma_f32_16x16x32_f16 v[54:57], v[162:165], v[184:187], v[54:57]
	v_mfma_f32_16x16x32_f16 v[50:53], v[176:179], v[184:187], v[50:53]
	v_mfma_f32_16x16x32_f16 v[38:41], v[162:165], v[192:195], v[38:41]
	v_mfma_f32_16x16x32_f16 v[34:37], v[176:179], v[192:195], v[34:37]
	v_mfma_f32_16x16x32_f16 v[22:25], v[162:165], v[200:203], v[22:25]
	v_mfma_f32_16x16x32_f16 v[18:21], v[176:179], v[200:203], v[18:21]
	v_mfma_f32_16x16x32_f16 v[6:9], v[162:165], v[208:211], v[6:9]
	v_mfma_f32_16x16x32_f16 v[2:5], v[176:179], v[208:211], v[2:5]
	v_mfma_f32_16x16x32_f16 v[54:57], v[172:175], v[188:191], v[54:57]
	v_mfma_f32_16x16x32_f16 v[50:53], v[180:183], v[188:191], v[50:53]
	v_mfma_f32_16x16x32_f16 v[38:41], v[172:175], v[196:199], v[38:41]
	v_mfma_f32_16x16x32_f16 v[34:37], v[180:183], v[196:199], v[34:37]
	v_mfma_f32_16x16x32_f16 v[22:25], v[172:175], v[204:207], v[22:25]
	v_mfma_f32_16x16x32_f16 v[18:21], v[180:183], v[204:207], v[18:21]
	v_mfma_f32_16x16x32_f16 v[6:9], v[172:175], v[212:215], v[6:9]
	v_mfma_f32_16x16x32_f16 v[2:5], v[180:183], v[212:215], v[2:5]
	s_barrier
	s_add_i32 s47, s47, 2
	s_add_u32 s20, s20, 0x100
	s_addc_u32 s21, s21, 0
	s_add_u32 s45, s45, 0x100
	s_addc_u32 s46, s46, 0
	s_cmp_gt_u32 s47, 13
	s_cbranch_scc0 .LBB0_715
	s_and_b64 vcc, exec, s[10:11]
	s_cbranch_vccz .LBB0_718
	s_barrier

; #define GM_STAGE(bufoff, gbase, voff) do { _Pragma("unroll") for (int _i = 0; _i < 2; ++_i) \
;         __builtin_amdgcn_global_load_lds((const unsigned*)((const char*)(gbase) + (voff)[_i]), (LAS unsigned*)(lds + (bufoff) + ldsw + _i * 8192), 16, 0, 0); } while (0)
; #define GM_LDA(dst, b, h) do { _Pragma("unroll") for (int m = 0; m < 4; ++m) _Pragma("unroll") for (int k = 0; k < 2; ++k) dst[m][k] = *(const LAS s16x8*)(lds + GM_SA(b, h) + aoff + m * 2048 + k * 1024); } while (0)
; #define GM_LDB(dst, b, h) do { _Pragma("unroll") for (int n = 0; n < 2; ++n) _Pragma("unroll") for (int k = 0; k < 2; ++k) dst[n][k] = *(const LAS s16x8*)(lds + GM_SB(b, h) + boff + n * 2048 + k * 1024); } while (0)
; #define GM_MMA(ai, bj, At, Bt) do { __builtin_amdgcn_s_setprio(1); _Pragma("unroll") for (int m = 0; m < 4; ++m) _Pragma("unroll") for (int n = 0; n < 2; ++n) _Pragma("unroll") for (int k = 0; k < 2; ++k) \
;         acc[ai][bj][m][n] = mma16<BF>(Bt[n][k], At[m][k], acc[ai][bj][m][n]); __builtin_amdgcn_s_setprio(0); } while (0)
; #define GM_WAIT_V(n) asm volatile("s_waitcnt vmcnt(" #n ")" ::: "memory")
; #define GM_WAIT_L(n) asm volatile("s_waitcnt lgkmcnt(" #n ")" ::: "memory")
; #define GM_BAR __builtin_amdgcn_s_barrier()
; template <bool BF, bool GATHER = false, class Epi, class Hook>
; __device__ __forceinline__ void gemm_phase(LAS unsigned char* lds, const Gemm g, const Order& S, const Epi& E, Hook& HK) {
;     ...
;             const char* a1 = cA + (size_t)(t + 1) * kstep;
;             const char* a2 = last ? nA : cA + (size_t)(t + 2) * kstep; const char* b2 = last ? nB : cB + (size_t)(t + 2) * kstep;
;             const char* a3 = a2 + kstep; const char* b3 = b2 + kstep;
;             unsigned s0[2], s1[2];
;             if constexpr (GATHER) { s0[0] = last ? nA0[0] : gA0[0]; s0[1] = last ? nA0[1] : gA0[1]; s1[0] = last ? nA1[0] : gA1[0]; s1[1] = last ? nA1[1] : gA1[1]; }
;             GM_LDB(B0, 0, 0); GM_LDB(B1, 0, 1); GM_SCHED; GM_LDA(At, 0, 0); GM_STA_H1(GM_SA(1, 1), a1, gA1);
;             GM_WAIT_V(8); GM_WAIT_L(0); GM_BAR; GM_MMA(0, 0, At, B0); GM_MMA(0, 1, At, B1); GM_BAR; GM_SCHED;
;             GM_LDA(At, 0, 1); GM_STAGE(GM_SB(0, 0), b2, voffB); GM_STAGE(GM_SB(0, 1), b2 + hstepB, voffB); GM_STA_H0(GM_SA(0, 0), a2, s0);
;             GM_WAIT_V(8); GM_WAIT_L(0); GM_BAR; GM_MMA(1, 0, At, B0); GM_MMA(1, 1, At, B1); GM_BAR; GM_SCHED;
.LBB0_1011:
	s_add_u32 s22, s90, s2
	s_addc_u32 s23, s91, s3
	s_add_u32 s24, s22, 0x11e00100
	s_addc_u32 s25, s23, 0
	s_add_u32 s44, s21, s2
	s_addc_u32 s45, s42, s3
	s_cmpk_eq_i32 s2, 0x700
	s_cselect_b64 vcc, -1, 0
	s_and_b64 s[22:23], vcc, exec
	v_cndmask_b32_e32 v134, v142, v159, vcc
	s_cselect_b32 s25, s69, s25
	s_cselect_b32 s24, s68, s24
	v_cndmask_b32_e32 v228, v146, v162, vcc
	v_cndmask_b32_e32 v141, v158, v160, vcc
	v_cndmask_b32_e32 v145, v157, v161, vcc
	s_cselect_b32 s23, s1, s45
	s_cselect_b32 s22, s0, s44
	v_lshl_add_u64 v[230:231], v[150:151], 0, s[2:3]
	s_add_i32 m0, s28, 0xc000
	global_load_lds_dwordx4 v[230:231], off
	v_lshl_add_u64 v[230:231], v[148:149], 0, s[2:3]
	s_add_i32 m0, s28, 0xe000
	s_nop 0
	global_load_lds_dwordx4 v[230:231], off
	v_add_u32_e32 v244, s35, v156
	ds_read_b128 v[164:167], v244
	ds_read_b128 v[168:171], v244 offset:1024
	ds_read_b128 v[172:175], v244 offset:2048
	ds_read_b128 v[176:179], v244 offset:3072
	v_add_u32_e32 v244, s36, v156
	ds_read_b128 v[180:183], v244
	ds_read_b128 v[184:187], v244 offset:1024
	ds_read_b128 v[188:191], v244 offset:2048
	ds_read_b128 v[192:195], v244 offset:3072
	ds_read_b128 v[196:199], v147
	ds_read_b128 v[200:203], v147 offset:1024
	ds_read_b128 v[204:207], v147 offset:2048
	ds_read_b128 v[208:211], v147 offset:3072
	ds_read_b128 v[212:215], v147 offset:4096
	ds_read_b128 v[216:219], v147 offset:5120
	ds_read_b128 v[220:223], v147 offset:6144
	ds_read_b128 v[224:227], v147 offset:7168
	s_waitcnt vmcnt(8)
	s_waitcnt lgkmcnt(0)
	s_barrier
	s_waitcnt lgkmcnt(0)
	v_mfma_f32_16x16x32_bf16 v[98:101], v[164:167], v[196:199], v[98:101]
	v_mfma_f32_16x16x32_bf16 v[94:97], v[172:175], v[196:199], v[94:97]
	v_mfma_f32_16x16x32_bf16 v[90:93], v[164:167], v[204:207], v[90:93]
	v_mfma_f32_16x16x32_bf16 v[86:89], v[172:175], v[204:207], v[86:89]
	v_mfma_f32_16x16x32_bf16 v[82:85], v[164:167], v[212:215], v[82:85]
	v_mfma_f32_16x16x32_bf16 v[78:81], v[172:175], v[212:215], v[78:81]
	v_mfma_f32_16x16x32_bf16 v[74:77], v[164:167], v[220:223], v[74:77]
	v_mfma_f32_16x16x32_bf16 v[70:73], v[172:175], v[220:223], v[70:73]
	v_mfma_f32_16x16x32_bf16 v[98:101], v[168:171], v[200:203], v[98:101]
	v_mfma_f32_16x16x32_bf16 v[94:97], v[176:179], v[200:203], v[94:97]
	v_mfma_f32_16x16x32_bf16 v[90:93], v[168:171], v[208:211], v[90:93]
	v_mfma_f32_16x16x32_bf16 v[86:89], v[176:179], v[208:211], v[86:89]
	v_mfma_f32_16x16x32_bf16 v[82:85], v[168:171], v[216:219], v[82:85]
	v_mfma_f32_16x16x32_bf16 v[78:81], v[176:179], v[216:219], v[78:81]
	v_mfma_f32_16x16x32_bf16 v[74:77], v[168:171], v[224:227], v[74:77]
	v_mfma_f32_16x16x32_bf16 v[70:73], v[176:179], v[224:227], v[70:73]
	v_mfma_f32_16x16x32_bf16 v[66:69], v[180:183], v[196:199], v[66:69]
	v_mfma_f32_16x16x32_bf16 v[62:65], v[188:191], v[196:199], v[62:65]
	v_mfma_f32_16x16x32_bf16 v[58:61], v[180:183], v[204:207], v[58:61]
	v_mfma_f32_16x16x32_bf16 v[54:57], v[188:191], v[204:207], v[54:57]
	v_mfma_f32_16x16x32_bf16 v[50:53], v[180:183], v[212:215], v[50:53]
	v_mfma_f32_16x16x32_bf16 v[46:49], v[188:191], v[212:215], v[46:49]
	v_mfma_f32_16x16x32_bf16 v[42:45], v[180:183], v[220:223], v[42:45]
	v_mfma_f32_16x16x32_bf16 v[38:41], v[188:191], v[220:223], v[38:41]
	v_mfma_f32_16x16x32_bf16 v[66:69], v[184:187], v[200:203], v[66:69]
	v_mfma_f32_16x16x32_bf16 v[62:65], v[192:195], v[200:203], v[62:65]
	v_mfma_f32_16x16x32_bf16 v[58:61], v[184:187], v[208:211], v[58:61]
	v_mfma_f32_16x16x32_bf16 v[54:57], v[192:195], v[208:211], v[54:57]
	v_mfma_f32_16x16x32_bf16 v[50:53], v[184:187], v[216:219], v[50:53]
	v_mfma_f32_16x16x32_bf16 v[46:49], v[192:195], v[216:219], v[46:49]
	v_mfma_f32_16x16x32_bf16 v[42:45], v[184:187], v[224:227], v[42:45]
	v_mfma_f32_16x16x32_bf16 v[38:41], v[192:195], v[224:227], v[38:41]
	s_barrier
	s_add_i32 s44, s35, s11
	v_lshl_add_u64 v[230:231], s[22:23], 0, v[130:131]
	s_mov_b32 m0, s44
	global_load_lds_dwordx4 v[230:231], off
	s_add_i32 m0, s44, 0x2000
	s_add_u32 s44, s22, 0x40000
	v_lshl_add_u64 v[232:233], s[22:23], 0, v[132:133]
	s_addc_u32 s45, s23, 0
	s_add_i32 s46, s36, s11
	global_load_lds_dwordx4 v[232:233], off
	v_lshl_add_u64 v[234:235], s[44:45], 0, v[130:131]
	s_mov_b32 m0, s46
	v_mov_b32_e32 v229, v135
	global_load_lds_dwordx4 v[234:235], off
	v_lshl_add_u64 v[234:235], s[44:45], 0, v[132:133]
	s_add_i32 m0, s46, 0x2000
	s_nop 0
	global_load_lds_dwordx4 v[234:235], off
	s_mov_b32 m0, s28
	v_lshl_add_u64 v[234:235], s[24:25], 0, v[134:135]
	global_load_lds_dwordx4 v134, s[24:25]
	s_mov_b32 m0, s29
	s_nop 0
	global_load_lds_dwordx4 v228, s[24:25]
	v_lshl_add_u64 v[228:229], s[24:25], 0, v[228:229]
	ds_read_b128 v[196:199], v147 offset:16384
	ds_read_b128 v[200:203], v147 offset:17408
	ds_read_b128 v[204:207], v147 offset:18432
	ds_read_b128 v[208:211], v147 offset:19456
	ds_read_b128 v[212:215], v147 offset:20480
	ds_read_b128 v[216:219], v147 offset:21504
	ds_read_b128 v[220:223], v147 offset:22528
	ds_read_b128 v[224:227], v147 offset:23552
	s_waitcnt vmcnt(8)
	s_waitcnt lgkmcnt(0)
	s_barrier
; #define GM_STAGE(bufoff, gbase, voff) do { _Pragma("unroll") for (int _i = 0; _i < 2; ++_i) \
;         __builtin_amdgcn_global_load_lds((const unsigned*)((const char*)(gbase) + (voff)[_i]), (LAS unsigned*)(lds + (bufoff) + ldsw + _i * 8192), 16, 0, 0); } while (0)
; #define GM_LDA(dst, b, h) do { _Pragma("unroll") for (int m = 0; m < 4; ++m) _Pragma("unroll") for (int k = 0; k < 2; ++k) dst[m][k] = *(const LAS s16x8*)(lds + GM_SA(b, h) + aoff + m * 2048 + k * 1024); } while (0)
; #define GM_LDB(dst, b, h) do { _Pragma("unroll") for (int n = 0; n < 2; ++n) _Pragma("unroll") for (int k = 0; k < 2; ++k) dst[n][k] = *(const LAS s16x8*)(lds + GM_SB(b, h) + boff + n * 2048 + k * 1024); } while (0)
; #define GM_MMA(ai, bj, At, Bt) do { __builtin_amdgcn_s_setprio(1); _Pragma("unroll") for (int m = 0; m < 4; ++m) _Pragma("unroll") for (int n = 0; n < 2; ++n) _Pragma("unroll") for (int k = 0; k < 2; ++k) \
;         acc[ai][bj][m][n] = mma16<BF>(Bt[n][k], At[m][k], acc[ai][bj][m][n]); __builtin_amdgcn_s_setprio(0); } while (0)
; #define GM_WAIT_V(n) asm volatile("s_waitcnt vmcnt(" #n ")" ::: "memory")
; #define GM_WAIT_L(n) asm volatile("s_waitcnt lgkmcnt(" #n ")" ::: "memory")
; #define GM_BAR __builtin_amdgcn_s_barrier()
; #define GM_SCHED __builtin_amdgcn_sched_barrier(0)
; #define GM_STA_H0(buf, p, o0) do { if constexpr (GATHER) GM_STAGE(buf, p, o0); else GM_STAGE(buf, p, voffA); } while (0)
; #define GM_STA_H1(buf, p, o1) do { if constexpr (GATHER) GM_STAGE(buf, p, o1); else GM_STAGE(buf, (p) + hstepB, voffA); } while (0)
; template <bool BF, bool GATHER = false, class Epi, class Hook>
; __device__ __forceinline__ void gemm_phase(LAS unsigned char* lds, const Gemm g, const Order& S, const Epi& E, Hook& HK) {
;     ...
;             GM_WAIT_V(8); GM_WAIT_L(0); GM_BAR; GM_MMA(1, 0, At, B0); GM_MMA(1, 1, At, B1); GM_BAR; GM_SCHED;
;             GM_LDB(B0, 1, 0); GM_LDB(B1, 1, 1); GM_SCHED; GM_LDA(At, 1, 0); GM_STA_H1(GM_SA(0, 1), a2, s1);
;             GM_WAIT_V(8); GM_WAIT_L(0); GM_BAR; GM_MMA(0, 0, At, B0); GM_MMA(0, 1, At, B1); GM_BAR; GM_SCHED;
;             GM_LDA(At, 1, 1); GM_STAGE(GM_SB(1, 0), b3, voffB); GM_STAGE(GM_SB(1, 1), b3 + hstepB, voffB); GM_STA_H0(GM_SA(1, 0), a3, s0);
;             GM_WAIT_V(8); GM_WAIT_L(0); GM_BAR; GM_MMA(1, 0, At, B0); GM_MMA(1, 1, At, B1); GM_BAR; GM_SCHED;
	s_waitcnt lgkmcnt(0)
	v_mfma_f32_16x16x32_bf16 v[34:37], v[164:167], v[196:199], v[34:37]
	v_mfma_f32_16x16x32_bf16 v[30:33], v[172:175], v[196:199], v[30:33]
	v_mfma_f32_16x16x32_bf16 v[26:29], v[164:167], v[204:207], v[26:29]
	v_mfma_f32_16x16x32_bf16 v[22:25], v[172:175], v[204:207], v[22:25]
	v_mfma_f32_16x16x32_bf16 v[18:21], v[164:167], v[212:215], v[18:21]
	v_mfma_f32_16x16x32_bf16 v[14:17], v[172:175], v[212:215], v[14:17]
	v_mfma_f32_16x16x32_bf16 v[10:13], v[164:167], v[220:223], v[10:13]
	v_mfma_f32_16x16x32_bf16 v[6:9], v[172:175], v[220:223], v[6:9]
	v_mfma_f32_16x16x32_bf16 v[34:37], v[168:171], v[200:203], v[34:37]
	v_mfma_f32_16x16x32_bf16 v[30:33], v[176:179], v[200:203], v[30:33]
	v_mfma_f32_16x16x32_bf16 v[26:29], v[168:171], v[208:211], v[26:29]
	v_mfma_f32_16x16x32_bf16 v[22:25], v[176:179], v[208:211], v[22:25]
	v_mfma_f32_16x16x32_bf16 v[18:21], v[168:171], v[216:219], v[18:21]
	v_mfma_f32_16x16x32_bf16 v[14:17], v[176:179], v[216:219], v[14:17]
	v_mfma_f32_16x16x32_bf16 v[10:13], v[168:171], v[224:227], v[10:13]
	v_mfma_f32_16x16x32_bf16 v[6:9], v[176:179], v[224:227], v[6:9]
	v_mfma_f32_16x16x32_bf16 v[2:5], v[180:183], v[196:199], v[2:5]
	v_mfma_f32_16x16x32_bf16 v[102:105], v[188:191], v[196:199], v[102:105]
	v_mfma_f32_16x16x32_bf16 v[106:109], v[180:183], v[204:207], v[106:109]
	v_mfma_f32_16x16x32_bf16 v[110:113], v[188:191], v[204:207], v[110:113]
	v_mfma_f32_16x16x32_bf16 v[114:117], v[180:183], v[212:215], v[114:117]
	v_mfma_f32_16x16x32_bf16 v[118:121], v[188:191], v[212:215], v[118:121]
	v_mfma_f32_16x16x32_bf16 v[122:125], v[180:183], v[220:223], v[122:125]
	v_mfma_f32_16x16x32_bf16 v[126:129], v[188:191], v[220:223], v[126:129]
	v_mfma_f32_16x16x32_bf16 v[2:5], v[184:187], v[200:203], v[2:5]
	v_mfma_f32_16x16x32_bf16 v[102:105], v[192:195], v[200:203], v[102:105]
	v_mfma_f32_16x16x32_bf16 v[106:109], v[184:187], v[208:211], v[106:109]
	v_mfma_f32_16x16x32_bf16 v[110:113], v[192:195], v[208:211], v[110:113]
	v_mfma_f32_16x16x32_bf16 v[114:117], v[184:187], v[216:219], v[114:117]
	v_mfma_f32_16x16x32_bf16 v[118:121], v[192:195], v[216:219], v[118:121]
	v_mfma_f32_16x16x32_bf16 v[122:125], v[184:187], v[224:227], v[122:125]
	v_mfma_f32_16x16x32_bf16 v[126:129], v[192:195], v[224:227], v[126:129]
	s_barrier
	s_mov_b32 m0, s30
	global_load_lds_dwordx4 v141, s[24:25]
	s_mov_b32 m0, s31
	s_nop 0
	global_load_lds_dwordx4 v145, s[24:25]
	s_mov_b32 s45, 0x1c000
	s_mov_b32 s44, 0x18000
	v_add_u32_e32 v245, s44, v156
	ds_read_b128 v[164:167], v245
	ds_read_b128 v[168:171], v245 offset:1024
	ds_read_b128 v[172:175], v245 offset:2048
	ds_read_b128 v[176:179], v245 offset:3072
	v_add_u32_e32 v245, s45, v156
	ds_read_b128 v[180:183], v245
	ds_read_b128 v[184:187], v245 offset:1024
	ds_read_b128 v[188:191], v245 offset:2048
	ds_read_b128 v[192:195], v245 offset:3072
	ds_read_b128 v[196:199], v147 offset:32768
	ds_read_b128 v[200:203], v147 offset:33792
	ds_read_b128 v[204:207], v147 offset:34816
	ds_read_b128 v[208:211], v147 offset:35840
	ds_read_b128 v[212:215], v147 offset:36864
	ds_read_b128 v[216:219], v147 offset:37888
	ds_read_b128 v[220:223], v147 offset:38912
	ds_read_b128 v[224:227], v147 offset:39936
	s_waitcnt vmcnt(8)
	s_waitcnt lgkmcnt(0)
	s_barrier
	s_waitcnt lgkmcnt(0)
	v_mfma_f32_16x16x32_bf16 v[98:101], v[164:167], v[196:199], v[98:101]
	v_mfma_f32_16x16x32_bf16 v[94:97], v[172:175], v[196:199], v[94:97]
	v_mfma_f32_16x16x32_bf16 v[90:93], v[164:167], v[204:207], v[90:93]
	v_mfma_f32_16x16x32_bf16 v[86:89], v[172:175], v[204:207], v[86:89]
	v_mfma_f32_16x16x32_bf16 v[82:85], v[164:167], v[212:215], v[82:85]
	v_mfma_f32_16x16x32_bf16 v[78:81], v[172:175], v[212:215], v[78:81]
	v_mfma_f32_16x16x32_bf16 v[74:77], v[164:167], v[220:223], v[74:77]
	v_mfma_f32_16x16x32_bf16 v[70:73], v[172:175], v[220:223], v[70:73]
	v_mfma_f32_16x16x32_bf16 v[98:101], v[168:171], v[200:203], v[98:101]
	v_mfma_f32_16x16x32_bf16 v[94:97], v[176:179], v[200:203], v[94:97]
	v_mfma_f32_16x16x32_bf16 v[90:93], v[168:171], v[208:211], v[90:93]
	v_mfma_f32_16x16x32_bf16 v[86:89], v[176:179], v[208:211], v[86:89]
	v_mfma_f32_16x16x32_bf16 v[82:85], v[168:171], v[216:219], v[82:85]
	v_mfma_f32_16x16x32_bf16 v[78:81], v[176:179], v[216:219], v[78:81]
	v_mfma_f32_16x16x32_bf16 v[74:77], v[168:171], v[224:227], v[74:77]
	v_mfma_f32_16x16x32_bf16 v[70:73], v[176:179], v[224:227], v[70:73]
	v_mfma_f32_16x16x32_bf16 v[66:69], v[180:183], v[196:199], v[66:69]
	v_mfma_f32_16x16x32_bf16 v[62:65], v[188:191], v[196:199], v[62:65]
	v_mfma_f32_16x16x32_bf16 v[58:61], v[180:183], v[204:207], v[58:61]
	v_mfma_f32_16x16x32_bf16 v[54:57], v[188:191], v[204:207], v[54:57]
	v_mfma_f32_16x16x32_bf16 v[50:53], v[180:183], v[212:215], v[50:53]
	v_mfma_f32_16x16x32_bf16 v[46:49], v[188:191], v[212:215], v[46:49]
	v_mfma_f32_16x16x32_bf16 v[42:45], v[180:183], v[220:223], v[42:45]
	v_mfma_f32_16x16x32_bf16 v[38:41], v[188:191], v[220:223], v[38:41]
	v_mfma_f32_16x16x32_bf16 v[66:69], v[184:187], v[200:203], v[66:69]
	v_mfma_f32_16x16x32_bf16 v[62:65], v[192:195], v[200:203], v[62:65]
	v_mfma_f32_16x16x32_bf16 v[58:61], v[184:187], v[208:211], v[58:61]
	v_mfma_f32_16x16x32_bf16 v[54:57], v[192:195], v[208:211], v[54:57]
	v_mfma_f32_16x16x32_bf16 v[50:53], v[184:187], v[216:219], v[50:53]
	v_mfma_f32_16x16x32_bf16 v[46:49], v[192:195], v[216:219], v[46:49]
	v_mfma_f32_16x16x32_bf16 v[42:45], v[184:187], v[224:227], v[42:45]
	v_mfma_f32_16x16x32_bf16 v[38:41], v[192:195], v[224:227], v[38:41]
	s_barrier
; #define GM_STAGE(bufoff, gbase, voff) do { _Pragma("unroll") for (int _i = 0; _i < 2; ++_i) \
;         __builtin_amdgcn_global_load_lds((const unsigned*)((const char*)(gbase) + (voff)[_i]), (LAS unsigned*)(lds + (bufoff) + ldsw + _i * 8192), 16, 0, 0); } while (0)
; #define GM_LDA(dst, b, h) do { _Pragma("unroll") for (int m = 0; m < 4; ++m) _Pragma("unroll") for (int k = 0; k < 2; ++k) dst[m][k] = *(const LAS s16x8*)(lds + GM_SA(b, h) + aoff + m * 2048 + k * 1024); } while (0)
; #define GM_MMA(ai, bj, At, Bt) do { __builtin_amdgcn_s_setprio(1); _Pragma("unroll") for (int m = 0; m < 4; ++m) _Pragma("unroll") for (int n = 0; n < 2; ++n) _Pragma("unroll") for (int k = 0; k < 2; ++k) \
;         acc[ai][bj][m][n] = mma16<BF>(Bt[n][k], At[m][k], acc[ai][bj][m][n]); __builtin_amdgcn_s_setprio(0); } while (0)
; #define GM_WAIT_V(n) asm volatile("s_waitcnt vmcnt(" #n ")" ::: "memory")
; #define GM_WAIT_L(n) asm volatile("s_waitcnt lgkmcnt(" #n ")" ::: "memory")
; #define GM_BAR __builtin_amdgcn_s_barrier()
; #define GM_SCHED __builtin_amdgcn_sched_barrier(0)
; #define GM_STA_H0(buf, p, o0) do { if constexpr (GATHER) GM_STAGE(buf, p, o0); else GM_STAGE(buf, p, voffA); } while (0)
; template <bool BF, bool GATHER = false, class Epi, class Hook>
; __device__ __forceinline__ void gemm_phase(LAS unsigned char* lds, const Gemm g, const Order& S, const Epi& E, Hook& HK) {
;     ...
;             GM_WAIT_V(8); GM_WAIT_L(0); GM_BAR; GM_MMA(0, 0, At, B0); GM_MMA(0, 1, At, B1); GM_BAR; GM_SCHED;
;             GM_LDA(At, 1, 1); GM_STAGE(GM_SB(1, 0), b3, voffB); GM_STAGE(GM_SB(1, 1), b3 + hstepB, voffB); GM_STA_H0(GM_SA(1, 0), a3, s0);
;             GM_WAIT_V(8); GM_WAIT_L(0); GM_BAR; GM_MMA(1, 0, At, B0); GM_MMA(1, 1, At, B1); GM_BAR; GM_SCHED;
;         }
	s_add_i32 s24, s44, s11
	v_lshl_add_u64 v[230:231], v[230:231], 0, s[14:15]
	s_mov_b32 m0, s24
	global_load_lds_dwordx4 v[230:231], off
	s_add_i32 m0, s24, 0x2000
	s_add_u32 s22, s22, 0x40080
	v_lshl_add_u64 v[230:231], v[232:233], 0, s[14:15]
	s_addc_u32 s23, s23, 0
	s_add_i32 s24, s45, s11
	global_load_lds_dwordx4 v[230:231], off
	v_lshl_add_u64 v[230:231], s[22:23], 0, v[130:131]
	s_mov_b32 m0, s24
	v_lshl_add_u64 v[228:229], v[228:229], 0, s[14:15]
	global_load_lds_dwordx4 v[230:231], off
	v_lshl_add_u64 v[230:231], s[22:23], 0, v[132:133]
	s_add_i32 m0, s24, 0x2000
	s_nop 0
	global_load_lds_dwordx4 v[230:231], off
	v_lshl_add_u64 v[230:231], v[234:235], 0, s[14:15]
	s_mov_b32 m0, s33
	s_nop 0
	global_load_lds_dwordx4 v[230:231], off
	s_mov_b32 m0, s34
	s_nop 0
	global_load_lds_dwordx4 v[228:229], off
	ds_read_b128 v[196:199], v147 offset:49152
	ds_read_b128 v[200:203], v147 offset:50176
	ds_read_b128 v[204:207], v147 offset:51200
	ds_read_b128 v[208:211], v147 offset:52224
	ds_read_b128 v[212:215], v147 offset:53248
	ds_read_b128 v[216:219], v147 offset:54272
	ds_read_b128 v[220:223], v147 offset:55296
	ds_read_b128 v[224:227], v147 offset:56320
	s_waitcnt vmcnt(8)
	s_waitcnt lgkmcnt(0)
	s_barrier
	s_waitcnt lgkmcnt(0)
	v_mfma_f32_16x16x32_bf16 v[34:37], v[164:167], v[196:199], v[34:37]
	v_mfma_f32_16x16x32_bf16 v[30:33], v[172:175], v[196:199], v[30:33]
	v_mfma_f32_16x16x32_bf16 v[26:29], v[164:167], v[204:207], v[26:29]
	v_mfma_f32_16x16x32_bf16 v[22:25], v[172:175], v[204:207], v[22:25]
	v_mfma_f32_16x16x32_bf16 v[18:21], v[164:167], v[212:215], v[18:21]
	v_mfma_f32_16x16x32_bf16 v[14:17], v[172:175], v[212:215], v[14:17]
	v_mfma_f32_16x16x32_bf16 v[10:13], v[164:167], v[220:223], v[10:13]
	v_mfma_f32_16x16x32_bf16 v[6:9], v[172:175], v[220:223], v[6:9]
	v_mfma_f32_16x16x32_bf16 v[34:37], v[168:171], v[200:203], v[34:37]
	v_mfma_f32_16x16x32_bf16 v[30:33], v[176:179], v[200:203], v[30:33]
	v_mfma_f32_16x16x32_bf16 v[26:29], v[168:171], v[208:211], v[26:29]
	v_mfma_f32_16x16x32_bf16 v[22:25], v[176:179], v[208:211], v[22:25]
	v_mfma_f32_16x16x32_bf16 v[18:21], v[168:171], v[216:219], v[18:21]
	v_mfma_f32_16x16x32_bf16 v[14:17], v[176:179], v[216:219], v[14:17]
	v_mfma_f32_16x16x32_bf16 v[10:13], v[168:171], v[224:227], v[10:13]
	v_mfma_f32_16x16x32_bf16 v[6:9], v[176:179], v[224:227], v[6:9]
	v_mfma_f32_16x16x32_bf16 v[2:5], v[180:183], v[196:199], v[2:5]
	v_mfma_f32_16x16x32_bf16 v[102:105], v[188:191], v[196:199], v[102:105]
	v_mfma_f32_16x16x32_bf16 v[106:109], v[180:183], v[204:207], v[106:109]
	v_mfma_f32_16x16x32_bf16 v[110:113], v[188:191], v[204:207], v[110:113]
	v_mfma_f32_16x16x32_bf16 v[114:117], v[180:183], v[212:215], v[114:117]
	v_mfma_f32_16x16x32_bf16 v[118:121], v[188:191], v[212:215], v[118:121]
	v_mfma_f32_16x16x32_bf16 v[122:125], v[180:183], v[220:223], v[122:125]
	v_mfma_f32_16x16x32_bf16 v[126:129], v[188:191], v[220:223], v[126:129]
	v_mfma_f32_16x16x32_bf16 v[2:5], v[184:187], v[200:203], v[2:5]
	v_mfma_f32_16x16x32_bf16 v[102:105], v[192:195], v[200:203], v[102:105]
	v_mfma_f32_16x16x32_bf16 v[106:109], v[184:187], v[208:211], v[106:109]
	v_mfma_f32_16x16x32_bf16 v[110:113], v[192:195], v[208:211], v[110:113]
	v_mfma_f32_16x16x32_bf16 v[114:117], v[184:187], v[216:219], v[114:117]
	v_mfma_f32_16x16x32_bf16 v[118:121], v[192:195], v[216:219], v[118:121]
	v_mfma_f32_16x16x32_bf16 v[122:125], v[184:187], v[224:227], v[122:125]
	v_mfma_f32_16x16x32_bf16 v[126:129], v[192:195], v[224:227], v[126:129]
	s_barrier
	s_add_i32 s43, s43, 2
	s_add_u32 s2, s2, 0x100
	s_addc_u32 s3, s3, 0
	s_cmp_gt_u32 s43, 13
	s_cbranch_scc0 .LBB0_1011
	s_and_b64 vcc, exec, s[18:19]
	s_cbranch_vccz .LBB0_1014
	s_barrier

; #define GM_STAGE(bufoff, gbase, voff) do { _Pragma("unroll") for (int _i = 0; _i < 2; ++_i) \
;         __builtin_amdgcn_global_load_lds((const unsigned*)((const char*)(gbase) + (voff)[_i]), (LAS unsigned*)(lds + (bufoff) + ldsw + _i * 8192), 16, 0, 0); } while (0)
; #define GM_LDA(dst, b, h) do { _Pragma("unroll") for (int m = 0; m < 4; ++m) _Pragma("unroll") for (int k = 0; k < 2; ++k) dst[m][k] = *(const LAS s16x8*)(lds + GM_SA(b, h) + aoff + m * 2048 + k * 1024); } while (0)
; #define GM_LDB(dst, b, h) do { _Pragma("unroll") for (int n = 0; n < 2; ++n) _Pragma("unroll") for (int k = 0; k < 2; ++k) dst[n][k] = *(const LAS s16x8*)(lds + GM_SB(b, h) + boff + n * 2048 + k * 1024); } while (0)
; #define GM_MMA(ai, bj, At, Bt) do { __builtin_amdgcn_s_setprio(1); _Pragma("unroll") for (int m = 0; m < 4; ++m) _Pragma("unroll") for (int n = 0; n < 2; ++n) _Pragma("unroll") for (int k = 0; k < 2; ++k) \
;         acc[ai][bj][m][n] = mma16<BF>(Bt[n][k], At[m][k], acc[ai][bj][m][n]); __builtin_amdgcn_s_setprio(0); } while (0)
; #define GM_WAIT_V(n) asm volatile("s_waitcnt vmcnt(" #n ")" ::: "memory")
; #define GM_WAIT_L(n) asm volatile("s_waitcnt lgkmcnt(" #n ")" ::: "memory")
; #define GM_BAR __builtin_amdgcn_s_barrier()
; template <bool BF, bool GATHER = false, class Epi, class Hook>
; __device__ __forceinline__ void gemm_phase(LAS unsigned char* lds, const Gemm g, const Order& S, const Epi& E, Hook& HK) {
;     ...
;             const char* a1 = cA + (size_t)(t + 1) * kstep;
;             const char* a2 = last ? nA : cA + (size_t)(t + 2) * kstep; const char* b2 = last ? nB : cB + (size_t)(t + 2) * kstep;
;             const char* a3 = a2 + kstep; const char* b3 = b2 + kstep;
;             unsigned s0[2], s1[2];
;             if constexpr (GATHER) { s0[0] = last ? nA0[0] : gA0[0]; s0[1] = last ? nA0[1] : gA0[1]; s1[0] = last ? nA1[0] : gA1[0]; s1[1] = last ? nA1[1] : gA1[1]; }
;             GM_LDB(B0, 0, 0); GM_LDB(B1, 0, 1); GM_SCHED; GM_LDA(At, 0, 0); GM_STA_H1(GM_SA(1, 1), a1, gA1);
;             GM_WAIT_V(8); GM_WAIT_L(0); GM_BAR; GM_MMA(0, 0, At, B0); GM_MMA(0, 1, At, B1); GM_BAR; GM_SCHED;
;             GM_LDA(At, 0, 1); GM_STAGE(GM_SB(0, 0), b2, voffB); GM_STAGE(GM_SB(0, 1), b2 + hstepB, voffB); GM_STA_H0(GM_SA(0, 0), a2, s0);
;             GM_WAIT_V(8); GM_WAIT_L(0); GM_BAR; GM_MMA(1, 0, At, B0); GM_MMA(1, 1, At, B1); GM_BAR; GM_SCHED;
.LBB0_1102:
	s_add_u32 s22, s2, 0x100
	s_addc_u32 s23, s3, 0
	s_cmp_eq_u32 s51, 40
	s_cselect_b32 s27, s7, s23
	s_cselect_b32 s26, s6, s22
	s_cselect_b32 s25, s21, s50
	s_cselect_b32 s24, s20, s49
	v_lshl_add_u64 v[216:217], s[2:3], 0, v[138:139]
	s_add_i32 m0, s29, 0xc000
	global_load_lds_dwordx4 v[216:217], off
	v_lshl_add_u64 v[216:217], s[2:3], 0, v[140:141]
	s_add_i32 m0, s29, 0xe000
	s_nop 0
	global_load_lds_dwordx4 v[216:217], off
	ds_read_b128 v[146:149], v153
	ds_read_b128 v[156:159], v153 offset:1024
	ds_read_b128 v[160:163], v153 offset:2048
	ds_read_b128 v[164:167], v153 offset:3072
	ds_read_b128 v[168:171], v154
	ds_read_b128 v[172:175], v154 offset:1024
	ds_read_b128 v[176:179], v154 offset:2048
	ds_read_b128 v[180:183], v154 offset:3072
	ds_read_b128 v[184:187], v155
	ds_read_b128 v[188:191], v155 offset:1024
	ds_read_b128 v[192:195], v155 offset:2048
	ds_read_b128 v[196:199], v155 offset:3072
	ds_read_b128 v[200:203], v155 offset:4096
	ds_read_b128 v[204:207], v155 offset:5120
	ds_read_b128 v[208:211], v155 offset:6144
	ds_read_b128 v[212:215], v155 offset:7168
	s_waitcnt vmcnt(8)
	s_waitcnt lgkmcnt(0)
	s_barrier
	s_waitcnt lgkmcnt(0)
	v_mfma_f32_16x16x32_bf16 v[126:129], v[146:149], v[184:187], v[126:129]
	v_mfma_f32_16x16x32_bf16 v[122:125], v[160:163], v[184:187], v[122:125]
	v_mfma_f32_16x16x32_bf16 v[110:113], v[146:149], v[192:195], v[110:113]
	v_mfma_f32_16x16x32_bf16 v[106:109], v[160:163], v[192:195], v[106:109]
	v_mfma_f32_16x16x32_bf16 v[94:97], v[146:149], v[200:203], v[94:97]
	v_mfma_f32_16x16x32_bf16 v[90:93], v[160:163], v[200:203], v[90:93]
	v_mfma_f32_16x16x32_bf16 v[78:81], v[146:149], v[208:211], v[78:81]
	v_mfma_f32_16x16x32_bf16 v[74:77], v[160:163], v[208:211], v[74:77]
	v_mfma_f32_16x16x32_bf16 v[126:129], v[156:159], v[188:191], v[126:129]
	v_mfma_f32_16x16x32_bf16 v[122:125], v[164:167], v[188:191], v[122:125]
	v_mfma_f32_16x16x32_bf16 v[110:113], v[156:159], v[196:199], v[110:113]
	v_mfma_f32_16x16x32_bf16 v[106:109], v[164:167], v[196:199], v[106:109]
	v_mfma_f32_16x16x32_bf16 v[94:97], v[156:159], v[204:207], v[94:97]
	v_mfma_f32_16x16x32_bf16 v[90:93], v[164:167], v[204:207], v[90:93]
	v_mfma_f32_16x16x32_bf16 v[78:81], v[156:159], v[212:215], v[78:81]
	v_mfma_f32_16x16x32_bf16 v[74:77], v[164:167], v[212:215], v[74:77]
	v_mfma_f32_16x16x32_bf16 v[118:121], v[168:171], v[184:187], v[118:121]
	v_mfma_f32_16x16x32_bf16 v[114:117], v[176:179], v[184:187], v[114:117]
	v_mfma_f32_16x16x32_bf16 v[102:105], v[168:171], v[192:195], v[102:105]
	v_mfma_f32_16x16x32_bf16 v[98:101], v[176:179], v[192:195], v[98:101]
	v_mfma_f32_16x16x32_bf16 v[86:89], v[168:171], v[200:203], v[86:89]
	v_mfma_f32_16x16x32_bf16 v[82:85], v[176:179], v[200:203], v[82:85]
	v_mfma_f32_16x16x32_bf16 v[70:73], v[168:171], v[208:211], v[70:73]
	v_mfma_f32_16x16x32_bf16 v[66:69], v[176:179], v[208:211], v[66:69]
	v_mfma_f32_16x16x32_bf16 v[118:121], v[172:175], v[188:191], v[118:121]
	v_mfma_f32_16x16x32_bf16 v[114:117], v[180:183], v[188:191], v[114:117]
	v_mfma_f32_16x16x32_bf16 v[102:105], v[172:175], v[196:199], v[102:105]
	v_mfma_f32_16x16x32_bf16 v[98:101], v[180:183], v[196:199], v[98:101]
	v_mfma_f32_16x16x32_bf16 v[86:89], v[172:175], v[204:207], v[86:89]
	v_mfma_f32_16x16x32_bf16 v[82:85], v[180:183], v[204:207], v[82:85]
	v_mfma_f32_16x16x32_bf16 v[70:73], v[172:175], v[212:215], v[70:73]
	v_mfma_f32_16x16x32_bf16 v[66:69], v[180:183], v[212:215], v[66:69]
	s_barrier
	s_add_i32 s2, s42, s28
	v_lshl_add_u64 v[216:217], s[24:25], 0, v[132:133]
	s_mov_b32 m0, s2
	global_load_lds_dwordx4 v[216:217], off
	s_add_i32 m0, s2, 0x2000
	s_add_u32 s2, s24, 0xb0000
	v_lshl_add_u64 v[218:219], s[24:25], 0, v[136:137]
	s_addc_u32 s3, s25, 0
	s_add_i32 s52, s43, s28
	global_load_lds_dwordx4 v[218:219], off
	v_lshl_add_u64 v[220:221], s[2:3], 0, v[132:133]
	s_mov_b32 m0, s52
	v_lshl_add_u64 v[222:223], s[26:27], 0, v[134:135]
	global_load_lds_dwordx4 v[220:221], off
	v_lshl_add_u64 v[220:221], s[2:3], 0, v[136:137]
	s_add_i32 m0, s52, 0x2000
	s_nop 0
	global_load_lds_dwordx4 v[220:221], off
	v_lshl_add_u64 v[220:221], s[26:27], 0, v[130:131]
	s_mov_b32 m0, s29
	s_nop 0
	global_load_lds_dwordx4 v[220:221], off
	s_mov_b32 m0, s30
	s_nop 0
	global_load_lds_dwordx4 v[222:223], off
	ds_read_b128 v[184:187], v155 offset:16384
	ds_read_b128 v[188:191], v155 offset:17408
	ds_read_b128 v[192:195], v155 offset:18432
	ds_read_b128 v[196:199], v155 offset:19456
	ds_read_b128 v[200:203], v155 offset:20480
	ds_read_b128 v[204:207], v155 offset:21504
	ds_read_b128 v[208:211], v155 offset:22528
	ds_read_b128 v[212:215], v155 offset:23552
	s_waitcnt vmcnt(8)
	s_waitcnt lgkmcnt(0)
	s_barrier
; #define GM_STAGE(bufoff, gbase, voff) do { _Pragma("unroll") for (int _i = 0; _i < 2; ++_i) \
;         __builtin_amdgcn_global_load_lds((const unsigned*)((const char*)(gbase) + (voff)[_i]), (LAS unsigned*)(lds + (bufoff) + ldsw + _i * 8192), 16, 0, 0); } while (0)
; #define GM_LDA(dst, b, h) do { _Pragma("unroll") for (int m = 0; m < 4; ++m) _Pragma("unroll") for (int k = 0; k < 2; ++k) dst[m][k] = *(const LAS s16x8*)(lds + GM_SA(b, h) + aoff + m * 2048 + k * 1024); } while (0)
; #define GM_LDB(dst, b, h) do { _Pragma("unroll") for (int n = 0; n < 2; ++n) _Pragma("unroll") for (int k = 0; k < 2; ++k) dst[n][k] = *(const LAS s16x8*)(lds + GM_SB(b, h) + boff + n * 2048 + k * 1024); } while (0)
; #define GM_MMA(ai, bj, At, Bt) do { __builtin_amdgcn_s_setprio(1); _Pragma("unroll") for (int m = 0; m < 4; ++m) _Pragma("unroll") for (int n = 0; n < 2; ++n) _Pragma("unroll") for (int k = 0; k < 2; ++k) \
;         acc[ai][bj][m][n] = mma16<BF>(Bt[n][k], At[m][k], acc[ai][bj][m][n]); __builtin_amdgcn_s_setprio(0); } while (0)
; #define GM_WAIT_V(n) asm volatile("s_waitcnt vmcnt(" #n ")" ::: "memory")
; #define GM_WAIT_L(n) asm volatile("s_waitcnt lgkmcnt(" #n ")" ::: "memory")
; #define GM_BAR __builtin_amdgcn_s_barrier()
; #define GM_SCHED __builtin_amdgcn_sched_barrier(0)
; #define GM_STA_H0(buf, p, o0) do { if constexpr (GATHER) GM_STAGE(buf, p, o0); else GM_STAGE(buf, p, voffA); } while (0)
; #define GM_STA_H1(buf, p, o1) do { if constexpr (GATHER) GM_STAGE(buf, p, o1); else GM_STAGE(buf, (p) + hstepB, voffA); } while (0)
; template <bool BF, bool GATHER = false, class Epi, class Hook>
; __device__ __forceinline__ void gemm_phase(LAS unsigned char* lds, const Gemm g, const Order& S, const Epi& E, Hook& HK) {
;     ...
;             GM_WAIT_V(8); GM_WAIT_L(0); GM_BAR; GM_MMA(1, 0, At, B0); GM_MMA(1, 1, At, B1); GM_BAR; GM_SCHED;
;             GM_LDB(B0, 1, 0); GM_LDB(B1, 1, 1); GM_SCHED; GM_LDA(At, 1, 0); GM_STA_H1(GM_SA(0, 1), a2, s1);
;             GM_WAIT_V(8); GM_WAIT_L(0); GM_BAR; GM_MMA(0, 0, At, B0); GM_MMA(0, 1, At, B1); GM_BAR; GM_SCHED;
;             GM_LDA(At, 1, 1); GM_STAGE(GM_SB(1, 0), b3, voffB); GM_STAGE(GM_SB(1, 1), b3 + hstepB, voffB); GM_STA_H0(GM_SA(1, 0), a3, s0);
;             GM_WAIT_V(8); GM_WAIT_L(0); GM_BAR; GM_MMA(1, 0, At, B0); GM_MMA(1, 1, At, B1); GM_BAR; GM_SCHED;
	s_waitcnt lgkmcnt(0)
	v_mfma_f32_16x16x32_bf16 v[62:65], v[146:149], v[184:187], v[62:65]
	v_mfma_f32_16x16x32_bf16 v[58:61], v[160:163], v[184:187], v[58:61]
	v_mfma_f32_16x16x32_bf16 v[46:49], v[146:149], v[192:195], v[46:49]
	v_mfma_f32_16x16x32_bf16 v[42:45], v[160:163], v[192:195], v[42:45]
	v_mfma_f32_16x16x32_bf16 v[30:33], v[146:149], v[200:203], v[30:33]
	v_mfma_f32_16x16x32_bf16 v[26:29], v[160:163], v[200:203], v[26:29]
	v_mfma_f32_16x16x32_bf16 v[14:17], v[146:149], v[208:211], v[14:17]
	v_mfma_f32_16x16x32_bf16 v[10:13], v[160:163], v[208:211], v[10:13]
	v_mfma_f32_16x16x32_bf16 v[62:65], v[156:159], v[188:191], v[62:65]
	v_mfma_f32_16x16x32_bf16 v[58:61], v[164:167], v[188:191], v[58:61]
	v_mfma_f32_16x16x32_bf16 v[46:49], v[156:159], v[196:199], v[46:49]
	v_mfma_f32_16x16x32_bf16 v[42:45], v[164:167], v[196:199], v[42:45]
	v_mfma_f32_16x16x32_bf16 v[30:33], v[156:159], v[204:207], v[30:33]
	v_mfma_f32_16x16x32_bf16 v[26:29], v[164:167], v[204:207], v[26:29]
	v_mfma_f32_16x16x32_bf16 v[14:17], v[156:159], v[212:215], v[14:17]
	v_mfma_f32_16x16x32_bf16 v[10:13], v[164:167], v[212:215], v[10:13]
	v_mfma_f32_16x16x32_bf16 v[54:57], v[168:171], v[184:187], v[54:57]
	v_mfma_f32_16x16x32_bf16 v[50:53], v[176:179], v[184:187], v[50:53]
	v_mfma_f32_16x16x32_bf16 v[38:41], v[168:171], v[192:195], v[38:41]
	v_mfma_f32_16x16x32_bf16 v[34:37], v[176:179], v[192:195], v[34:37]
	v_mfma_f32_16x16x32_bf16 v[22:25], v[168:171], v[200:203], v[22:25]
	v_mfma_f32_16x16x32_bf16 v[18:21], v[176:179], v[200:203], v[18:21]
	v_mfma_f32_16x16x32_bf16 v[6:9], v[168:171], v[208:211], v[6:9]
	v_mfma_f32_16x16x32_bf16 v[2:5], v[176:179], v[208:211], v[2:5]
	v_mfma_f32_16x16x32_bf16 v[54:57], v[172:175], v[188:191], v[54:57]
	v_mfma_f32_16x16x32_bf16 v[50:53], v[180:183], v[188:191], v[50:53]
	v_mfma_f32_16x16x32_bf16 v[38:41], v[172:175], v[196:199], v[38:41]
	v_mfma_f32_16x16x32_bf16 v[34:37], v[180:183], v[196:199], v[34:37]
	v_mfma_f32_16x16x32_bf16 v[22:25], v[172:175], v[204:207], v[22:25]
	v_mfma_f32_16x16x32_bf16 v[18:21], v[180:183], v[204:207], v[18:21]
	v_mfma_f32_16x16x32_bf16 v[6:9], v[172:175], v[212:215], v[6:9]
	v_mfma_f32_16x16x32_bf16 v[2:5], v[180:183], v[212:215], v[2:5]
	s_barrier
	s_add_u32 s2, s26, 0xb0000
	s_addc_u32 s3, s27, 0
	s_mov_b32 m0, s31
	v_lshl_add_u64 v[224:225], s[2:3], 0, v[130:131]
	global_load_lds_dwordx4 v[224:225], off
	v_lshl_add_u64 v[224:225], s[2:3], 0, v[134:135]
	s_mov_b32 m0, s33
	s_nop 0
	global_load_lds_dwordx4 v[224:225], off
	s_mov_b32 s53, 0x1c000
	s_mov_b32 s52, 0x18000
	v_add_u32_e32 v244, s52, v150
	v_add_u32_e32 v245, s53, v150
	ds_read_b128 v[146:149], v244
	ds_read_b128 v[156:159], v244 offset:1024
	ds_read_b128 v[160:163], v244 offset:2048
	ds_read_b128 v[164:167], v244 offset:3072
	ds_read_b128 v[168:171], v245
	ds_read_b128 v[172:175], v245 offset:1024
	ds_read_b128 v[176:179], v245 offset:2048
	ds_read_b128 v[180:183], v245 offset:3072
	ds_read_b128 v[184:187], v155 offset:32768
	ds_read_b128 v[188:191], v155 offset:33792
	ds_read_b128 v[192:195], v155 offset:34816
	ds_read_b128 v[196:199], v155 offset:35840
	ds_read_b128 v[200:203], v155 offset:36864
	ds_read_b128 v[204:207], v155 offset:37888
	ds_read_b128 v[208:211], v155 offset:38912
	ds_read_b128 v[212:215], v155 offset:39936
	s_waitcnt vmcnt(8)
	s_waitcnt lgkmcnt(0)
	s_barrier
	s_waitcnt lgkmcnt(0)
	v_mfma_f32_16x16x32_bf16 v[126:129], v[146:149], v[184:187], v[126:129]
	v_mfma_f32_16x16x32_bf16 v[122:125], v[160:163], v[184:187], v[122:125]
	v_mfma_f32_16x16x32_bf16 v[110:113], v[146:149], v[192:195], v[110:113]
	v_mfma_f32_16x16x32_bf16 v[106:109], v[160:163], v[192:195], v[106:109]
	v_mfma_f32_16x16x32_bf16 v[94:97], v[146:149], v[200:203], v[94:97]
	v_mfma_f32_16x16x32_bf16 v[90:93], v[160:163], v[200:203], v[90:93]
	v_mfma_f32_16x16x32_bf16 v[78:81], v[146:149], v[208:211], v[78:81]
	v_mfma_f32_16x16x32_bf16 v[74:77], v[160:163], v[208:211], v[74:77]
	v_mfma_f32_16x16x32_bf16 v[126:129], v[156:159], v[188:191], v[126:129]
	v_mfma_f32_16x16x32_bf16 v[122:125], v[164:167], v[188:191], v[122:125]
	v_mfma_f32_16x16x32_bf16 v[110:113], v[156:159], v[196:199], v[110:113]
	v_mfma_f32_16x16x32_bf16 v[106:109], v[164:167], v[196:199], v[106:109]
	v_mfma_f32_16x16x32_bf16 v[94:97], v[156:159], v[204:207], v[94:97]
	v_mfma_f32_16x16x32_bf16 v[90:93], v[164:167], v[204:207], v[90:93]
	v_mfma_f32_16x16x32_bf16 v[78:81], v[156:159], v[212:215], v[78:81]
	v_mfma_f32_16x16x32_bf16 v[74:77], v[164:167], v[212:215], v[74:77]
	v_mfma_f32_16x16x32_bf16 v[118:121], v[168:171], v[184:187], v[118:121]
	v_mfma_f32_16x16x32_bf16 v[114:117], v[176:179], v[184:187], v[114:117]
	v_mfma_f32_16x16x32_bf16 v[102:105], v[168:171], v[192:195], v[102:105]
	v_mfma_f32_16x16x32_bf16 v[98:101], v[176:179], v[192:195], v[98:101]
	v_mfma_f32_16x16x32_bf16 v[86:89], v[168:171], v[200:203], v[86:89]
	v_mfma_f32_16x16x32_bf16 v[82:85], v[176:179], v[200:203], v[82:85]
	v_mfma_f32_16x16x32_bf16 v[70:73], v[168:171], v[208:211], v[70:73]
	v_mfma_f32_16x16x32_bf16 v[66:69], v[176:179], v[208:211], v[66:69]
	v_mfma_f32_16x16x32_bf16 v[118:121], v[172:175], v[188:191], v[118:121]
	v_mfma_f32_16x16x32_bf16 v[114:117], v[180:183], v[188:191], v[114:117]
	v_mfma_f32_16x16x32_bf16 v[102:105], v[172:175], v[196:199], v[102:105]
	v_mfma_f32_16x16x32_bf16 v[98:101], v[180:183], v[196:199], v[98:101]
	v_mfma_f32_16x16x32_bf16 v[86:89], v[172:175], v[204:207], v[86:89]
	v_mfma_f32_16x16x32_bf16 v[82:85], v[180:183], v[204:207], v[82:85]
	v_mfma_f32_16x16x32_bf16 v[70:73], v[172:175], v[212:215], v[70:73]
	v_mfma_f32_16x16x32_bf16 v[66:69], v[180:183], v[212:215], v[66:69]
	s_barrier
; #define GM_STAGE(bufoff, gbase, voff) do { _Pragma("unroll") for (int _i = 0; _i < 2; ++_i) \
;         __builtin_amdgcn_global_load_lds((const unsigned*)((const char*)(gbase) + (voff)[_i]), (LAS unsigned*)(lds + (bufoff) + ldsw + _i * 8192), 16, 0, 0); } while (0)
; #define GM_LDA(dst, b, h) do { _Pragma("unroll") for (int m = 0; m < 4; ++m) _Pragma("unroll") for (int k = 0; k < 2; ++k) dst[m][k] = *(const LAS s16x8*)(lds + GM_SA(b, h) + aoff + m * 2048 + k * 1024); } while (0)
; #define GM_MMA(ai, bj, At, Bt) do { __builtin_amdgcn_s_setprio(1); _Pragma("unroll") for (int m = 0; m < 4; ++m) _Pragma("unroll") for (int n = 0; n < 2; ++n) _Pragma("unroll") for (int k = 0; k < 2; ++k) \
;         acc[ai][bj][m][n] = mma16<BF>(Bt[n][k], At[m][k], acc[ai][bj][m][n]); __builtin_amdgcn_s_setprio(0); } while (0)
; #define GM_WAIT_V(n) asm volatile("s_waitcnt vmcnt(" #n ")" ::: "memory")
; #define GM_WAIT_L(n) asm volatile("s_waitcnt lgkmcnt(" #n ")" ::: "memory")
; #define GM_BAR __builtin_amdgcn_s_barrier()
; #define GM_SCHED __builtin_amdgcn_sched_barrier(0)
; #define GM_STA_H0(buf, p, o0) do { if constexpr (GATHER) GM_STAGE(buf, p, o0); else GM_STAGE(buf, p, voffA); } while (0)
; template <bool BF, bool GATHER = false, class Epi, class Hook>
; __device__ __forceinline__ void gemm_phase(LAS unsigned char* lds, const Gemm g, const Order& S, const Epi& E, Hook& HK) {
;     ...
;             GM_WAIT_V(8); GM_WAIT_L(0); GM_BAR; GM_MMA(0, 0, At, B0); GM_MMA(0, 1, At, B1); GM_BAR; GM_SCHED;
;             GM_LDA(At, 1, 1); GM_STAGE(GM_SB(1, 0), b3, voffB); GM_STAGE(GM_SB(1, 1), b3 + hstepB, voffB); GM_STA_H0(GM_SA(1, 0), a3, s0);
;             GM_WAIT_V(8); GM_WAIT_L(0); GM_BAR; GM_MMA(1, 0, At, B0); GM_MMA(1, 1, At, B1); GM_BAR; GM_SCHED;
;         }
	s_add_i32 s2, s52, s28
	v_lshl_add_u64 v[216:217], v[216:217], 0, s[12:13]
	s_mov_b32 m0, s2
	global_load_lds_dwordx4 v[216:217], off
	s_add_i32 m0, s2, 0x2000
	s_add_u32 s2, s24, 0xb0080
	v_lshl_add_u64 v[216:217], v[218:219], 0, s[12:13]
	s_addc_u32 s3, s25, 0
	s_add_i32 s24, s53, s28
	global_load_lds_dwordx4 v[216:217], off
	v_lshl_add_u64 v[216:217], s[2:3], 0, v[132:133]
	s_mov_b32 m0, s24
	s_nop 0
	global_load_lds_dwordx4 v[216:217], off
	v_lshl_add_u64 v[216:217], s[2:3], 0, v[136:137]
	s_add_i32 m0, s24, 0x2000
	s_nop 0
	global_load_lds_dwordx4 v[216:217], off
	v_lshl_add_u64 v[216:217], v[220:221], 0, s[12:13]
	s_mov_b32 m0, s36
	s_nop 0
	global_load_lds_dwordx4 v[216:217], off
	v_lshl_add_u64 v[216:217], v[222:223], 0, s[12:13]
	s_mov_b32 m0, s37
	s_nop 0
	global_load_lds_dwordx4 v[216:217], off
	ds_read_b128 v[184:187], v155 offset:49152
	ds_read_b128 v[188:191], v155 offset:50176
	ds_read_b128 v[192:195], v155 offset:51200
	ds_read_b128 v[196:199], v155 offset:52224
	ds_read_b128 v[200:203], v155 offset:53248
	ds_read_b128 v[204:207], v155 offset:54272
	ds_read_b128 v[208:211], v155 offset:55296
	ds_read_b128 v[212:215], v155 offset:56320
	s_waitcnt vmcnt(8)
	s_waitcnt lgkmcnt(0)
	s_barrier
	s_waitcnt lgkmcnt(0)
	v_mfma_f32_16x16x32_bf16 v[62:65], v[146:149], v[184:187], v[62:65]
	v_mfma_f32_16x16x32_bf16 v[58:61], v[160:163], v[184:187], v[58:61]
	v_mfma_f32_16x16x32_bf16 v[46:49], v[146:149], v[192:195], v[46:49]
	v_mfma_f32_16x16x32_bf16 v[42:45], v[160:163], v[192:195], v[42:45]
	v_mfma_f32_16x16x32_bf16 v[30:33], v[146:149], v[200:203], v[30:33]
	v_mfma_f32_16x16x32_bf16 v[26:29], v[160:163], v[200:203], v[26:29]
	v_mfma_f32_16x16x32_bf16 v[14:17], v[146:149], v[208:211], v[14:17]
	v_mfma_f32_16x16x32_bf16 v[10:13], v[160:163], v[208:211], v[10:13]
	v_mfma_f32_16x16x32_bf16 v[62:65], v[156:159], v[188:191], v[62:65]
	v_mfma_f32_16x16x32_bf16 v[58:61], v[164:167], v[188:191], v[58:61]
	v_mfma_f32_16x16x32_bf16 v[46:49], v[156:159], v[196:199], v[46:49]
	v_mfma_f32_16x16x32_bf16 v[42:45], v[164:167], v[196:199], v[42:45]
	v_mfma_f32_16x16x32_bf16 v[30:33], v[156:159], v[204:207], v[30:33]
	v_mfma_f32_16x16x32_bf16 v[26:29], v[164:167], v[204:207], v[26:29]
	v_mfma_f32_16x16x32_bf16 v[14:17], v[156:159], v[212:215], v[14:17]
	v_mfma_f32_16x16x32_bf16 v[10:13], v[164:167], v[212:215], v[10:13]
	v_mfma_f32_16x16x32_bf16 v[54:57], v[168:171], v[184:187], v[54:57]
	v_mfma_f32_16x16x32_bf16 v[50:53], v[176:179], v[184:187], v[50:53]
	v_mfma_f32_16x16x32_bf16 v[38:41], v[168:171], v[192:195], v[38:41]
	v_mfma_f32_16x16x32_bf16 v[34:37], v[176:179], v[192:195], v[34:37]
	v_mfma_f32_16x16x32_bf16 v[22:25], v[168:171], v[200:203], v[22:25]
	v_mfma_f32_16x16x32_bf16 v[18:21], v[176:179], v[200:203], v[18:21]
	v_mfma_f32_16x16x32_bf16 v[6:9], v[168:171], v[208:211], v[6:9]
	v_mfma_f32_16x16x32_bf16 v[2:5], v[176:179], v[208:211], v[2:5]
	v_mfma_f32_16x16x32_bf16 v[54:57], v[172:175], v[188:191], v[54:57]
	v_mfma_f32_16x16x32_bf16 v[50:53], v[180:183], v[188:191], v[50:53]
	v_mfma_f32_16x16x32_bf16 v[38:41], v[172:175], v[196:199], v[38:41]
	v_mfma_f32_16x16x32_bf16 v[34:37], v[180:183], v[196:199], v[34:37]
	v_mfma_f32_16x16x32_bf16 v[22:25], v[172:175], v[204:207], v[22:25]
	v_mfma_f32_16x16x32_bf16 v[18:21], v[180:183], v[204:207], v[18:21]
	v_mfma_f32_16x16x32_bf16 v[6:9], v[172:175], v[212:215], v[6:9]
	v_mfma_f32_16x16x32_bf16 v[2:5], v[180:183], v[212:215], v[2:5]
	s_barrier
	s_add_i32 s51, s51, 2
	s_add_u32 s49, s49, 0x100
	s_addc_u32 s50, s50, 0
	s_cmp_gt_u32 s51, 41
	s_mov_b64 s[2:3], s[22:23]
	s_cbranch_scc0 .LBB0_1102
	s_and_b64 vcc, exec, s[14:15]
	s_cbranch_vccz .LBB0_1105
	s_barrier

; #define LAS __attribute__((address_space(3)))
; template <bool BF> __device__ __forceinline__ unsigned pk16(float lo, float hi) { return BF ? pkb(lo, hi) : pkh(lo, hi); }
; template <bool BF, class RowMap>
; __device__ __forceinline__ void cvt_block(const float* W, int K, int N, f16* WT, const RowMap& rm, int item, int tid, LAS unsigned char* S) {
;     const int lane = tid & 63, wave = tid >> 6;
;     const int nblk = N / 128, kb = item / nblk, nb = item % nblk, k0 = 256 * kb, n0 = 128 * nb;
;     const float* src = W + (size_t)(k0 + 32 * wave + (lane >> 5)) * N + n0 + 4 * (lane & 31);
;     f32x4 v[16];
; #pragma unroll
;     for (int i = 0; i < 16; ++i) v[i] = *(const f32x4*)(src + (size_t)(2 * i) * N);
; #pragma unroll
;     for (int i = 0; i < 16; ++i) { u32x2 w; w.x = pk16<BF>(v[i][0], v[i][1]); w.y = pk16<BF>(v[i][2], v[i][3]);
;         *(LAS u32x2*)(S + (32 * wave + 2 * i + (lane >> 5)) * CVB_RS + 8 * (lane & 31)) = w; }
; __device__ __forceinline__ void cvt_moe(const float* w1, const float* w3, const float* w2, f16* W13, f16* W2T, int tid, LAS unsigned char* S) {
;     constexpr int I13 = (DM / 256) * (DE / 128), I2 = (DE / 256) * (DM / 128);
;     constexpr int NIT = NE * (2 * I13 + I2);
;     for (int it = blockIdx.x; it < NIT; it += gridDim.x) {
;         const int e = it / (2 * I13 + I2); int r = it % (2 * I13 + I2);
;         if (r < I13) { cvt_block<MOE_BF16>(w1 + (size_t)e * DM * DE, DM, DE, W13 + (size_t)e * 2 * DE * DM, MapGLU{0}, r, tid, S); continue; } r -= I13;
;         if (r < I13) { cvt_block<MOE_BF16>(w3 + (size_t)e * DM * DE, DM, DE, W13 + (size_t)e * 2 * DE * DM, MapGLU{128}, r, tid, S); continue; } r -= I13;
;         cvt_block<MOE_BF16>(w2 + (size_t)e * DE * DM, DE, DM, W2T + (size_t)e * DM * DE, MapPlain{}, r, tid, S);
.LBB0_1209:
	s_mul_hi_i32 s0, s35, 0x3e0f83e1
	s_lshr_b32 s2, s0, 31
	s_ashr_i32 s37, s0, 6
	s_add_i32 s37, s37, s2
	s_mul_i32 s0, s37, 0xfffffef8
	s_add_i32 s36, s35, s0
	s_cmpk_gt_i32 s36, 0x57
	s_mov_b64 s[2:3], -1
	s_cbranch_scc0 .LBB0_1215
	s_cmpk_gt_u32 s36, 0xaf
	s_cbranch_scc0 .LBB0_1212
	v_readlane_b32 s40, v251, 0
	s_mul_i32 s2, s37, 0xb00000
	v_readlane_b32 s44, v251, 4
	s_mul_hi_i32 s0, s37, 0xb00000
	v_readlane_b32 s41, v251, 1
	v_readlane_b32 s45, v251, 5
	s_add_u32 s40, s44, s2
	s_addc_u32 s41, s45, s0
	s_mul_i32 s2, s37, 0x580000
	s_mul_hi_i32 s0, s37, 0x580000
	s_add_u32 s3, s78, s2
	v_readlane_b32 s2, v250, 16
	s_addc_u32 s38, s2, s0
	s_lshl_b32 s0, s37, 8
	s_sub_i32 s0, s6, s0
	s_and_b32 s39, s0, 0xf00
	v_or_b32_e32 v5, s39, v1
	s_and_b32 s2, s4, 0x380
	v_lshlrev_b32_e32 v22, 12, v5
	v_mov_b32_e32 v23, v3
	v_lshl_add_u64 v[22:23], s[40:41], 0, v[22:23]
	s_lshl_b32 s0, s2, 2
	v_lshl_add_u64 v[22:23], v[22:23], 0, s[0:1]
	v_lshl_add_u64 v[82:83], v[22:23], 0, v[2:3]
	s_movk_i32 s0, 0x2000
	v_add_co_u32_e32 v26, vcc, s0, v82
	s_movk_i32 s0, 0x4000
	s_nop 0
	v_addc_co_u32_e32 v27, vcc, 0, v83, vcc
	v_add_co_u32_e32 v30, vcc, s0, v82
	s_movk_i32 s0, 0x6000
	s_nop 0
	v_addc_co_u32_e32 v31, vcc, 0, v83, vcc
	v_add_co_u32_e32 v34, vcc, s0, v82
	s_mov_b32 s0, 0x8000
	s_nop 0
	v_addc_co_u32_e32 v35, vcc, 0, v83, vcc
	v_add_co_u32_e32 v38, vcc, s0, v82
	global_load_dwordx4 v[22:25], v[82:83], off nt
	s_nop 0
	global_load_dwordx4 v[26:29], v[26:27], off nt
	v_addc_co_u32_e32 v39, vcc, 0, v83, vcc
	v_add_co_u32_e32 v42, vcc, s10, v82
	global_load_dwordx4 v[30:33], v[30:31], off nt
	s_nop 0
	global_load_dwordx4 v[34:37], v[34:35], off nt
	v_addc_co_u32_e32 v43, vcc, 0, v83, vcc
	v_add_co_u32_e32 v46, vcc, s11, v82
	global_load_dwordx4 v[38:41], v[38:39], off nt
	s_nop 0
	global_load_dwordx4 v[42:45], v[42:43], off nt
	v_addc_co_u32_e32 v47, vcc, 0, v83, vcc
	v_add_co_u32_e32 v50, vcc, s12, v82
	s_lshl_b32 s0, s39, 1
	s_nop 0
	v_addc_co_u32_e32 v51, vcc, 0, v83, vcc
	v_add_co_u32_e32 v54, vcc, s13, v82
	global_load_dwordx4 v[46:49], v[46:47], off nt
	s_nop 0
	global_load_dwordx4 v[50:53], v[50:51], off nt
	v_addc_co_u32_e32 v55, vcc, 0, v83, vcc
	v_add_co_u32_e32 v58, vcc, s14, v82
	s_add_u32 s40, s3, s0
	s_nop 0
	v_addc_co_u32_e32 v59, vcc, 0, v83, vcc
	v_add_co_u32_e32 v62, vcc, s15, v82
	global_load_dwordx4 v[54:57], v[54:55], off nt
	s_nop 0
	global_load_dwordx4 v[58:61], v[58:59], off nt
	v_addc_co_u32_e32 v63, vcc, 0, v83, vcc
	v_add_co_u32_e32 v66, vcc, s16, v82
	s_addc_u32 s41, s38, 0
	s_nop 0
	v_addc_co_u32_e32 v67, vcc, 0, v83, vcc
	v_add_co_u32_e32 v70, vcc, s17, v82
	global_load_dwordx4 v[62:65], v[62:63], off nt
	s_nop 0
	global_load_dwordx4 v[66:69], v[66:67], off nt
	v_addc_co_u32_e32 v71, vcc, 0, v83, vcc
	v_add_co_u32_e32 v74, vcc, s18, v82
	v_mov_b32_e32 v5, v3
	s_nop 0
	v_addc_co_u32_e32 v75, vcc, 0, v83, vcc
	v_add_co_u32_e32 v78, vcc, s19, v82
	global_load_dwordx4 v[70:73], v[70:71], off nt
	s_nop 0
	global_load_dwordx4 v[74:77], v[74:75], off nt
	v_addc_co_u32_e32 v79, vcc, 0, v83, vcc
	v_add_co_u32_e32 v82, vcc, s20, v82
	global_load_dwordx4 v[78:81], v[78:79], off nt
	s_nop 0
	v_addc_co_u32_e32 v83, vcc, 0, v83, vcc
	global_load_dwordx4 v[82:85], v[82:83], off nt
	v_readlane_b32 s42, v251, 2
	v_readlane_b32 s43, v251, 3
	v_readlane_b32 s46, v251, 6
	v_readlane_b32 s47, v251, 7
	s_waitcnt vmcnt(15)
	v_cvt_pk_bf16_f32 v22, v22, v23
	v_cvt_pk_bf16_f32 v23, v24, v25
	s_waitcnt vmcnt(14)
	v_cvt_pk_bf16_f32 v24, v26, v27
	v_cvt_pk_bf16_f32 v25, v28, v29
	ds_write2_b64 v14, v[22:23], v[24:25] offset1:66
	s_waitcnt vmcnt(13)
	v_cvt_pk_bf16_f32 v22, v30, v31
	v_cvt_pk_bf16_f32 v23, v32, v33
	s_waitcnt vmcnt(12)
	v_cvt_pk_bf16_f32 v24, v34, v35
	v_cvt_pk_bf16_f32 v25, v36, v37
	ds_write2_b64 v14, v[22:23], v[24:25] offset0:132 offset1:198
	s_waitcnt vmcnt(11)
	v_cvt_pk_bf16_f32 v22, v38, v39
	v_cvt_pk_bf16_f32 v23, v40, v41
	s_waitcnt vmcnt(10)
	v_cvt_pk_bf16_f32 v24, v42, v43
	v_cvt_pk_bf16_f32 v25, v44, v45
	ds_write2_b64 v18, v[22:23], v[24:25] offset0:8 offset1:74
	s_waitcnt vmcnt(9)
	v_cvt_pk_bf16_f32 v22, v46, v47
	v_cvt_pk_bf16_f32 v23, v48, v49
	s_waitcnt vmcnt(8)
	v_cvt_pk_bf16_f32 v24, v50, v51
	v_cvt_pk_bf16_f32 v25, v52, v53
	ds_write2_b64 v18, v[22:23], v[24:25] offset0:140 offset1:206
	s_waitcnt vmcnt(7)
	v_cvt_pk_bf16_f32 v22, v54, v55
	v_cvt_pk_bf16_f32 v23, v56, v57
	s_waitcnt vmcnt(6)
	v_cvt_pk_bf16_f32 v24, v58, v59
	v_cvt_pk_bf16_f32 v25, v60, v61
	ds_write2_b64 v19, v[22:23], v[24:25] offset0:16 offset1:82
	s_waitcnt vmcnt(5)
	v_cvt_pk_bf16_f32 v22, v62, v63
	v_cvt_pk_bf16_f32 v23, v64, v65
	s_waitcnt vmcnt(4)
	v_cvt_pk_bf16_f32 v24, v66, v67
	v_cvt_pk_bf16_f32 v25, v68, v69
	ds_write2_b64 v19, v[22:23], v[24:25] offset0:148 offset1:214
	s_waitcnt vmcnt(3)
	v_cvt_pk_bf16_f32 v22, v70, v71
	v_cvt_pk_bf16_f32 v23, v72, v73
	s_waitcnt vmcnt(2)
	v_cvt_pk_bf16_f32 v24, v74, v75
	v_cvt_pk_bf16_f32 v25, v76, v77
	ds_write2_b64 v20, v[22:23], v[24:25] offset0:24 offset1:90
	s_waitcnt vmcnt(1)
	v_cvt_pk_bf16_f32 v22, v78, v79
	v_cvt_pk_bf16_f32 v23, v80, v81
	s_waitcnt vmcnt(0)
	v_cvt_pk_bf16_f32 v24, v82, v83
	v_cvt_pk_bf16_f32 v25, v84, v85
	ds_write2_b64 v20, v[22:23], v[24:25] offset0:156 offset1:222
	s_waitcnt lgkmcnt(0)
	s_barrier
; #define LAS __attribute__((address_space(3)))
; #define LDS_WAIT() asm volatile("s_waitcnt lgkmcnt(0)" ::: "memory")
; template <bool BF, class RowMap>
; __device__ __forceinline__ void cvt_block(const float* W, int K, int N, f16* WT, const RowMap& rm, int item, int tid, LAS unsigned char* S) {
;     ...
;     const int nblk = N / 128, kb = item / nblk, nb = item % nblk, k0 = 256 * kb, n0 = 128 * nb;
;     const float* src = W + (size_t)(k0 + 32 * wave + (lane >> 5)) * N + n0 + 4 * (lane & 31);
;     f32x4 v[16];
; #pragma unroll
;     for (int i = 0; i < 16; ++i) v[i] = *(const f32x4*)(src + (size_t)(2 * i) * N);
;     ...
;     __syncthreads();
; #pragma unroll
;     for (int st = 0; st < 8; ++st) *(LAS u32x4*)(T + (16 * wave + i16) * CVT_TS + 16 * (4 * st + g)) = wv[st];
;     LDS_WAIT();
; #pragma unroll
;     for (int j = 0; j < 8; ++j) { const int nr = 16 * wave + 2 * j + (lane >> 5), ch = lane & 31;
;         const u32x4 w = *(const LAS u32x4*)(T + nr * CVT_TS + 16 * ch);
;         *(u32x4*)(WT + (size_t)rm(n0 + nr) * K + k0 + 8 * ch) = w; }
;     __syncthreads();
	ds_read_b64_tr_b16 v[22:23], v15
	ds_read_b64_tr_b16 v[24:25], v15 offset:1056
	ds_read_b64_tr_b16 v[26:27], v15 offset:8448
	ds_read_b64_tr_b16 v[28:29], v15 offset:9504
	ds_read_b64_tr_b16 v[30:31], v15 offset:16896
	ds_read_b64_tr_b16 v[32:33], v15 offset:17952
	ds_read_b64_tr_b16 v[34:35], v15 offset:25344
	ds_read_b64_tr_b16 v[36:37], v15 offset:26400
	ds_read_b64_tr_b16 v[38:39], v15 offset:33792
	ds_read_b64_tr_b16 v[40:41], v15 offset:34848
	ds_read_b64_tr_b16 v[42:43], v15 offset:42240
	ds_read_b64_tr_b16 v[44:45], v15 offset:43296
	ds_read_b64_tr_b16 v[46:47], v15 offset:50688
	ds_read_b64_tr_b16 v[48:49], v15 offset:51744
	ds_read_b64_tr_b16 v[50:51], v15 offset:59136
	ds_read_b64_tr_b16 v[52:53], v15 offset:60192
	s_waitcnt lgkmcnt(0)
	s_barrier
	ds_write_b128 v16, v[22:25]
	ds_write_b128 v16, v[26:29] offset:64
	ds_write_b128 v16, v[30:33] offset:128
	ds_write_b128 v16, v[34:37] offset:192
	ds_write_b128 v16, v[38:41] offset:256
	ds_write_b128 v16, v[42:45] offset:320
	ds_write_b128 v16, v[46:49] offset:384
	ds_write_b128 v16, v[50:53] offset:448
	s_waitcnt lgkmcnt(0)
	v_lshl_add_u64 v[30:31], s[40:41], 0, v[4:5]
	ds_read_b128 v[22:25], v17
	v_or_b32_e32 v5, s2, v6
	v_mul_u32_u24_e32 v26, 0x1600, v5
	v_mov_b32_e32 v27, v3
	v_lshl_add_u64 v[32:33], v[30:31], 0, v[26:27]
	ds_read_b128 v[26:29], v17 offset:1056
	v_or_b32_e32 v5, s2, v7
	s_waitcnt lgkmcnt(1)
	global_store_dwordx4 v[32:33], v[22:25], off
	s_nop 1
	v_mul_u32_u24_e32 v22, 0x1600, v5
	v_mov_b32_e32 v23, v3
	v_lshl_add_u64 v[22:23], v[30:31], 0, v[22:23]
	s_waitcnt lgkmcnt(0)
	global_store_dwordx4 v[22:23], v[26:29], off
	ds_read_b128 v[22:25], v17 offset:2112
	v_or_b32_e32 v5, s2, v8
	v_mul_u32_u24_e32 v26, 0x1600, v5
	v_mov_b32_e32 v27, v3
	v_lshl_add_u64 v[32:33], v[30:31], 0, v[26:27]
	ds_read_b128 v[26:29], v17 offset:3168
	v_or_b32_e32 v5, s2, v9
	s_waitcnt lgkmcnt(1)
	global_store_dwordx4 v[32:33], v[22:25], off
	s_nop 1
	v_mul_u32_u24_e32 v22, 0x1600, v5
	v_mov_b32_e32 v23, v3
	v_lshl_add_u64 v[22:23], v[30:31], 0, v[22:23]
	s_waitcnt lgkmcnt(0)
	global_store_dwordx4 v[22:23], v[26:29], off
	ds_read_b128 v[22:25], v17 offset:4224
	v_or_b32_e32 v5, s2, v10
	v_mul_u32_u24_e32 v26, 0x1600, v5
	v_mov_b32_e32 v27, v3
	v_lshl_add_u64 v[32:33], v[30:31], 0, v[26:27]
	ds_read_b128 v[26:29], v17 offset:5280
	v_or_b32_e32 v5, s2, v11
	s_waitcnt lgkmcnt(1)
	global_store_dwordx4 v[32:33], v[22:25], off
	s_nop 1
	v_mul_u32_u24_e32 v22, 0x1600, v5
	v_mov_b32_e32 v23, v3
	v_lshl_add_u64 v[22:23], v[30:31], 0, v[22:23]
	s_waitcnt lgkmcnt(0)
	global_store_dwordx4 v[22:23], v[26:29], off
	ds_read_b128 v[22:25], v17 offset:6336
	v_or_b32_e32 v5, s2, v12
	v_mul_u32_u24_e32 v26, 0x1600, v5
	v_mov_b32_e32 v27, v3
	v_lshl_add_u64 v[32:33], v[30:31], 0, v[26:27]
	ds_read_b128 v[26:29], v17 offset:7392
	v_or_b32_e32 v5, s2, v13
	s_waitcnt lgkmcnt(1)
	global_store_dwordx4 v[32:33], v[22:25], off
	s_mov_b64 s[2:3], 0
	s_nop 0
	v_mul_u32_u24_e32 v22, 0x1600, v5
	v_mov_b32_e32 v23, v3
	v_lshl_add_u64 v[22:23], v[30:31], 0, v[22:23]
	s_waitcnt lgkmcnt(0)
	global_store_dwordx4 v[22:23], v[26:29], off
	s_barrier
.LBB0_1212:
	s_andn2_b64 vcc, exec, s[2:3]
	s_cbranch_vccnz .LBB0_1214
	v_readlane_b32 s40, v251, 0
	s_mul_i32 s2, s37, 0xb00000
	v_readlane_b32 s42, v251, 2
	s_mul_hi_i32 s0, s37, 0xb00000
	v_readlane_b32 s41, v251, 1
	v_readlane_b32 s43, v251, 3
	s_add_u32 s40, s42, s2
	s_addc_u32 s41, s43, s0
	s_add_u32 s3, s84, s2
	s_addc_u32 s38, s85, s0
	s_add_i32 s0, s36, 0xffa8
	s_bfe_u32 s2, s0, 0x70001
	s_mulk_i32 s2, 0xbb
	s_bfe_u32 s39, s2, 0x5000b
	s_mul_i32 s2, s39, 22
	s_sub_i32 s2, s0, s2
	v_lshl_or_b32 v5, s39, 8, v1
	s_and_b32 s0, s2, 0xff
	v_mul_u32_u24_e32 v22, 0x2c00, v5
	v_mov_b32_e32 v23, v3
	v_lshl_add_u64 v[22:23], s[40:41], 0, v[22:23]
	s_lshl_b32 s0, s0, 9
	v_lshl_add_u64 v[22:23], v[22:23], 0, s[0:1]
	v_lshl_add_u64 v[82:83], v[22:23], 0, v[2:3]
	v_add_co_u32_e32 v26, vcc, s21, v82
	s_lshl_b32 s0, s39, 9
	s_nop 0
	v_addc_co_u32_e32 v27, vcc, 0, v83, vcc
	v_add_co_u32_e32 v30, vcc, s22, v82
	global_load_dwordx4 v[22:25], v[82:83], off nt
	s_nop 0
	global_load_dwordx4 v[26:29], v[26:27], off offset:2048 nt
	v_addc_co_u32_e32 v31, vcc, 0, v83, vcc
	v_add_co_u32_e32 v34, vcc, s13, v82
	s_add_u32 s40, s3, s0
	s_nop 0
	v_addc_co_u32_e32 v35, vcc, 0, v83, vcc
	v_add_co_u32_e32 v38, vcc, s16, v82
	global_load_dwordx4 v[30:33], v[30:31], off nt
	s_nop 0
	global_load_dwordx4 v[34:37], v[34:35], off offset:2048 nt
	v_addc_co_u32_e32 v39, vcc, 0, v83, vcc
	v_add_co_u32_e32 v42, vcc, s23, v82
	s_addc_u32 s41, s38, 0
	s_nop 0
	v_addc_co_u32_e32 v43, vcc, 0, v83, vcc
	v_add_co_u32_e32 v46, vcc, s24, v82
	global_load_dwordx4 v[38:41], v[38:39], off nt
	s_nop 0
	global_load_dwordx4 v[42:45], v[42:43], off offset:2048 nt
	v_addc_co_u32_e32 v47, vcc, 0, v83, vcc
	v_add_co_u32_e32 v50, vcc, s25, v82
	s_lshl_b32 s0, s2, 8
	s_nop 0
	v_addc_co_u32_e32 v51, vcc, 0, v83, vcc
	v_add_co_u32_e32 v54, vcc, s26, v82
	global_load_dwordx4 v[46:49], v[46:47], off nt
	s_nop 0
	global_load_dwordx4 v[50:53], v[50:51], off offset:2048 nt
	v_addc_co_u32_e32 v55, vcc, 0, v83, vcc
	v_add_co_u32_e32 v58, vcc, s27, v82
	v_mov_b32_e32 v5, v3
	s_nop 0
	v_addc_co_u32_e32 v59, vcc, 0, v83, vcc
	v_add_co_u32_e32 v62, vcc, s28, v82
	global_load_dwordx4 v[54:57], v[54:55], off nt
	s_nop 0
	global_load_dwordx4 v[58:61], v[58:59], off offset:2048 nt
	v_addc_co_u32_e32 v63, vcc, 0, v83, vcc
	v_add_co_u32_e32 v66, vcc, s29, v82
	s_and_b32 s0, s0, 0x3f00
	s_nop 0
	v_addc_co_u32_e32 v67, vcc, 0, v83, vcc
	v_add_co_u32_e32 v70, vcc, s30, v82
	global_load_dwordx4 v[62:65], v[62:63], off nt
	s_nop 0
	global_load_dwordx4 v[66:69], v[66:67], off offset:2048 nt
	v_addc_co_u32_e32 v71, vcc, 0, v83, vcc
	v_add_co_u32_e32 v74, vcc, s31, v82
	v_readlane_b32 s44, v251, 4
	s_nop 0
	v_addc_co_u32_e32 v75, vcc, 0, v83, vcc
	v_add_co_u32_e32 v78, vcc, s33, v82
	global_load_dwordx4 v[70:73], v[70:71], off nt
	s_nop 0
	global_load_dwordx4 v[74:77], v[74:75], off offset:2048 nt
	v_addc_co_u32_e32 v79, vcc, 0, v83, vcc
	v_add_co_u32_e32 v82, vcc, s34, v82
	global_load_dwordx4 v[78:81], v[78:79], off nt
	s_nop 0
	v_addc_co_u32_e32 v83, vcc, 0, v83, vcc
	global_load_dwordx4 v[82:85], v[82:83], off offset:2048 nt
	v_readlane_b32 s45, v251, 5
	v_readlane_b32 s46, v251, 6
	v_readlane_b32 s47, v251, 7
	s_waitcnt vmcnt(15)
; #define LAS __attribute__((address_space(3)))
; #define LDS_WAIT() asm volatile("s_waitcnt lgkmcnt(0)" ::: "memory")
; template <bool BF> __device__ __forceinline__ unsigned pk16(float lo, float hi) { return BF ? pkb(lo, hi) : pkh(lo, hi); }
; template <bool BF, class RowMap>
; __device__ __forceinline__ void cvt_block(const float* W, int K, int N, f16* WT, const RowMap& rm, int item, int tid, LAS unsigned char* S) {
;     ...
;     for (int i = 0; i < 16; ++i) { u32x2 w; w.x = pk16<BF>(v[i][0], v[i][1]); w.y = pk16<BF>(v[i][2], v[i][3]);
;         *(LAS u32x2*)(S + (32 * wave + 2 * i + (lane >> 5)) * CVB_RS + 8 * (lane & 31)) = w; }
;     __syncthreads();
;     const int g = lane >> 4, i16 = lane & 15, q_ = i16 >> 2, p_ = i16 & 3;
;     LAS unsigned char* T = S;
;     u32x4 wv[8];
; #pragma unroll
;     for (int st = 0; st < 8; ++st) {
;         const int ch = 4 * st + g;
;         const LAS unsigned char* ap = S + (8 * ch + q_) * CVB_RS + (16 * wave + 4 * p_) * 2;
;         const s16x4 lo = __builtin_amdgcn_ds_read_tr16_b64_v4i16((LAS s16x4*)ap);
;         const s16x4 hi = __builtin_amdgcn_ds_read_tr16_b64_v4i16((LAS s16x4*)(ap + 4 * CVB_RS));
;         const u32x2 l2 = __builtin_bit_cast(u32x2, lo), h2 = __builtin_bit_cast(u32x2, hi); wv[st].x = l2.x; wv[st].y = l2.y; wv[st].z = h2.x; wv[st].w = h2.y;
;     }
;     __syncthreads();
; #pragma unroll
;     for (int st = 0; st < 8; ++st) *(LAS u32x4*)(T + (16 * wave + i16) * CVT_TS + 16 * (4 * st + g)) = wv[st];
;     LDS_WAIT();
; #pragma unroll
;     for (int j = 0; j < 8; ++j) { const int nr = 16 * wave + 2 * j + (lane >> 5), ch = lane & 31;
;         const u32x4 w = *(const LAS u32x4*)(T + nr * CVT_TS + 16 * ch);
;         *(u32x4*)(WT + (size_t)rm(n0 + nr) * K + k0 + 8 * ch) = w; }
	v_cvt_pk_bf16_f32 v22, v22, v23
	v_cvt_pk_bf16_f32 v23, v24, v25
	s_waitcnt vmcnt(14)
	v_cvt_pk_bf16_f32 v24, v26, v27
	v_cvt_pk_bf16_f32 v25, v28, v29
	ds_write2_b64 v14, v[22:23], v[24:25] offset1:66
	s_waitcnt vmcnt(13)
	v_cvt_pk_bf16_f32 v22, v30, v31
	v_cvt_pk_bf16_f32 v23, v32, v33
	s_waitcnt vmcnt(12)
	v_cvt_pk_bf16_f32 v24, v34, v35
	v_cvt_pk_bf16_f32 v25, v36, v37
	ds_write2_b64 v14, v[22:23], v[24:25] offset0:132 offset1:198
	s_waitcnt vmcnt(11)
	v_cvt_pk_bf16_f32 v22, v38, v39
	v_cvt_pk_bf16_f32 v23, v40, v41
	s_waitcnt vmcnt(10)
	v_cvt_pk_bf16_f32 v24, v42, v43
	v_cvt_pk_bf16_f32 v25, v44, v45
	ds_write2_b64 v18, v[22:23], v[24:25] offset0:8 offset1:74
	s_waitcnt vmcnt(9)
	v_cvt_pk_bf16_f32 v22, v46, v47
	v_cvt_pk_bf16_f32 v23, v48, v49
	s_waitcnt vmcnt(8)
	v_cvt_pk_bf16_f32 v24, v50, v51
	v_cvt_pk_bf16_f32 v25, v52, v53
	ds_write2_b64 v18, v[22:23], v[24:25] offset0:140 offset1:206
	s_waitcnt vmcnt(7)
	v_cvt_pk_bf16_f32 v22, v54, v55
	v_cvt_pk_bf16_f32 v23, v56, v57
	s_waitcnt vmcnt(6)
	v_cvt_pk_bf16_f32 v24, v58, v59
	v_cvt_pk_bf16_f32 v25, v60, v61
	ds_write2_b64 v19, v[22:23], v[24:25] offset0:16 offset1:82
	s_waitcnt vmcnt(5)
	v_cvt_pk_bf16_f32 v22, v62, v63
	v_cvt_pk_bf16_f32 v23, v64, v65
	s_waitcnt vmcnt(4)
	v_cvt_pk_bf16_f32 v24, v66, v67
	v_cvt_pk_bf16_f32 v25, v68, v69
	ds_write2_b64 v19, v[22:23], v[24:25] offset0:148 offset1:214
	s_waitcnt vmcnt(3)
	v_cvt_pk_bf16_f32 v22, v70, v71
	v_cvt_pk_bf16_f32 v23, v72, v73
	s_waitcnt vmcnt(2)
	v_cvt_pk_bf16_f32 v24, v74, v75
	v_cvt_pk_bf16_f32 v25, v76, v77
	ds_write2_b64 v20, v[22:23], v[24:25] offset0:24 offset1:90
	s_waitcnt vmcnt(1)
	v_cvt_pk_bf16_f32 v22, v78, v79
	v_cvt_pk_bf16_f32 v23, v80, v81
	s_waitcnt vmcnt(0)
	v_cvt_pk_bf16_f32 v24, v82, v83
	v_cvt_pk_bf16_f32 v25, v84, v85
	ds_write2_b64 v20, v[22:23], v[24:25] offset0:156 offset1:222
	s_waitcnt lgkmcnt(0)
	s_barrier
	ds_read_b64_tr_b16 v[22:23], v15
	ds_read_b64_tr_b16 v[24:25], v15 offset:1056
	ds_read_b64_tr_b16 v[26:27], v15 offset:8448
	ds_read_b64_tr_b16 v[28:29], v15 offset:9504
	ds_read_b64_tr_b16 v[30:31], v15 offset:16896
	ds_read_b64_tr_b16 v[32:33], v15 offset:17952
	ds_read_b64_tr_b16 v[34:35], v15 offset:25344
	ds_read_b64_tr_b16 v[36:37], v15 offset:26400
	ds_read_b64_tr_b16 v[38:39], v15 offset:33792
	ds_read_b64_tr_b16 v[40:41], v15 offset:34848
	ds_read_b64_tr_b16 v[42:43], v15 offset:42240
	ds_read_b64_tr_b16 v[44:45], v15 offset:43296
	ds_read_b64_tr_b16 v[46:47], v15 offset:50688
	ds_read_b64_tr_b16 v[48:49], v15 offset:51744
	ds_read_b64_tr_b16 v[50:51], v15 offset:59136
	ds_read_b64_tr_b16 v[52:53], v15 offset:60192
	s_waitcnt lgkmcnt(0)
	s_barrier
	ds_write_b128 v16, v[22:25]
	ds_write_b128 v16, v[26:29] offset:64
	ds_write_b128 v16, v[30:33] offset:128
	ds_write_b128 v16, v[34:37] offset:192
	ds_write_b128 v16, v[38:41] offset:256
	ds_write_b128 v16, v[42:45] offset:320
	ds_write_b128 v16, v[46:49] offset:384
	ds_write_b128 v16, v[50:53] offset:448
	s_waitcnt lgkmcnt(0)
	v_lshl_add_u64 v[30:31], s[40:41], 0, v[4:5]
	v_or_b32_e32 v5, s0, v6
	ds_read_b128 v[22:25], v17
	v_lshlrev_b32_e32 v5, 11, v5
	v_or_b32_e32 v26, 0x40000, v5
	v_mov_b32_e32 v27, v3
	v_lshl_add_u64 v[32:33], v[30:31], 0, v[26:27]
	ds_read_b128 v[26:29], v17 offset:1056
	s_waitcnt lgkmcnt(1)
	global_store_dwordx4 v[32:33], v[22:25], off
	s_nop 1
	v_or_b32_e32 v22, 0x41000, v5
	v_mov_b32_e32 v23, v3
	v_lshl_add_u64 v[22:23], v[30:31], 0, v[22:23]
	s_waitcnt lgkmcnt(0)
	global_store_dwordx4 v[22:23], v[26:29], off
	ds_read_b128 v[22:25], v17 offset:2112
	s_nop 0
	v_or_b32_e32 v26, 0x42000, v5
	v_mov_b32_e32 v27, v3
	v_lshl_add_u64 v[32:33], v[30:31], 0, v[26:27]
	ds_read_b128 v[26:29], v17 offset:3168
	s_waitcnt lgkmcnt(1)
	global_store_dwordx4 v[32:33], v[22:25], off
	s_nop 1
	v_or_b32_e32 v22, 0x43000, v5
	v_mov_b32_e32 v23, v3
	v_lshl_add_u64 v[22:23], v[30:31], 0, v[22:23]
	s_waitcnt lgkmcnt(0)
	global_store_dwordx4 v[22:23], v[26:29], off
	ds_read_b128 v[22:25], v17 offset:4224
	s_nop 0
	v_or_b32_e32 v26, 0x44000, v5
	v_mov_b32_e32 v27, v3
	v_lshl_add_u64 v[32:33], v[30:31], 0, v[26:27]
	ds_read_b128 v[26:29], v17 offset:5280
	s_waitcnt lgkmcnt(1)
	global_store_dwordx4 v[32:33], v[22:25], off
	s_nop 1
	v_or_b32_e32 v22, 0x45000, v5
	v_mov_b32_e32 v23, v3
	v_lshl_add_u64 v[22:23], v[30:31], 0, v[22:23]
	s_waitcnt lgkmcnt(0)
	global_store_dwordx4 v[22:23], v[26:29], off
	ds_read_b128 v[22:25], v17 offset:6336
	s_nop 0
	v_or_b32_e32 v26, 0x46000, v5
	v_mov_b32_e32 v27, v3
	v_lshl_add_u64 v[32:33], v[30:31], 0, v[26:27]
	ds_read_b128 v[26:29], v17 offset:7392
	s_waitcnt lgkmcnt(1)
	global_store_dwordx4 v[32:33], v[22:25], off
	s_nop 1
	v_or_b32_e32 v22, 0x47000, v5
	v_mov_b32_e32 v23, v3
	v_lshl_add_u64 v[22:23], v[30:31], 0, v[22:23]
	s_waitcnt lgkmcnt(0)
	global_store_dwordx4 v[22:23], v[26:29], off
	s_barrier

; #define LAS __attribute__((address_space(3)))
; template <bool BF> __device__ __forceinline__ unsigned pk16(float lo, float hi) { return BF ? pkb(lo, hi) : pkh(lo, hi); }
; template <bool BF, class RowMap>
; __device__ __forceinline__ void cvt_block(const float* W, int K, int N, f16* WT, const RowMap& rm, int item, int tid, LAS unsigned char* S) {
;     ...
;     const int nblk = N / 128, kb = item / nblk, nb = item % nblk, k0 = 256 * kb, n0 = 128 * nb;
;     const float* src = W + (size_t)(k0 + 32 * wave + (lane >> 5)) * N + n0 + 4 * (lane & 31);
;     f32x4 v[16];
; #pragma unroll
;     for (int i = 0; i < 16; ++i) v[i] = *(const f32x4*)(src + (size_t)(2 * i) * N);
; #pragma unroll
;     for (int i = 0; i < 16; ++i) { u32x2 w; w.x = pk16<BF>(v[i][0], v[i][1]); w.y = pk16<BF>(v[i][2], v[i][3]);
;         *(LAS u32x2*)(S + (32 * wave + 2 * i + (lane >> 5)) * CVB_RS + 8 * (lane & 31)) = w; }
; __device__ __forceinline__ void cvt_moe(const float* w1, const float* w3, const float* w2, f16* W13, f16* W2T, int tid, LAS unsigned char* S) {
;     ...
;     for (int it = blockIdx.x; it < NIT; it += gridDim.x) {
;         const int e = it / (2 * I13 + I2); int r = it % (2 * I13 + I2);
;         if (r < I13) { cvt_block<MOE_BF16>(w1 + (size_t)e * DM * DE, DM, DE, W13 + (size_t)e * 2 * DE * DM, MapGLU{0}, r, tid, S); continue; } r -= I13;
.LBB0_1215:
	s_andn2_b64 vcc, exec, s[2:3]
	s_cbranch_vccnz .LBB0_1208
	s_mul_hi_i32 s2, s37, 0xb00000
	s_mul_i32 s37, s37, 0xb00000
	v_readlane_b32 s40, v251, 0
	v_readlane_b32 s41, v251, 1
	s_add_u32 s38, s40, s37
	s_addc_u32 s39, s41, s2
	s_add_u32 s0, s84, s37
	s_addc_u32 s37, s85, s2
	s_mul_i32 s2, s36, 0xba3
	s_lshr_b32 s3, s2, 31
	s_lshr_b32 s2, s2, 16
	s_add_i32 s2, s2, s3
	s_sext_i32_i16 s3, s2
	s_mul_i32 s2, s2, 22
	s_sub_i32 s2, s36, s2
	s_sext_i32_i16 s36, s2
	s_lshl_b32 s2, s3, 8
	v_or_b32_e32 v5, s2, v1
	v_mul_i32_i24_e32 v22, 0x2c00, v5
	s_lshl_b32 s40, s36, 7
	v_ashrrev_i32_e32 v23, 31, v22
	v_lshl_add_u64 v[22:23], s[38:39], 0, v[22:23]
	s_ashr_i32 s41, s40, 31
	v_lshl_add_u64 v[22:23], s[40:41], 2, v[22:23]
	v_lshl_add_u64 v[82:83], v[22:23], 0, v[2:3]
	v_add_co_u32_e32 v26, vcc, s21, v82
	s_ashr_i32 s3, s2, 31
	s_nop 0
	v_addc_co_u32_e32 v27, vcc, 0, v83, vcc
	v_add_co_u32_e32 v30, vcc, s22, v82
	global_load_dwordx4 v[22:25], v[82:83], off nt
	s_nop 0
	global_load_dwordx4 v[26:29], v[26:27], off offset:2048 nt
	v_addc_co_u32_e32 v31, vcc, 0, v83, vcc
	v_add_co_u32_e32 v34, vcc, s13, v82
	s_lshl_b64 s[2:3], s[2:3], 1
	s_nop 0
	v_addc_co_u32_e32 v35, vcc, 0, v83, vcc
	v_add_co_u32_e32 v38, vcc, s16, v82
	global_load_dwordx4 v[30:33], v[30:31], off nt
	s_nop 0
	global_load_dwordx4 v[34:37], v[34:35], off offset:2048 nt
	v_addc_co_u32_e32 v39, vcc, 0, v83, vcc
	v_add_co_u32_e32 v42, vcc, s23, v82
	s_add_u32 s2, s0, s2
	s_nop 0
	v_addc_co_u32_e32 v43, vcc, 0, v83, vcc
	v_add_co_u32_e32 v46, vcc, s24, v82
	global_load_dwordx4 v[38:41], v[38:39], off nt
	s_nop 0
	global_load_dwordx4 v[42:45], v[42:43], off offset:2048 nt
	v_addc_co_u32_e32 v47, vcc, 0, v83, vcc
	v_add_co_u32_e32 v50, vcc, s25, v82
	s_addc_u32 s3, s37, s3
	s_nop 0
	v_addc_co_u32_e32 v51, vcc, 0, v83, vcc
	v_add_co_u32_e32 v54, vcc, s26, v82
	global_load_dwordx4 v[46:49], v[46:47], off nt
	s_nop 0
	global_load_dwordx4 v[50:53], v[50:51], off offset:2048 nt
	v_addc_co_u32_e32 v55, vcc, 0, v83, vcc
	v_add_co_u32_e32 v58, vcc, s27, v82
	s_lshl_b32 s0, s36, 8
	s_nop 0
	v_addc_co_u32_e32 v59, vcc, 0, v83, vcc
	v_add_co_u32_e32 v62, vcc, s28, v82
	global_load_dwordx4 v[54:57], v[54:55], off nt
	s_nop 0
	global_load_dwordx4 v[58:61], v[58:59], off offset:2048 nt
	v_addc_co_u32_e32 v63, vcc, 0, v83, vcc
	v_add_co_u32_e32 v66, vcc, s29, v82
	v_mov_b32_e32 v5, v3
	s_nop 0
	v_addc_co_u32_e32 v67, vcc, 0, v83, vcc
	v_add_co_u32_e32 v70, vcc, s30, v82
	global_load_dwordx4 v[62:65], v[62:63], off nt
	s_nop 0
	global_load_dwordx4 v[66:69], v[66:67], off offset:2048 nt
	v_addc_co_u32_e32 v71, vcc, 0, v83, vcc
	v_add_co_u32_e32 v74, vcc, s31, v82
	v_readlane_b32 s42, v251, 2
	s_nop 0
	v_addc_co_u32_e32 v75, vcc, 0, v83, vcc
	v_add_co_u32_e32 v78, vcc, s33, v82
	global_load_dwordx4 v[70:73], v[70:71], off nt
	s_nop 0
	global_load_dwordx4 v[74:77], v[74:75], off offset:2048 nt
	v_addc_co_u32_e32 v79, vcc, 0, v83, vcc
	v_add_co_u32_e32 v82, vcc, s34, v82
	global_load_dwordx4 v[78:81], v[78:79], off nt
	s_nop 0
	v_addc_co_u32_e32 v83, vcc, 0, v83, vcc
	global_load_dwordx4 v[82:85], v[82:83], off offset:2048 nt
	v_readlane_b32 s43, v251, 3
	v_readlane_b32 s44, v251, 4
	v_readlane_b32 s45, v251, 5
	v_readlane_b32 s46, v251, 6
	v_readlane_b32 s47, v251, 7
	s_waitcnt vmcnt(15)
	v_cvt_pk_bf16_f32 v22, v22, v23
	v_cvt_pk_bf16_f32 v23, v24, v25
	s_waitcnt vmcnt(14)
	v_cvt_pk_bf16_f32 v24, v26, v27
	v_cvt_pk_bf16_f32 v25, v28, v29
	ds_write2_b64 v14, v[22:23], v[24:25] offset1:66
	s_waitcnt vmcnt(13)
	v_cvt_pk_bf16_f32 v22, v30, v31
	v_cvt_pk_bf16_f32 v23, v32, v33
	s_waitcnt vmcnt(12)
	v_cvt_pk_bf16_f32 v24, v34, v35
	v_cvt_pk_bf16_f32 v25, v36, v37
	ds_write2_b64 v14, v[22:23], v[24:25] offset0:132 offset1:198
	s_waitcnt vmcnt(11)
	v_cvt_pk_bf16_f32 v22, v38, v39
	v_cvt_pk_bf16_f32 v23, v40, v41
	s_waitcnt vmcnt(10)
	v_cvt_pk_bf16_f32 v24, v42, v43
	v_cvt_pk_bf16_f32 v25, v44, v45
	ds_write2_b64 v18, v[22:23], v[24:25] offset0:8 offset1:74
	s_waitcnt vmcnt(9)
	v_cvt_pk_bf16_f32 v22, v46, v47
	v_cvt_pk_bf16_f32 v23, v48, v49
	s_waitcnt vmcnt(8)
	v_cvt_pk_bf16_f32 v24, v50, v51
	v_cvt_pk_bf16_f32 v25, v52, v53
	ds_write2_b64 v18, v[22:23], v[24:25] offset0:140 offset1:206
	s_waitcnt vmcnt(7)
	v_cvt_pk_bf16_f32 v22, v54, v55
	v_cvt_pk_bf16_f32 v23, v56, v57
	s_waitcnt vmcnt(6)
	v_cvt_pk_bf16_f32 v24, v58, v59
	v_cvt_pk_bf16_f32 v25, v60, v61
	ds_write2_b64 v19, v[22:23], v[24:25] offset0:16 offset1:82
	s_waitcnt vmcnt(5)
	v_cvt_pk_bf16_f32 v22, v62, v63
	v_cvt_pk_bf16_f32 v23, v64, v65
	s_waitcnt vmcnt(4)
	v_cvt_pk_bf16_f32 v24, v66, v67
	v_cvt_pk_bf16_f32 v25, v68, v69
	ds_write2_b64 v19, v[22:23], v[24:25] offset0:148 offset1:214
	s_waitcnt vmcnt(3)
	v_cvt_pk_bf16_f32 v22, v70, v71
	v_cvt_pk_bf16_f32 v23, v72, v73
	s_waitcnt vmcnt(2)
	v_cvt_pk_bf16_f32 v24, v74, v75
	v_cvt_pk_bf16_f32 v25, v76, v77
	ds_write2_b64 v20, v[22:23], v[24:25] offset0:24 offset1:90
	s_waitcnt vmcnt(1)
	v_cvt_pk_bf16_f32 v22, v78, v79
	v_cvt_pk_bf16_f32 v23, v80, v81
	s_waitcnt vmcnt(0)
	v_cvt_pk_bf16_f32 v24, v82, v83
	v_cvt_pk_bf16_f32 v25, v84, v85
	ds_write2_b64 v20, v[22:23], v[24:25] offset0:156 offset1:222
	s_waitcnt lgkmcnt(0)
	s_barrier
; #define LAS __attribute__((address_space(3)))
; #define LDS_WAIT() asm volatile("s_waitcnt lgkmcnt(0)" ::: "memory")
; template <bool BF, class RowMap>
; __device__ __forceinline__ void cvt_block(const float* W, int K, int N, f16* WT, const RowMap& rm, int item, int tid, LAS unsigned char* S) {
;     ...
;     const int g = lane >> 4, i16 = lane & 15, q_ = i16 >> 2, p_ = i16 & 3;
;     LAS unsigned char* T = S;
;     u32x4 wv[8];
; #pragma unroll
;     for (int st = 0; st < 8; ++st) {
;         const int ch = 4 * st + g;
;         const LAS unsigned char* ap = S + (8 * ch + q_) * CVB_RS + (16 * wave + 4 * p_) * 2;
;         const s16x4 lo = __builtin_amdgcn_ds_read_tr16_b64_v4i16((LAS s16x4*)ap);
;         const s16x4 hi = __builtin_amdgcn_ds_read_tr16_b64_v4i16((LAS s16x4*)(ap + 4 * CVB_RS));
;         const u32x2 l2 = __builtin_bit_cast(u32x2, lo), h2 = __builtin_bit_cast(u32x2, hi); wv[st].x = l2.x; wv[st].y = l2.y; wv[st].z = h2.x; wv[st].w = h2.y;
;     }
;     __syncthreads();
; #pragma unroll
;     for (int st = 0; st < 8; ++st) *(LAS u32x4*)(T + (16 * wave + i16) * CVT_TS + 16 * (4 * st + g)) = wv[st];
;     LDS_WAIT();
; #pragma unroll
;     for (int j = 0; j < 8; ++j) { const int nr = 16 * wave + 2 * j + (lane >> 5), ch = lane & 31;
;         const u32x4 w = *(const LAS u32x4*)(T + nr * CVT_TS + 16 * ch);
;         *(u32x4*)(WT + (size_t)rm(n0 + nr) * K + k0 + 8 * ch) = w; }
;     __syncthreads();
	ds_read_b64_tr_b16 v[22:23], v15
	ds_read_b64_tr_b16 v[24:25], v15 offset:1056
	ds_read_b64_tr_b16 v[26:27], v15 offset:8448
	ds_read_b64_tr_b16 v[28:29], v15 offset:9504
	ds_read_b64_tr_b16 v[30:31], v15 offset:16896
	ds_read_b64_tr_b16 v[32:33], v15 offset:17952
	ds_read_b64_tr_b16 v[34:35], v15 offset:25344
	ds_read_b64_tr_b16 v[36:37], v15 offset:26400
	ds_read_b64_tr_b16 v[38:39], v15 offset:33792
	ds_read_b64_tr_b16 v[40:41], v15 offset:34848
	ds_read_b64_tr_b16 v[42:43], v15 offset:42240
	ds_read_b64_tr_b16 v[44:45], v15 offset:43296
	ds_read_b64_tr_b16 v[46:47], v15 offset:50688
	ds_read_b64_tr_b16 v[48:49], v15 offset:51744
	ds_read_b64_tr_b16 v[50:51], v15 offset:59136
	ds_read_b64_tr_b16 v[52:53], v15 offset:60192
	s_waitcnt lgkmcnt(0)
	s_barrier
	ds_write_b128 v16, v[22:25]
	ds_write_b128 v16, v[26:29] offset:64
	ds_write_b128 v16, v[30:33] offset:128
	ds_write_b128 v16, v[34:37] offset:192
	ds_write_b128 v16, v[38:41] offset:256
	ds_write_b128 v16, v[42:45] offset:320
	ds_write_b128 v16, v[46:49] offset:384
	ds_write_b128 v16, v[50:53] offset:448
	s_waitcnt lgkmcnt(0)
	ds_read_b128 v[22:25], v17
	v_or_b32_e32 v26, s0, v6
	v_ashrrev_i32_e32 v27, 31, v26
	v_lshl_add_u64 v[30:31], s[2:3], 0, v[4:5]
	v_lshlrev_b64 v[26:27], 11, v[26:27]
	v_lshl_add_u64 v[32:33], v[30:31], 0, v[26:27]
	ds_read_b128 v[26:29], v17 offset:1056
	s_waitcnt lgkmcnt(1)
	global_store_dwordx4 v[32:33], v[22:25], off
	s_nop 1
	v_or_b32_e32 v22, s0, v7
	v_ashrrev_i32_e32 v23, 31, v22
	v_lshlrev_b64 v[22:23], 11, v[22:23]
	v_lshl_add_u64 v[22:23], v[30:31], 0, v[22:23]
	s_waitcnt lgkmcnt(0)
	global_store_dwordx4 v[22:23], v[26:29], off
	ds_read_b128 v[22:25], v17 offset:2112
	s_nop 0
	v_or_b32_e32 v26, s0, v8
	v_ashrrev_i32_e32 v27, 31, v26
	v_lshlrev_b64 v[26:27], 11, v[26:27]
	v_lshl_add_u64 v[32:33], v[30:31], 0, v[26:27]
	ds_read_b128 v[26:29], v17 offset:3168
	s_waitcnt lgkmcnt(1)
	global_store_dwordx4 v[32:33], v[22:25], off
	s_nop 1
	v_or_b32_e32 v22, s0, v9
	v_ashrrev_i32_e32 v23, 31, v22
	v_lshlrev_b64 v[22:23], 11, v[22:23]
	v_lshl_add_u64 v[22:23], v[30:31], 0, v[22:23]
	s_waitcnt lgkmcnt(0)
	global_store_dwordx4 v[22:23], v[26:29], off
	ds_read_b128 v[22:25], v17 offset:4224
	s_nop 0
	v_or_b32_e32 v26, s0, v10
	v_ashrrev_i32_e32 v27, 31, v26
	v_lshlrev_b64 v[26:27], 11, v[26:27]
	v_lshl_add_u64 v[32:33], v[30:31], 0, v[26:27]
	ds_read_b128 v[26:29], v17 offset:5280
	s_waitcnt lgkmcnt(1)
	global_store_dwordx4 v[32:33], v[22:25], off
	s_nop 1
	v_or_b32_e32 v22, s0, v11
	v_ashrrev_i32_e32 v23, 31, v22
	v_lshlrev_b64 v[22:23], 11, v[22:23]
	v_lshl_add_u64 v[22:23], v[30:31], 0, v[22:23]
	s_waitcnt lgkmcnt(0)
	global_store_dwordx4 v[22:23], v[26:29], off
	ds_read_b128 v[22:25], v17 offset:6336
	s_nop 0
	v_or_b32_e32 v26, s0, v12
	v_ashrrev_i32_e32 v27, 31, v26
	v_lshlrev_b64 v[26:27], 11, v[26:27]
	v_lshl_add_u64 v[32:33], v[30:31], 0, v[26:27]
	ds_read_b128 v[26:29], v17 offset:7392
	s_waitcnt lgkmcnt(1)
	global_store_dwordx4 v[32:33], v[22:25], off
	s_nop 1
	v_or_b32_e32 v22, s0, v13
	v_ashrrev_i32_e32 v23, 31, v22
	v_lshlrev_b64 v[22:23], 11, v[22:23]
	v_lshl_add_u64 v[22:23], v[30:31], 0, v[22:23]
	s_waitcnt lgkmcnt(0)
	global_store_dwordx4 v[22:23], v[26:29], off
	s_barrier
	s_branch .LBB0_1208

; #define GM_STAGE(bufoff, gbase, voff) do { _Pragma("unroll") for (int _i = 0; _i < 2; ++_i) \
;         __builtin_amdgcn_global_load_lds((const unsigned*)((const char*)(gbase) + (voff)[_i]), (LAS unsigned*)(lds + (bufoff) + ldsw + _i * 8192), 16, 0, 0); } while (0)
; #define GM_LDA(dst, b, h) do { _Pragma("unroll") for (int m = 0; m < 4; ++m) _Pragma("unroll") for (int k = 0; k < 2; ++k) dst[m][k] = *(const LAS s16x8*)(lds + GM_SA(b, h) + aoff + m * 2048 + k * 1024); } while (0)
; #define GM_LDB(dst, b, h) do { _Pragma("unroll") for (int n = 0; n < 2; ++n) _Pragma("unroll") for (int k = 0; k < 2; ++k) dst[n][k] = *(const LAS s16x8*)(lds + GM_SB(b, h) + boff + n * 2048 + k * 1024); } while (0)
; #define GM_MMA(ai, bj, At, Bt) do { __builtin_amdgcn_s_setprio(1); _Pragma("unroll") for (int m = 0; m < 4; ++m) _Pragma("unroll") for (int n = 0; n < 2; ++n) _Pragma("unroll") for (int k = 0; k < 2; ++k) \
;         acc[ai][bj][m][n] = mma16<BF>(Bt[n][k], At[m][k], acc[ai][bj][m][n]); __builtin_amdgcn_s_setprio(0); } while (0)
; #define GM_WAIT_V(n) asm volatile("s_waitcnt vmcnt(" #n ")" ::: "memory")
; #define GM_WAIT_L(n) asm volatile("s_waitcnt lgkmcnt(" #n ")" ::: "memory")
; #define GM_BAR __builtin_amdgcn_s_barrier()
; #define GM_SCHED __builtin_amdgcn_sched_barrier(0)
; #define GM_STA_H0(buf, p, o0) do { if constexpr (GATHER) GM_STAGE(buf, p, o0); else GM_STAGE(buf, p, voffA); } while (0)
; #define GM_STA_H1(buf, p, o1) do { if constexpr (GATHER) GM_STAGE(buf, p, o1); else GM_STAGE(buf, (p) + hstepB, voffA); } while (0)
; template <bool BF, bool GATHER = false, class Epi, class Hook>
; __device__ __forceinline__ void gemm_phase(LAS unsigned char* lds, const Gemm g, const Order& S, const Epi& E, Hook& HK) {
;     ...
;             GM_LDB(B0, 0, 0); GM_LDB(B1, 0, 1); GM_SCHED; GM_LDA(At, 0, 0); GM_STA_H1(GM_SA(1, 1), a1, gA1);
;             GM_WAIT_V(8); GM_WAIT_L(0); GM_BAR; GM_MMA(0, 0, At, B0); GM_MMA(0, 1, At, B1); GM_BAR; GM_SCHED;
;             GM_LDA(At, 0, 1); GM_STAGE(GM_SB(0, 0), b2, voffB); GM_STAGE(GM_SB(0, 1), b2 + hstepB, voffB); GM_STA_H0(GM_SA(0, 0), a2, s0);
;             GM_WAIT_V(8); GM_WAIT_L(0); GM_BAR; GM_MMA(1, 0, At, B0); GM_MMA(1, 1, At, B1); GM_BAR; GM_SCHED;
.LBB0_1281:
	s_add_u32 s22, s20, 0xfffc0080
	s_addc_u32 s23, s21, -1
	s_cmp_eq_u32 s47, 12
	s_cselect_b32 s25, s3, s23
	s_cselect_b32 s24, s13, s22
	s_cselect_b32 s23, s15, s46
	s_cselect_b32 s22, s44, s45
	v_lshl_add_u64 v[218:219], s[20:21], 0, v[140:141]
	s_add_i32 m0, s30, 0xc000
	global_load_lds_dwordx4 v[218:219], off
	v_lshl_add_u64 v[218:219], s[20:21], 0, v[142:143]
	s_add_i32 m0, s30, 0xe000
	s_nop 0
	global_load_lds_dwordx4 v[218:219], off
	ds_read_b128 v[154:157], v151
	ds_read_b128 v[158:161], v151 offset:1024
	ds_read_b128 v[162:165], v151 offset:2048
	ds_read_b128 v[166:169], v151 offset:3072
	ds_read_b128 v[170:173], v152
	ds_read_b128 v[174:177], v152 offset:1024
	ds_read_b128 v[178:181], v152 offset:2048
	ds_read_b128 v[182:185], v152 offset:3072
	ds_read_b128 v[186:189], v153
	ds_read_b128 v[190:193], v153 offset:1024
	ds_read_b128 v[194:197], v153 offset:2048
	ds_read_b128 v[198:201], v153 offset:3072
	ds_read_b128 v[202:205], v153 offset:4096
	ds_read_b128 v[206:209], v153 offset:5120
	ds_read_b128 v[210:213], v153 offset:6144
	ds_read_b128 v[214:217], v153 offset:7168
	s_waitcnt vmcnt(8)
	s_waitcnt lgkmcnt(0)
	s_barrier
	s_waitcnt lgkmcnt(0)
	v_mfma_f32_16x16x32_f16 v[126:129], v[154:157], v[186:189], v[126:129]
	v_mfma_f32_16x16x32_f16 v[118:121], v[162:165], v[186:189], v[118:121]
	v_mfma_f32_16x16x32_f16 v[110:113], v[154:157], v[194:197], v[110:113]
	v_mfma_f32_16x16x32_f16 v[102:105], v[162:165], v[194:197], v[102:105]
	v_mfma_f32_16x16x32_f16 v[94:97], v[154:157], v[202:205], v[94:97]
	v_mfma_f32_16x16x32_f16 v[86:89], v[162:165], v[202:205], v[86:89]
	v_mfma_f32_16x16x32_f16 v[78:81], v[154:157], v[210:213], v[78:81]
	v_mfma_f32_16x16x32_f16 v[70:73], v[162:165], v[210:213], v[70:73]
	v_mfma_f32_16x16x32_f16 v[126:129], v[158:161], v[190:193], v[126:129]
	v_mfma_f32_16x16x32_f16 v[118:121], v[166:169], v[190:193], v[118:121]
	v_mfma_f32_16x16x32_f16 v[110:113], v[158:161], v[198:201], v[110:113]
	v_mfma_f32_16x16x32_f16 v[102:105], v[166:169], v[198:201], v[102:105]
	v_mfma_f32_16x16x32_f16 v[94:97], v[158:161], v[206:209], v[94:97]
	v_mfma_f32_16x16x32_f16 v[86:89], v[166:169], v[206:209], v[86:89]
	v_mfma_f32_16x16x32_f16 v[78:81], v[158:161], v[214:217], v[78:81]
	v_mfma_f32_16x16x32_f16 v[70:73], v[166:169], v[214:217], v[70:73]
	v_mfma_f32_16x16x32_f16 v[122:125], v[170:173], v[186:189], v[122:125]
	v_mfma_f32_16x16x32_f16 v[114:117], v[178:181], v[186:189], v[114:117]
	v_mfma_f32_16x16x32_f16 v[106:109], v[170:173], v[194:197], v[106:109]
	v_mfma_f32_16x16x32_f16 v[98:101], v[178:181], v[194:197], v[98:101]
	v_mfma_f32_16x16x32_f16 v[90:93], v[170:173], v[202:205], v[90:93]
	v_mfma_f32_16x16x32_f16 v[82:85], v[178:181], v[202:205], v[82:85]
	v_mfma_f32_16x16x32_f16 v[74:77], v[170:173], v[210:213], v[74:77]
	v_mfma_f32_16x16x32_f16 v[66:69], v[178:181], v[210:213], v[66:69]
	v_mfma_f32_16x16x32_f16 v[122:125], v[174:177], v[190:193], v[122:125]
	v_mfma_f32_16x16x32_f16 v[114:117], v[182:185], v[190:193], v[114:117]
	v_mfma_f32_16x16x32_f16 v[106:109], v[174:177], v[198:201], v[106:109]
	v_mfma_f32_16x16x32_f16 v[98:101], v[182:185], v[198:201], v[98:101]
	v_mfma_f32_16x16x32_f16 v[90:93], v[174:177], v[206:209], v[90:93]
	v_mfma_f32_16x16x32_f16 v[82:85], v[182:185], v[206:209], v[82:85]
	v_mfma_f32_16x16x32_f16 v[74:77], v[174:177], v[214:217], v[74:77]
	v_mfma_f32_16x16x32_f16 v[66:69], v[182:185], v[214:217], v[66:69]
	s_barrier
	s_add_i32 s48, s40, s28
	v_lshl_add_u64 v[218:219], s[22:23], 0, v[134:135]
	s_mov_b32 m0, s48
	global_load_lds_dwordx4 v[218:219], off
	s_add_i32 m0, s48, 0x2000
	s_add_u32 s48, s22, 0x40000
	v_lshl_add_u64 v[220:221], s[22:23], 0, v[130:131]
	s_addc_u32 s49, s23, 0
	s_add_i32 s50, s41, s28
	global_load_lds_dwordx4 v[220:221], off
	v_lshl_add_u64 v[222:223], s[48:49], 0, v[134:135]
	s_mov_b32 m0, s50
	v_lshl_add_u64 v[224:225], s[24:25], 0, v[132:133]
	global_load_lds_dwordx4 v[222:223], off
	v_lshl_add_u64 v[222:223], s[48:49], 0, v[130:131]
	s_add_i32 m0, s50, 0x2000
	s_nop 0
	global_load_lds_dwordx4 v[222:223], off
	v_lshl_add_u64 v[222:223], s[24:25], 0, v[136:137]
	s_mov_b32 m0, s30
	s_nop 0
	global_load_lds_dwordx4 v[222:223], off
	s_mov_b32 m0, s31
	s_nop 0
	global_load_lds_dwordx4 v[224:225], off
	ds_read_b128 v[186:189], v153 offset:16384
	ds_read_b128 v[190:193], v153 offset:17408
	ds_read_b128 v[194:197], v153 offset:18432
	ds_read_b128 v[198:201], v153 offset:19456
	ds_read_b128 v[202:205], v153 offset:20480
	ds_read_b128 v[206:209], v153 offset:21504
	ds_read_b128 v[210:213], v153 offset:22528
	ds_read_b128 v[214:217], v153 offset:23552
	s_waitcnt vmcnt(8)
	s_waitcnt lgkmcnt(0)
	s_barrier
; #define GM_LDA(dst, b, h) do { _Pragma("unroll") for (int m = 0; m < 4; ++m) _Pragma("unroll") for (int k = 0; k < 2; ++k) dst[m][k] = *(const LAS s16x8*)(lds + GM_SA(b, h) + aoff + m * 2048 + k * 1024); } while (0)
; #define GM_LDB(dst, b, h) do { _Pragma("unroll") for (int n = 0; n < 2; ++n) _Pragma("unroll") for (int k = 0; k < 2; ++k) dst[n][k] = *(const LAS s16x8*)(lds + GM_SB(b, h) + boff + n * 2048 + k * 1024); } while (0)
; #define GM_MMA(ai, bj, At, Bt) do { __builtin_amdgcn_s_setprio(1); _Pragma("unroll") for (int m = 0; m < 4; ++m) _Pragma("unroll") for (int n = 0; n < 2; ++n) _Pragma("unroll") for (int k = 0; k < 2; ++k) \
;         acc[ai][bj][m][n] = mma16<BF>(Bt[n][k], At[m][k], acc[ai][bj][m][n]); __builtin_amdgcn_s_setprio(0); } while (0)
; #define GM_WAIT_V(n) asm volatile("s_waitcnt vmcnt(" #n ")" ::: "memory")
; #define GM_WAIT_L(n) asm volatile("s_waitcnt lgkmcnt(" #n ")" ::: "memory")
; #define GM_BAR __builtin_amdgcn_s_barrier()
; #define GM_SCHED __builtin_amdgcn_sched_barrier(0)
; #define GM_STA_H1(buf, p, o1) do { if constexpr (GATHER) GM_STAGE(buf, p, o1); else GM_STAGE(buf, (p) + hstepB, voffA); } while (0)
; template <bool BF, bool GATHER = false, class Epi, class Hook>
; __device__ __forceinline__ void gemm_phase(LAS unsigned char* lds, const Gemm g, const Order& S, const Epi& E, Hook& HK) {
;     ...
;             GM_WAIT_V(8); GM_WAIT_L(0); GM_BAR; GM_MMA(1, 0, At, B0); GM_MMA(1, 1, At, B1); GM_BAR; GM_SCHED;
;             GM_LDB(B0, 1, 0); GM_LDB(B1, 1, 1); GM_SCHED; GM_LDA(At, 1, 0); GM_STA_H1(GM_SA(0, 1), a2, s1);
;             GM_WAIT_V(8); GM_WAIT_L(0); GM_BAR; GM_MMA(0, 0, At, B0); GM_MMA(0, 1, At, B1); GM_BAR; GM_SCHED;
	s_waitcnt lgkmcnt(0)
	v_mfma_f32_16x16x32_f16 v[62:65], v[154:157], v[186:189], v[62:65]
	v_mfma_f32_16x16x32_f16 v[54:57], v[162:165], v[186:189], v[54:57]
	v_mfma_f32_16x16x32_f16 v[46:49], v[154:157], v[194:197], v[46:49]
	v_mfma_f32_16x16x32_f16 v[38:41], v[162:165], v[194:197], v[38:41]
	v_mfma_f32_16x16x32_f16 v[30:33], v[154:157], v[202:205], v[30:33]
	v_mfma_f32_16x16x32_f16 v[22:25], v[162:165], v[202:205], v[22:25]
	v_mfma_f32_16x16x32_f16 v[14:17], v[154:157], v[210:213], v[14:17]
	v_mfma_f32_16x16x32_f16 v[6:9], v[162:165], v[210:213], v[6:9]
	v_mfma_f32_16x16x32_f16 v[62:65], v[158:161], v[190:193], v[62:65]
	v_mfma_f32_16x16x32_f16 v[54:57], v[166:169], v[190:193], v[54:57]
	v_mfma_f32_16x16x32_f16 v[46:49], v[158:161], v[198:201], v[46:49]
	v_mfma_f32_16x16x32_f16 v[38:41], v[166:169], v[198:201], v[38:41]
	v_mfma_f32_16x16x32_f16 v[30:33], v[158:161], v[206:209], v[30:33]
	v_mfma_f32_16x16x32_f16 v[22:25], v[166:169], v[206:209], v[22:25]
	v_mfma_f32_16x16x32_f16 v[14:17], v[158:161], v[214:217], v[14:17]
	v_mfma_f32_16x16x32_f16 v[6:9], v[166:169], v[214:217], v[6:9]
	v_mfma_f32_16x16x32_f16 v[58:61], v[170:173], v[186:189], v[58:61]
	v_mfma_f32_16x16x32_f16 v[50:53], v[178:181], v[186:189], v[50:53]
	v_mfma_f32_16x16x32_f16 v[42:45], v[170:173], v[194:197], v[42:45]
	v_mfma_f32_16x16x32_f16 v[34:37], v[178:181], v[194:197], v[34:37]
	v_mfma_f32_16x16x32_f16 v[26:29], v[170:173], v[202:205], v[26:29]
	v_mfma_f32_16x16x32_f16 v[18:21], v[178:181], v[202:205], v[18:21]
	v_mfma_f32_16x16x32_f16 v[10:13], v[170:173], v[210:213], v[10:13]
	v_mfma_f32_16x16x32_f16 v[2:5], v[178:181], v[210:213], v[2:5]
	v_mfma_f32_16x16x32_f16 v[58:61], v[174:177], v[190:193], v[58:61]
	v_mfma_f32_16x16x32_f16 v[50:53], v[182:185], v[190:193], v[50:53]
	v_mfma_f32_16x16x32_f16 v[42:45], v[174:177], v[198:201], v[42:45]
	v_mfma_f32_16x16x32_f16 v[34:37], v[182:185], v[198:201], v[34:37]
	v_mfma_f32_16x16x32_f16 v[26:29], v[174:177], v[206:209], v[26:29]
	v_mfma_f32_16x16x32_f16 v[18:21], v[182:185], v[206:209], v[18:21]
	v_mfma_f32_16x16x32_f16 v[10:13], v[174:177], v[214:217], v[10:13]
	v_mfma_f32_16x16x32_f16 v[2:5], v[182:185], v[214:217], v[2:5]
	s_barrier
	s_add_u32 s24, s24, 0x40000
	s_addc_u32 s25, s25, 0
	s_mov_b32 m0, s33
	v_lshl_add_u64 v[226:227], s[24:25], 0, v[136:137]
	global_load_lds_dwordx4 v[226:227], off
	v_lshl_add_u64 v[226:227], s[24:25], 0, v[132:133]
	s_mov_b32 m0, s34
	s_nop 0
	global_load_lds_dwordx4 v[226:227], off
	s_mov_b32 s49, 0x1c000
	s_mov_b32 s48, 0x18000
	v_add_u32_e32 v244, s48, v148
	ds_read_b128 v[154:157], v244
	ds_read_b128 v[158:161], v244 offset:1024
	ds_read_b128 v[162:165], v244 offset:2048
	ds_read_b128 v[166:169], v244 offset:3072
	v_add_u32_e32 v244, s49, v148
	ds_read_b128 v[170:173], v244
	ds_read_b128 v[174:177], v244 offset:1024
	ds_read_b128 v[178:181], v244 offset:2048
	ds_read_b128 v[182:185], v244 offset:3072
	ds_read_b128 v[186:189], v153 offset:32768
	ds_read_b128 v[190:193], v153 offset:33792
	ds_read_b128 v[194:197], v153 offset:34816
	ds_read_b128 v[198:201], v153 offset:35840
	ds_read_b128 v[202:205], v153 offset:36864
	ds_read_b128 v[206:209], v153 offset:37888
	ds_read_b128 v[210:213], v153 offset:38912
	ds_read_b128 v[214:217], v153 offset:39936
	s_waitcnt vmcnt(8)
	s_waitcnt lgkmcnt(0)
	s_barrier
	s_waitcnt lgkmcnt(0)
	v_mfma_f32_16x16x32_f16 v[126:129], v[154:157], v[186:189], v[126:129]
	v_mfma_f32_16x16x32_f16 v[118:121], v[162:165], v[186:189], v[118:121]
	v_mfma_f32_16x16x32_f16 v[110:113], v[154:157], v[194:197], v[110:113]
	v_mfma_f32_16x16x32_f16 v[102:105], v[162:165], v[194:197], v[102:105]
	v_mfma_f32_16x16x32_f16 v[94:97], v[154:157], v[202:205], v[94:97]
	v_mfma_f32_16x16x32_f16 v[86:89], v[162:165], v[202:205], v[86:89]
	v_mfma_f32_16x16x32_f16 v[78:81], v[154:157], v[210:213], v[78:81]
	v_mfma_f32_16x16x32_f16 v[70:73], v[162:165], v[210:213], v[70:73]
	v_mfma_f32_16x16x32_f16 v[126:129], v[158:161], v[190:193], v[126:129]
	v_mfma_f32_16x16x32_f16 v[118:121], v[166:169], v[190:193], v[118:121]
	v_mfma_f32_16x16x32_f16 v[110:113], v[158:161], v[198:201], v[110:113]
	v_mfma_f32_16x16x32_f16 v[102:105], v[166:169], v[198:201], v[102:105]
	v_mfma_f32_16x16x32_f16 v[94:97], v[158:161], v[206:209], v[94:97]
	v_mfma_f32_16x16x32_f16 v[86:89], v[166:169], v[206:209], v[86:89]
	v_mfma_f32_16x16x32_f16 v[78:81], v[158:161], v[214:217], v[78:81]
	v_mfma_f32_16x16x32_f16 v[70:73], v[166:169], v[214:217], v[70:73]
	v_mfma_f32_16x16x32_f16 v[122:125], v[170:173], v[186:189], v[122:125]
	v_mfma_f32_16x16x32_f16 v[114:117], v[178:181], v[186:189], v[114:117]
	v_mfma_f32_16x16x32_f16 v[106:109], v[170:173], v[194:197], v[106:109]
	v_mfma_f32_16x16x32_f16 v[98:101], v[178:181], v[194:197], v[98:101]
	v_mfma_f32_16x16x32_f16 v[90:93], v[170:173], v[202:205], v[90:93]
	v_mfma_f32_16x16x32_f16 v[82:85], v[178:181], v[202:205], v[82:85]
	v_mfma_f32_16x16x32_f16 v[74:77], v[170:173], v[210:213], v[74:77]
	v_mfma_f32_16x16x32_f16 v[66:69], v[178:181], v[210:213], v[66:69]
	v_mfma_f32_16x16x32_f16 v[122:125], v[174:177], v[190:193], v[122:125]
	v_mfma_f32_16x16x32_f16 v[114:117], v[182:185], v[190:193], v[114:117]
	v_mfma_f32_16x16x32_f16 v[106:109], v[174:177], v[198:201], v[106:109]
	v_mfma_f32_16x16x32_f16 v[98:101], v[182:185], v[198:201], v[98:101]
	v_mfma_f32_16x16x32_f16 v[90:93], v[174:177], v[206:209], v[90:93]
	v_mfma_f32_16x16x32_f16 v[82:85], v[182:185], v[206:209], v[82:85]
	v_mfma_f32_16x16x32_f16 v[74:77], v[174:177], v[214:217], v[74:77]
	v_mfma_f32_16x16x32_f16 v[66:69], v[182:185], v[214:217], v[66:69]
	s_barrier
; #define GM_STAGE(bufoff, gbase, voff) do { _Pragma("unroll") for (int _i = 0; _i < 2; ++_i) \
;         __builtin_amdgcn_global_load_lds((const unsigned*)((const char*)(gbase) + (voff)[_i]), (LAS unsigned*)(lds + (bufoff) + ldsw + _i * 8192), 16, 0, 0); } while (0)
; #define GM_LDA(dst, b, h) do { _Pragma("unroll") for (int m = 0; m < 4; ++m) _Pragma("unroll") for (int k = 0; k < 2; ++k) dst[m][k] = *(const LAS s16x8*)(lds + GM_SA(b, h) + aoff + m * 2048 + k * 1024); } while (0)
; #define GM_MMA(ai, bj, At, Bt) do { __builtin_amdgcn_s_setprio(1); _Pragma("unroll") for (int m = 0; m < 4; ++m) _Pragma("unroll") for (int n = 0; n < 2; ++n) _Pragma("unroll") for (int k = 0; k < 2; ++k) \
;         acc[ai][bj][m][n] = mma16<BF>(Bt[n][k], At[m][k], acc[ai][bj][m][n]); __builtin_amdgcn_s_setprio(0); } while (0)
; #define GM_WAIT_V(n) asm volatile("s_waitcnt vmcnt(" #n ")" ::: "memory")
; #define GM_WAIT_L(n) asm volatile("s_waitcnt lgkmcnt(" #n ")" ::: "memory")
; #define GM_BAR __builtin_amdgcn_s_barrier()
; #define GM_SCHED __builtin_amdgcn_sched_barrier(0)
; #define GM_STA_H0(buf, p, o0) do { if constexpr (GATHER) GM_STAGE(buf, p, o0); else GM_STAGE(buf, p, voffA); } while (0)
; template <bool BF, bool GATHER = false, class Epi, class Hook>
; __device__ __forceinline__ void gemm_phase(LAS unsigned char* lds, const Gemm g, const Order& S, const Epi& E, Hook& HK) {
;     ...
;         for (int t = 0; t < nt; t += 2) {
;     ...
;             GM_LDA(At, 1, 1); GM_STAGE(GM_SB(1, 0), b3, voffB); GM_STAGE(GM_SB(1, 1), b3 + hstepB, voffB); GM_STA_H0(GM_SA(1, 0), a3, s0);
;             GM_WAIT_V(8); GM_WAIT_L(0); GM_BAR; GM_MMA(1, 0, At, B0); GM_MMA(1, 1, At, B1); GM_BAR; GM_SCHED;
;     ...
;         if (wr == 0) GM_BAR;
	s_add_i32 s24, s48, s28
	v_lshl_add_u64 v[218:219], v[218:219], 0, s[8:9]
	s_mov_b32 m0, s24
	global_load_lds_dwordx4 v[218:219], off
	s_add_i32 m0, s24, 0x2000
	s_add_u32 s22, s22, 0x40080
	v_lshl_add_u64 v[218:219], v[220:221], 0, s[8:9]
	s_addc_u32 s23, s23, 0
	s_add_i32 s24, s49, s28
	global_load_lds_dwordx4 v[218:219], off
	v_lshl_add_u64 v[218:219], s[22:23], 0, v[134:135]
	s_mov_b32 m0, s24
	s_nop 0
	global_load_lds_dwordx4 v[218:219], off
	v_lshl_add_u64 v[218:219], s[22:23], 0, v[130:131]
	s_add_i32 m0, s24, 0x2000
	s_nop 0
	global_load_lds_dwordx4 v[218:219], off
	v_lshl_add_u64 v[218:219], v[222:223], 0, s[8:9]
	s_mov_b32 m0, s37
	s_nop 0
	global_load_lds_dwordx4 v[218:219], off
	v_lshl_add_u64 v[218:219], v[224:225], 0, s[8:9]
	s_mov_b32 m0, s38
	s_nop 0
	global_load_lds_dwordx4 v[218:219], off
	ds_read_b128 v[186:189], v153 offset:49152
	ds_read_b128 v[190:193], v153 offset:50176
	ds_read_b128 v[194:197], v153 offset:51200
	ds_read_b128 v[198:201], v153 offset:52224
	ds_read_b128 v[202:205], v153 offset:53248
	ds_read_b128 v[206:209], v153 offset:54272
	ds_read_b128 v[210:213], v153 offset:55296
	ds_read_b128 v[214:217], v153 offset:56320
	s_waitcnt vmcnt(8)
	s_waitcnt lgkmcnt(0)
	s_barrier
	s_waitcnt lgkmcnt(0)
	v_mfma_f32_16x16x32_f16 v[62:65], v[154:157], v[186:189], v[62:65]
	v_mfma_f32_16x16x32_f16 v[54:57], v[162:165], v[186:189], v[54:57]
	v_mfma_f32_16x16x32_f16 v[46:49], v[154:157], v[194:197], v[46:49]
	v_mfma_f32_16x16x32_f16 v[38:41], v[162:165], v[194:197], v[38:41]
	v_mfma_f32_16x16x32_f16 v[30:33], v[154:157], v[202:205], v[30:33]
	v_mfma_f32_16x16x32_f16 v[22:25], v[162:165], v[202:205], v[22:25]
	v_mfma_f32_16x16x32_f16 v[14:17], v[154:157], v[210:213], v[14:17]
	v_mfma_f32_16x16x32_f16 v[6:9], v[162:165], v[210:213], v[6:9]
	v_mfma_f32_16x16x32_f16 v[62:65], v[158:161], v[190:193], v[62:65]
	v_mfma_f32_16x16x32_f16 v[54:57], v[166:169], v[190:193], v[54:57]
	v_mfma_f32_16x16x32_f16 v[46:49], v[158:161], v[198:201], v[46:49]
	v_mfma_f32_16x16x32_f16 v[38:41], v[166:169], v[198:201], v[38:41]
	v_mfma_f32_16x16x32_f16 v[30:33], v[158:161], v[206:209], v[30:33]
	v_mfma_f32_16x16x32_f16 v[22:25], v[166:169], v[206:209], v[22:25]
	v_mfma_f32_16x16x32_f16 v[14:17], v[158:161], v[214:217], v[14:17]
	v_mfma_f32_16x16x32_f16 v[6:9], v[166:169], v[214:217], v[6:9]
	v_mfma_f32_16x16x32_f16 v[58:61], v[170:173], v[186:189], v[58:61]
	v_mfma_f32_16x16x32_f16 v[50:53], v[178:181], v[186:189], v[50:53]
	v_mfma_f32_16x16x32_f16 v[42:45], v[170:173], v[194:197], v[42:45]
	v_mfma_f32_16x16x32_f16 v[34:37], v[178:181], v[194:197], v[34:37]
	v_mfma_f32_16x16x32_f16 v[26:29], v[170:173], v[202:205], v[26:29]
	v_mfma_f32_16x16x32_f16 v[18:21], v[178:181], v[202:205], v[18:21]
	v_mfma_f32_16x16x32_f16 v[10:13], v[170:173], v[210:213], v[10:13]
	v_mfma_f32_16x16x32_f16 v[2:5], v[178:181], v[210:213], v[2:5]
	v_mfma_f32_16x16x32_f16 v[58:61], v[174:177], v[190:193], v[58:61]
	v_mfma_f32_16x16x32_f16 v[50:53], v[182:185], v[190:193], v[50:53]
	v_mfma_f32_16x16x32_f16 v[42:45], v[174:177], v[198:201], v[42:45]
	v_mfma_f32_16x16x32_f16 v[34:37], v[182:185], v[198:201], v[34:37]
	v_mfma_f32_16x16x32_f16 v[26:29], v[174:177], v[206:209], v[26:29]
	v_mfma_f32_16x16x32_f16 v[18:21], v[182:185], v[206:209], v[18:21]
	v_mfma_f32_16x16x32_f16 v[10:13], v[174:177], v[214:217], v[10:13]
	v_mfma_f32_16x16x32_f16 v[2:5], v[182:185], v[214:217], v[2:5]
	s_barrier
	s_add_i32 s47, s47, 2
	s_add_u32 s20, s20, 0x100
	s_addc_u32 s21, s21, 0
	s_add_u32 s45, s45, 0x100
	s_addc_u32 s46, s46, 0
	s_cmp_gt_u32 s47, 13
	s_cbranch_scc0 .LBB0_1281
	s_and_b64 vcc, exec, s[10:11]
	s_cbranch_vccnz .LBB0_1286
	v_lshl_add_u32 v154, s2, 8, v1
	s_cmp_gt_i32 s43, 7
	s_mov_b64 s[2:3], -1
	s_cbranch_scc1 .LBB0_1287

; #define GM_STAGE(bufoff, gbase, voff) do { _Pragma("unroll") for (int _i = 0; _i < 2; ++_i) \
;         __builtin_amdgcn_global_load_lds((const unsigned*)((const char*)(gbase) + (voff)[_i]), (LAS unsigned*)(lds + (bufoff) + ldsw + _i * 8192), 16, 0, 0); } while (0)
; #define GM_LDA(dst, b, h) do { _Pragma("unroll") for (int m = 0; m < 4; ++m) _Pragma("unroll") for (int k = 0; k < 2; ++k) dst[m][k] = *(const LAS s16x8*)(lds + GM_SA(b, h) + aoff + m * 2048 + k * 1024); } while (0)
; #define GM_LDB(dst, b, h) do { _Pragma("unroll") for (int n = 0; n < 2; ++n) _Pragma("unroll") for (int k = 0; k < 2; ++k) dst[n][k] = *(const LAS s16x8*)(lds + GM_SB(b, h) + boff + n * 2048 + k * 1024); } while (0)
; #define GM_MMA(ai, bj, At, Bt) do { __builtin_amdgcn_s_setprio(1); _Pragma("unroll") for (int m = 0; m < 4; ++m) _Pragma("unroll") for (int n = 0; n < 2; ++n) _Pragma("unroll") for (int k = 0; k < 2; ++k) \
;         acc[ai][bj][m][n] = mma16<BF>(Bt[n][k], At[m][k], acc[ai][bj][m][n]); __builtin_amdgcn_s_setprio(0); } while (0)
; #define GM_WAIT_V(n) asm volatile("s_waitcnt vmcnt(" #n ")" ::: "memory")
; #define GM_WAIT_L(n) asm volatile("s_waitcnt lgkmcnt(" #n ")" ::: "memory")
; #define GM_BAR __builtin_amdgcn_s_barrier()
; #define GM_SCHED __builtin_amdgcn_sched_barrier(0)
; #define GM_STA_H0(buf, p, o0) do { if constexpr (GATHER) GM_STAGE(buf, p, o0); else GM_STAGE(buf, p, voffA); } while (0)
; #define GM_STA_H1(buf, p, o1) do { if constexpr (GATHER) GM_STAGE(buf, p, o1); else GM_STAGE(buf, (p) + hstepB, voffA); } while (0)
; template <bool BF, bool GATHER = false, class Epi, class Hook>
; __device__ __forceinline__ void gemm_phase(LAS unsigned char* lds, const Gemm g, const Order& S, const Epi& E, Hook& HK) {
;     ...
;             GM_LDB(B0, 0, 0); GM_LDB(B1, 0, 1); GM_SCHED; GM_LDA(At, 0, 0); GM_STA_H1(GM_SA(1, 1), a1, gA1);
;             GM_WAIT_V(8); GM_WAIT_L(0); GM_BAR; GM_MMA(0, 0, At, B0); GM_MMA(0, 1, At, B1); GM_BAR; GM_SCHED;
;             GM_LDA(At, 0, 1); GM_STAGE(GM_SB(0, 0), b2, voffB); GM_STAGE(GM_SB(0, 1), b2 + hstepB, voffB); GM_STA_H0(GM_SA(0, 0), a2, s0);
;             GM_WAIT_V(8); GM_WAIT_L(0); GM_BAR; GM_MMA(1, 0, At, B0); GM_MMA(1, 1, At, B1); GM_BAR; GM_SCHED;
.LBB0_1480:
	s_add_u32 s24, s22, 0xfffc0080
	s_addc_u32 s25, s23, -1
	s_cmp_eq_u32 s49, 12
	s_cselect_b32 s27, s15, s25
	s_cselect_b32 s26, s45, s24
	s_cselect_b32 s25, s17, s48
	s_cselect_b32 s24, s46, s47
	v_lshl_add_u64 v[216:217], s[22:23], 0, v[154:155]
	s_add_i32 m0, s33, 0xc000
	global_load_lds_dwordx4 v[216:217], off
	v_lshl_add_u64 v[216:217], s[22:23], 0, v[156:157]
	s_add_i32 m0, s33, 0xe000
	s_nop 0
	global_load_lds_dwordx4 v[216:217], off
	ds_read_b128 v[122:125], v168
	ds_read_b128 v[126:129], v168 offset:1024
	ds_read_b128 v[130:133], v168 offset:2048
	ds_read_b128 v[134:137], v168 offset:3072
	ds_read_b128 v[162:165], v169
	ds_read_b128 v[172:175], v169 offset:1024
	ds_read_b128 v[176:179], v169 offset:2048
	ds_read_b128 v[180:183], v169 offset:3072
	ds_read_b128 v[184:187], v170
	ds_read_b128 v[188:191], v170 offset:1024
	ds_read_b128 v[192:195], v170 offset:2048
	ds_read_b128 v[196:199], v170 offset:3072
	ds_read_b128 v[200:203], v170 offset:4096
	ds_read_b128 v[204:207], v170 offset:5120
	ds_read_b128 v[208:211], v170 offset:6144
	ds_read_b128 v[212:215], v170 offset:7168
	s_waitcnt vmcnt(8)
	s_waitcnt lgkmcnt(0)
	s_barrier
	s_waitcnt lgkmcnt(0)
	v_mfma_f32_16x16x32_f16 v[142:145], v[122:125], v[184:187], v[142:145]
	v_mfma_f32_16x16x32_f16 v[138:141], v[130:133], v[184:187], v[138:141]
	v_mfma_f32_16x16x32_f16 v[110:113], v[122:125], v[192:195], v[110:113]
	v_mfma_f32_16x16x32_f16 v[106:109], v[130:133], v[192:195], v[106:109]
	v_mfma_f32_16x16x32_f16 v[94:97], v[122:125], v[200:203], v[94:97]
	v_mfma_f32_16x16x32_f16 v[90:93], v[130:133], v[200:203], v[90:93]
	v_mfma_f32_16x16x32_f16 v[78:81], v[122:125], v[208:211], v[78:81]
	v_mfma_f32_16x16x32_f16 v[74:77], v[130:133], v[208:211], v[74:77]
	v_mfma_f32_16x16x32_f16 v[142:145], v[126:129], v[188:191], v[142:145]
	v_mfma_f32_16x16x32_f16 v[138:141], v[134:137], v[188:191], v[138:141]
	v_mfma_f32_16x16x32_f16 v[110:113], v[126:129], v[196:199], v[110:113]
	v_mfma_f32_16x16x32_f16 v[106:109], v[134:137], v[196:199], v[106:109]
	v_mfma_f32_16x16x32_f16 v[94:97], v[126:129], v[204:207], v[94:97]
	v_mfma_f32_16x16x32_f16 v[90:93], v[134:137], v[204:207], v[90:93]
	v_mfma_f32_16x16x32_f16 v[78:81], v[126:129], v[212:215], v[78:81]
	v_mfma_f32_16x16x32_f16 v[74:77], v[134:137], v[212:215], v[74:77]
	v_mfma_f32_16x16x32_f16 v[118:121], v[162:165], v[184:187], v[118:121]
	v_mfma_f32_16x16x32_f16 v[114:117], v[176:179], v[184:187], v[114:117]
	v_mfma_f32_16x16x32_f16 v[102:105], v[162:165], v[192:195], v[102:105]
	v_mfma_f32_16x16x32_f16 v[98:101], v[176:179], v[192:195], v[98:101]
	v_mfma_f32_16x16x32_f16 v[86:89], v[162:165], v[200:203], v[86:89]
	v_mfma_f32_16x16x32_f16 v[82:85], v[176:179], v[200:203], v[82:85]
	v_mfma_f32_16x16x32_f16 v[70:73], v[162:165], v[208:211], v[70:73]
	v_mfma_f32_16x16x32_f16 v[66:69], v[176:179], v[208:211], v[66:69]
	v_mfma_f32_16x16x32_f16 v[118:121], v[172:175], v[188:191], v[118:121]
	v_mfma_f32_16x16x32_f16 v[114:117], v[180:183], v[188:191], v[114:117]
	v_mfma_f32_16x16x32_f16 v[102:105], v[172:175], v[196:199], v[102:105]
	v_mfma_f32_16x16x32_f16 v[98:101], v[180:183], v[196:199], v[98:101]
	v_mfma_f32_16x16x32_f16 v[86:89], v[172:175], v[204:207], v[86:89]
	v_mfma_f32_16x16x32_f16 v[82:85], v[180:183], v[204:207], v[82:85]
	v_mfma_f32_16x16x32_f16 v[70:73], v[172:175], v[212:215], v[70:73]
	v_mfma_f32_16x16x32_f16 v[66:69], v[180:183], v[212:215], v[66:69]
	s_barrier
	s_add_i32 s50, s43, s31
	v_lshl_add_u64 v[216:217], s[24:25], 0, v[148:149]
	s_mov_b32 m0, s50
	global_load_lds_dwordx4 v[216:217], off
	s_add_i32 m0, s50, 0x2000
	s_add_u32 s50, s24, 0x40000
	v_lshl_add_u64 v[218:219], s[24:25], 0, v[152:153]
	s_addc_u32 s51, s25, 0
	s_add_i32 s52, s44, s31
	global_load_lds_dwordx4 v[218:219], off
	v_lshl_add_u64 v[220:221], s[50:51], 0, v[148:149]
	s_mov_b32 m0, s52
	v_lshl_add_u64 v[222:223], s[26:27], 0, v[150:151]
	global_load_lds_dwordx4 v[220:221], off
	v_lshl_add_u64 v[220:221], s[50:51], 0, v[152:153]
	s_add_i32 m0, s52, 0x2000
	s_nop 0
	global_load_lds_dwordx4 v[220:221], off
	v_lshl_add_u64 v[220:221], s[26:27], 0, v[146:147]
	s_mov_b32 m0, s33
	s_nop 0
	global_load_lds_dwordx4 v[220:221], off
	s_mov_b32 m0, s34
	s_nop 0
	global_load_lds_dwordx4 v[222:223], off
	ds_read_b128 v[184:187], v170 offset:16384
	ds_read_b128 v[188:191], v170 offset:17408
	ds_read_b128 v[192:195], v170 offset:18432
	ds_read_b128 v[196:199], v170 offset:19456
	ds_read_b128 v[200:203], v170 offset:20480
	ds_read_b128 v[204:207], v170 offset:21504
	ds_read_b128 v[208:211], v170 offset:22528
	ds_read_b128 v[212:215], v170 offset:23552
	s_waitcnt vmcnt(8)
	s_waitcnt lgkmcnt(0)
	s_barrier
; #define GM_LDA(dst, b, h) do { _Pragma("unroll") for (int m = 0; m < 4; ++m) _Pragma("unroll") for (int k = 0; k < 2; ++k) dst[m][k] = *(const LAS s16x8*)(lds + GM_SA(b, h) + aoff + m * 2048 + k * 1024); } while (0)
; #define GM_LDB(dst, b, h) do { _Pragma("unroll") for (int n = 0; n < 2; ++n) _Pragma("unroll") for (int k = 0; k < 2; ++k) dst[n][k] = *(const LAS s16x8*)(lds + GM_SB(b, h) + boff + n * 2048 + k * 1024); } while (0)
; #define GM_MMA(ai, bj, At, Bt) do { __builtin_amdgcn_s_setprio(1); _Pragma("unroll") for (int m = 0; m < 4; ++m) _Pragma("unroll") for (int n = 0; n < 2; ++n) _Pragma("unroll") for (int k = 0; k < 2; ++k) \
;         acc[ai][bj][m][n] = mma16<BF>(Bt[n][k], At[m][k], acc[ai][bj][m][n]); __builtin_amdgcn_s_setprio(0); } while (0)
; #define GM_WAIT_V(n) asm volatile("s_waitcnt vmcnt(" #n ")" ::: "memory")
; #define GM_WAIT_L(n) asm volatile("s_waitcnt lgkmcnt(" #n ")" ::: "memory")
; #define GM_BAR __builtin_amdgcn_s_barrier()
; #define GM_SCHED __builtin_amdgcn_sched_barrier(0)
; #define GM_STA_H1(buf, p, o1) do { if constexpr (GATHER) GM_STAGE(buf, p, o1); else GM_STAGE(buf, (p) + hstepB, voffA); } while (0)
; template <bool BF, bool GATHER = false, class Epi, class Hook>
; __device__ __forceinline__ void gemm_phase(LAS unsigned char* lds, const Gemm g, const Order& S, const Epi& E, Hook& HK) {
;     ...
;             GM_WAIT_V(8); GM_WAIT_L(0); GM_BAR; GM_MMA(1, 0, At, B0); GM_MMA(1, 1, At, B1); GM_BAR; GM_SCHED;
;             GM_LDB(B0, 1, 0); GM_LDB(B1, 1, 1); GM_SCHED; GM_LDA(At, 1, 0); GM_STA_H1(GM_SA(0, 1), a2, s1);
;             GM_WAIT_V(8); GM_WAIT_L(0); GM_BAR; GM_MMA(0, 0, At, B0); GM_MMA(0, 1, At, B1); GM_BAR; GM_SCHED;
	s_waitcnt lgkmcnt(0)
	v_mfma_f32_16x16x32_f16 v[62:65], v[122:125], v[184:187], v[62:65]
	v_mfma_f32_16x16x32_f16 v[58:61], v[130:133], v[184:187], v[58:61]
	v_mfma_f32_16x16x32_f16 v[46:49], v[122:125], v[192:195], v[46:49]
	v_mfma_f32_16x16x32_f16 v[42:45], v[130:133], v[192:195], v[42:45]
	v_mfma_f32_16x16x32_f16 v[30:33], v[122:125], v[200:203], v[30:33]
	v_mfma_f32_16x16x32_f16 v[26:29], v[130:133], v[200:203], v[26:29]
	v_mfma_f32_16x16x32_f16 v[14:17], v[122:125], v[208:211], v[14:17]
	v_mfma_f32_16x16x32_f16 v[10:13], v[130:133], v[208:211], v[10:13]
	v_mfma_f32_16x16x32_f16 v[62:65], v[126:129], v[188:191], v[62:65]
	v_mfma_f32_16x16x32_f16 v[58:61], v[134:137], v[188:191], v[58:61]
	v_mfma_f32_16x16x32_f16 v[46:49], v[126:129], v[196:199], v[46:49]
	v_mfma_f32_16x16x32_f16 v[42:45], v[134:137], v[196:199], v[42:45]
	v_mfma_f32_16x16x32_f16 v[30:33], v[126:129], v[204:207], v[30:33]
	v_mfma_f32_16x16x32_f16 v[26:29], v[134:137], v[204:207], v[26:29]
	v_mfma_f32_16x16x32_f16 v[14:17], v[126:129], v[212:215], v[14:17]
	v_mfma_f32_16x16x32_f16 v[10:13], v[134:137], v[212:215], v[10:13]
	v_mfma_f32_16x16x32_f16 v[54:57], v[162:165], v[184:187], v[54:57]
	v_mfma_f32_16x16x32_f16 v[50:53], v[176:179], v[184:187], v[50:53]
	v_mfma_f32_16x16x32_f16 v[38:41], v[162:165], v[192:195], v[38:41]
	v_mfma_f32_16x16x32_f16 v[34:37], v[176:179], v[192:195], v[34:37]
	v_mfma_f32_16x16x32_f16 v[22:25], v[162:165], v[200:203], v[22:25]
	v_mfma_f32_16x16x32_f16 v[18:21], v[176:179], v[200:203], v[18:21]
	v_mfma_f32_16x16x32_f16 v[6:9], v[162:165], v[208:211], v[6:9]
	v_mfma_f32_16x16x32_f16 v[2:5], v[176:179], v[208:211], v[2:5]
	v_mfma_f32_16x16x32_f16 v[54:57], v[172:175], v[188:191], v[54:57]
	v_mfma_f32_16x16x32_f16 v[50:53], v[180:183], v[188:191], v[50:53]
	v_mfma_f32_16x16x32_f16 v[38:41], v[172:175], v[196:199], v[38:41]
	v_mfma_f32_16x16x32_f16 v[34:37], v[180:183], v[196:199], v[34:37]
	v_mfma_f32_16x16x32_f16 v[22:25], v[172:175], v[204:207], v[22:25]
	v_mfma_f32_16x16x32_f16 v[18:21], v[180:183], v[204:207], v[18:21]
	v_mfma_f32_16x16x32_f16 v[6:9], v[172:175], v[212:215], v[6:9]
	v_mfma_f32_16x16x32_f16 v[2:5], v[180:183], v[212:215], v[2:5]
	s_barrier
	s_add_u32 s26, s26, 0x40000
	s_addc_u32 s27, s27, 0
	s_mov_b32 m0, s35
	v_lshl_add_u64 v[224:225], s[26:27], 0, v[146:147]
	global_load_lds_dwordx4 v[224:225], off
	v_lshl_add_u64 v[224:225], s[26:27], 0, v[150:151]
	s_mov_b32 m0, s36
	s_nop 0
	global_load_lds_dwordx4 v[224:225], off
	s_mov_b32 s51, 0x1c000
	s_mov_b32 s50, 0x18000
	v_add_u32_e32 v244, s50, v166
	v_add_u32_e32 v245, s51, v166
	ds_read_b128 v[122:125], v244
	ds_read_b128 v[126:129], v244 offset:1024
	ds_read_b128 v[130:133], v244 offset:2048
	ds_read_b128 v[134:137], v244 offset:3072
	ds_read_b128 v[162:165], v245
	ds_read_b128 v[172:175], v245 offset:1024
	ds_read_b128 v[176:179], v245 offset:2048
	ds_read_b128 v[180:183], v245 offset:3072
	ds_read_b128 v[184:187], v170 offset:32768
	ds_read_b128 v[188:191], v170 offset:33792
	ds_read_b128 v[192:195], v170 offset:34816
	ds_read_b128 v[196:199], v170 offset:35840
	ds_read_b128 v[200:203], v170 offset:36864
	ds_read_b128 v[204:207], v170 offset:37888
	ds_read_b128 v[208:211], v170 offset:38912
	ds_read_b128 v[212:215], v170 offset:39936
	s_waitcnt vmcnt(8)
	s_waitcnt lgkmcnt(0)
	s_barrier
	s_waitcnt lgkmcnt(0)
	v_mfma_f32_16x16x32_f16 v[142:145], v[122:125], v[184:187], v[142:145]
	v_mfma_f32_16x16x32_f16 v[138:141], v[130:133], v[184:187], v[138:141]
	v_mfma_f32_16x16x32_f16 v[110:113], v[122:125], v[192:195], v[110:113]
	v_mfma_f32_16x16x32_f16 v[106:109], v[130:133], v[192:195], v[106:109]
	v_mfma_f32_16x16x32_f16 v[94:97], v[122:125], v[200:203], v[94:97]
	v_mfma_f32_16x16x32_f16 v[90:93], v[130:133], v[200:203], v[90:93]
	v_mfma_f32_16x16x32_f16 v[78:81], v[122:125], v[208:211], v[78:81]
	v_mfma_f32_16x16x32_f16 v[74:77], v[130:133], v[208:211], v[74:77]
	v_mfma_f32_16x16x32_f16 v[142:145], v[126:129], v[188:191], v[142:145]
	v_mfma_f32_16x16x32_f16 v[138:141], v[134:137], v[188:191], v[138:141]
	v_mfma_f32_16x16x32_f16 v[110:113], v[126:129], v[196:199], v[110:113]
	v_mfma_f32_16x16x32_f16 v[106:109], v[134:137], v[196:199], v[106:109]
	v_mfma_f32_16x16x32_f16 v[94:97], v[126:129], v[204:207], v[94:97]
	v_mfma_f32_16x16x32_f16 v[90:93], v[134:137], v[204:207], v[90:93]
	v_mfma_f32_16x16x32_f16 v[78:81], v[126:129], v[212:215], v[78:81]
	v_mfma_f32_16x16x32_f16 v[74:77], v[134:137], v[212:215], v[74:77]
	v_mfma_f32_16x16x32_f16 v[118:121], v[162:165], v[184:187], v[118:121]
	v_mfma_f32_16x16x32_f16 v[114:117], v[176:179], v[184:187], v[114:117]
	v_mfma_f32_16x16x32_f16 v[102:105], v[162:165], v[192:195], v[102:105]
	v_mfma_f32_16x16x32_f16 v[98:101], v[176:179], v[192:195], v[98:101]
	v_mfma_f32_16x16x32_f16 v[86:89], v[162:165], v[200:203], v[86:89]
	v_mfma_f32_16x16x32_f16 v[82:85], v[176:179], v[200:203], v[82:85]
	v_mfma_f32_16x16x32_f16 v[70:73], v[162:165], v[208:211], v[70:73]
	v_mfma_f32_16x16x32_f16 v[66:69], v[176:179], v[208:211], v[66:69]
	v_mfma_f32_16x16x32_f16 v[118:121], v[172:175], v[188:191], v[118:121]
	v_mfma_f32_16x16x32_f16 v[114:117], v[180:183], v[188:191], v[114:117]
	v_mfma_f32_16x16x32_f16 v[102:105], v[172:175], v[196:199], v[102:105]
	v_mfma_f32_16x16x32_f16 v[98:101], v[180:183], v[196:199], v[98:101]
	v_mfma_f32_16x16x32_f16 v[86:89], v[172:175], v[204:207], v[86:89]
	v_mfma_f32_16x16x32_f16 v[82:85], v[180:183], v[204:207], v[82:85]
	v_mfma_f32_16x16x32_f16 v[70:73], v[172:175], v[212:215], v[70:73]
	v_mfma_f32_16x16x32_f16 v[66:69], v[180:183], v[212:215], v[66:69]
	s_barrier
; #define GM_STAGE(bufoff, gbase, voff) do { _Pragma("unroll") for (int _i = 0; _i < 2; ++_i) \
;         __builtin_amdgcn_global_load_lds((const unsigned*)((const char*)(gbase) + (voff)[_i]), (LAS unsigned*)(lds + (bufoff) + ldsw + _i * 8192), 16, 0, 0); } while (0)
; #define GM_LDA(dst, b, h) do { _Pragma("unroll") for (int m = 0; m < 4; ++m) _Pragma("unroll") for (int k = 0; k < 2; ++k) dst[m][k] = *(const LAS s16x8*)(lds + GM_SA(b, h) + aoff + m * 2048 + k * 1024); } while (0)
; #define GM_MMA(ai, bj, At, Bt) do { __builtin_amdgcn_s_setprio(1); _Pragma("unroll") for (int m = 0; m < 4; ++m) _Pragma("unroll") for (int n = 0; n < 2; ++n) _Pragma("unroll") for (int k = 0; k < 2; ++k) \
;         acc[ai][bj][m][n] = mma16<BF>(Bt[n][k], At[m][k], acc[ai][bj][m][n]); __builtin_amdgcn_s_setprio(0); } while (0)
; #define GM_WAIT_V(n) asm volatile("s_waitcnt vmcnt(" #n ")" ::: "memory")
; #define GM_WAIT_L(n) asm volatile("s_waitcnt lgkmcnt(" #n ")" ::: "memory")
; #define GM_BAR __builtin_amdgcn_s_barrier()
; #define GM_SCHED __builtin_amdgcn_sched_barrier(0)
; #define GM_STA_H0(buf, p, o0) do { if constexpr (GATHER) GM_STAGE(buf, p, o0); else GM_STAGE(buf, p, voffA); } while (0)
; template <bool BF, bool GATHER = false, class Epi, class Hook>
; __device__ __forceinline__ void gemm_phase(LAS unsigned char* lds, const Gemm g, const Order& S, const Epi& E, Hook& HK) {
;     ...
;         for (int t = 0; t < nt; t += 2) {
;     ...
;             GM_LDA(At, 1, 1); GM_STAGE(GM_SB(1, 0), b3, voffB); GM_STAGE(GM_SB(1, 1), b3 + hstepB, voffB); GM_STA_H0(GM_SA(1, 0), a3, s0);
;             GM_WAIT_V(8); GM_WAIT_L(0); GM_BAR; GM_MMA(1, 0, At, B0); GM_MMA(1, 1, At, B1); GM_BAR; GM_SCHED;
;     ...
;         if (wr == 0) GM_BAR;
	s_add_i32 s26, s50, s31
	v_lshl_add_u64 v[216:217], v[216:217], 0, s[10:11]
	s_mov_b32 m0, s26
	global_load_lds_dwordx4 v[216:217], off
	s_add_i32 m0, s26, 0x2000
	s_add_u32 s24, s24, 0x40080
	v_lshl_add_u64 v[216:217], v[218:219], 0, s[10:11]
	s_addc_u32 s25, s25, 0
	s_add_i32 s26, s51, s31
	global_load_lds_dwordx4 v[216:217], off
	v_lshl_add_u64 v[216:217], s[24:25], 0, v[148:149]
	s_mov_b32 m0, s26
	s_nop 0
	global_load_lds_dwordx4 v[216:217], off
	v_lshl_add_u64 v[216:217], s[24:25], 0, v[152:153]
	s_add_i32 m0, s26, 0x2000
	s_nop 0
	global_load_lds_dwordx4 v[216:217], off
	v_lshl_add_u64 v[216:217], v[220:221], 0, s[10:11]
	s_mov_b32 m0, s40
	s_nop 0
	global_load_lds_dwordx4 v[216:217], off
	v_lshl_add_u64 v[216:217], v[222:223], 0, s[10:11]
	s_mov_b32 m0, s41
	s_nop 0
	global_load_lds_dwordx4 v[216:217], off
	ds_read_b128 v[184:187], v170 offset:49152
	ds_read_b128 v[188:191], v170 offset:50176
	ds_read_b128 v[192:195], v170 offset:51200
	ds_read_b128 v[196:199], v170 offset:52224
	ds_read_b128 v[200:203], v170 offset:53248
	ds_read_b128 v[204:207], v170 offset:54272
	ds_read_b128 v[208:211], v170 offset:55296
	ds_read_b128 v[212:215], v170 offset:56320
	s_waitcnt vmcnt(8)
	s_waitcnt lgkmcnt(0)
	s_barrier
	s_waitcnt lgkmcnt(0)
	v_mfma_f32_16x16x32_f16 v[62:65], v[122:125], v[184:187], v[62:65]
	v_mfma_f32_16x16x32_f16 v[58:61], v[130:133], v[184:187], v[58:61]
	v_mfma_f32_16x16x32_f16 v[46:49], v[122:125], v[192:195], v[46:49]
	v_mfma_f32_16x16x32_f16 v[42:45], v[130:133], v[192:195], v[42:45]
	v_mfma_f32_16x16x32_f16 v[30:33], v[122:125], v[200:203], v[30:33]
	v_mfma_f32_16x16x32_f16 v[26:29], v[130:133], v[200:203], v[26:29]
	v_mfma_f32_16x16x32_f16 v[14:17], v[122:125], v[208:211], v[14:17]
	v_mfma_f32_16x16x32_f16 v[10:13], v[130:133], v[208:211], v[10:13]
	v_mfma_f32_16x16x32_f16 v[62:65], v[126:129], v[188:191], v[62:65]
	v_mfma_f32_16x16x32_f16 v[58:61], v[134:137], v[188:191], v[58:61]
	v_mfma_f32_16x16x32_f16 v[46:49], v[126:129], v[196:199], v[46:49]
	v_mfma_f32_16x16x32_f16 v[42:45], v[134:137], v[196:199], v[42:45]
	v_mfma_f32_16x16x32_f16 v[30:33], v[126:129], v[204:207], v[30:33]
	v_mfma_f32_16x16x32_f16 v[26:29], v[134:137], v[204:207], v[26:29]
	v_mfma_f32_16x16x32_f16 v[14:17], v[126:129], v[212:215], v[14:17]
	v_mfma_f32_16x16x32_f16 v[10:13], v[134:137], v[212:215], v[10:13]
	v_mfma_f32_16x16x32_f16 v[54:57], v[162:165], v[184:187], v[54:57]
	v_mfma_f32_16x16x32_f16 v[50:53], v[176:179], v[184:187], v[50:53]
	v_mfma_f32_16x16x32_f16 v[38:41], v[162:165], v[192:195], v[38:41]
	v_mfma_f32_16x16x32_f16 v[34:37], v[176:179], v[192:195], v[34:37]
	v_mfma_f32_16x16x32_f16 v[22:25], v[162:165], v[200:203], v[22:25]
	v_mfma_f32_16x16x32_f16 v[18:21], v[176:179], v[200:203], v[18:21]
	v_mfma_f32_16x16x32_f16 v[6:9], v[162:165], v[208:211], v[6:9]
	v_mfma_f32_16x16x32_f16 v[2:5], v[176:179], v[208:211], v[2:5]
	v_mfma_f32_16x16x32_f16 v[54:57], v[172:175], v[188:191], v[54:57]
	v_mfma_f32_16x16x32_f16 v[50:53], v[180:183], v[188:191], v[50:53]
	v_mfma_f32_16x16x32_f16 v[38:41], v[172:175], v[196:199], v[38:41]
	v_mfma_f32_16x16x32_f16 v[34:37], v[180:183], v[196:199], v[34:37]
	v_mfma_f32_16x16x32_f16 v[22:25], v[172:175], v[204:207], v[22:25]
	v_mfma_f32_16x16x32_f16 v[18:21], v[180:183], v[204:207], v[18:21]
	v_mfma_f32_16x16x32_f16 v[6:9], v[172:175], v[212:215], v[6:9]
	v_mfma_f32_16x16x32_f16 v[2:5], v[180:183], v[212:215], v[2:5]
	s_barrier
	s_add_i32 s49, s49, 2
	s_add_u32 s22, s22, 0x100
	s_addc_u32 s23, s23, 0
	s_add_u32 s47, s47, 0x100
	s_addc_u32 s48, s48, 0
	s_cmp_gt_u32 s49, 13
	s_cbranch_scc0 .LBB0_1480
	s_and_b64 vcc, exec, s[12:13]
	s_cbranch_vccz .LBB0_1483
	s_barrier

; #define GM_STAGE(bufoff, gbase, voff) do { _Pragma("unroll") for (int _i = 0; _i < 2; ++_i) \
;         __builtin_amdgcn_global_load_lds((const unsigned*)((const char*)(gbase) + (voff)[_i]), (LAS unsigned*)(lds + (bufoff) + ldsw + _i * 8192), 16, 0, 0); } while (0)
; #define GM_LDA(dst, b, h) do { _Pragma("unroll") for (int m = 0; m < 4; ++m) _Pragma("unroll") for (int k = 0; k < 2; ++k) dst[m][k] = *(const LAS s16x8*)(lds + GM_SA(b, h) + aoff + m * 2048 + k * 1024); } while (0)
; #define GM_LDB(dst, b, h) do { _Pragma("unroll") for (int n = 0; n < 2; ++n) _Pragma("unroll") for (int k = 0; k < 2; ++k) dst[n][k] = *(const LAS s16x8*)(lds + GM_SB(b, h) + boff + n * 2048 + k * 1024); } while (0)
; #define GM_MMA(ai, bj, At, Bt) do { __builtin_amdgcn_s_setprio(1); _Pragma("unroll") for (int m = 0; m < 4; ++m) _Pragma("unroll") for (int n = 0; n < 2; ++n) _Pragma("unroll") for (int k = 0; k < 2; ++k) \
;         acc[ai][bj][m][n] = mma16<BF>(Bt[n][k], At[m][k], acc[ai][bj][m][n]); __builtin_amdgcn_s_setprio(0); } while (0)
; #define GM_WAIT_V(n) asm volatile("s_waitcnt vmcnt(" #n ")" ::: "memory")
; #define GM_WAIT_L(n) asm volatile("s_waitcnt lgkmcnt(" #n ")" ::: "memory")
; #define GM_BAR __builtin_amdgcn_s_barrier()
; #define GM_SCHED __builtin_amdgcn_sched_barrier(0)
; #define GM_STA_H0(buf, p, o0) do { if constexpr (GATHER) GM_STAGE(buf, p, o0); else GM_STAGE(buf, p, voffA); } while (0)
; #define GM_STA_H1(buf, p, o1) do { if constexpr (GATHER) GM_STAGE(buf, p, o1); else GM_STAGE(buf, (p) + hstepB, voffA); } while (0)
; template <bool BF, bool GATHER = false, class Epi, class Hook>
; __device__ __forceinline__ void gemm_phase(LAS unsigned char* lds, const Gemm g, const Order& S, const Epi& E, Hook& HK) {
;     ...
;             GM_LDB(B0, 0, 0); GM_LDB(B1, 0, 1); GM_SCHED; GM_LDA(At, 0, 0); GM_STA_H1(GM_SA(1, 1), a1, gA1);
;             GM_WAIT_V(8); GM_WAIT_L(0); GM_BAR; GM_MMA(0, 0, At, B0); GM_MMA(0, 1, At, B1); GM_BAR; GM_SCHED;
;             GM_LDA(At, 0, 1); GM_STAGE(GM_SB(0, 0), b2, voffB); GM_STAGE(GM_SB(0, 1), b2 + hstepB, voffB); GM_STA_H0(GM_SA(0, 0), a2, s0);
;             GM_WAIT_V(8); GM_WAIT_L(0); GM_BAR; GM_MMA(1, 0, At, B0); GM_MMA(1, 1, At, B1); GM_BAR; GM_SCHED;
.LBB0_1867:
	s_add_u32 s22, s2, 0x100
	s_addc_u32 s23, s3, 0
	s_cmp_eq_u32 s52, 40
	s_cselect_b32 s27, s7, s23
	s_cselect_b32 s26, s6, s22
	s_cselect_b32 s25, s21, s51
	s_cselect_b32 s24, s20, s50
	v_lshl_add_u64 v[216:217], s[2:3], 0, v[138:139]
	s_add_i32 m0, s29, 0xc000
	global_load_lds_dwordx4 v[216:217], off
	v_lshl_add_u64 v[216:217], s[2:3], 0, v[140:141]
	s_add_i32 m0, s29, 0xe000
	s_nop 0
	global_load_lds_dwordx4 v[216:217], off
	ds_read_b128 v[146:149], v153
	ds_read_b128 v[156:159], v153 offset:1024
	ds_read_b128 v[160:163], v153 offset:2048
	ds_read_b128 v[164:167], v153 offset:3072
	ds_read_b128 v[168:171], v154
	ds_read_b128 v[172:175], v154 offset:1024
	ds_read_b128 v[176:179], v154 offset:2048
	ds_read_b128 v[180:183], v154 offset:3072
	ds_read_b128 v[184:187], v155
	ds_read_b128 v[188:191], v155 offset:1024
	ds_read_b128 v[192:195], v155 offset:2048
	ds_read_b128 v[196:199], v155 offset:3072
	ds_read_b128 v[200:203], v155 offset:4096
	ds_read_b128 v[204:207], v155 offset:5120
	ds_read_b128 v[208:211], v155 offset:6144
	ds_read_b128 v[212:215], v155 offset:7168
	s_waitcnt vmcnt(8)
	s_waitcnt lgkmcnt(0)
	s_barrier
	s_waitcnt lgkmcnt(0)
	v_mfma_f32_16x16x32_bf16 v[126:129], v[146:149], v[184:187], v[126:129]
	v_mfma_f32_16x16x32_bf16 v[122:125], v[160:163], v[184:187], v[122:125]
	v_mfma_f32_16x16x32_bf16 v[110:113], v[146:149], v[192:195], v[110:113]
	v_mfma_f32_16x16x32_bf16 v[106:109], v[160:163], v[192:195], v[106:109]
	v_mfma_f32_16x16x32_bf16 v[94:97], v[146:149], v[200:203], v[94:97]
	v_mfma_f32_16x16x32_bf16 v[90:93], v[160:163], v[200:203], v[90:93]
	v_mfma_f32_16x16x32_bf16 v[78:81], v[146:149], v[208:211], v[78:81]
	v_mfma_f32_16x16x32_bf16 v[74:77], v[160:163], v[208:211], v[74:77]
	v_mfma_f32_16x16x32_bf16 v[126:129], v[156:159], v[188:191], v[126:129]
	v_mfma_f32_16x16x32_bf16 v[122:125], v[164:167], v[188:191], v[122:125]
	v_mfma_f32_16x16x32_bf16 v[110:113], v[156:159], v[196:199], v[110:113]
	v_mfma_f32_16x16x32_bf16 v[106:109], v[164:167], v[196:199], v[106:109]
	v_mfma_f32_16x16x32_bf16 v[94:97], v[156:159], v[204:207], v[94:97]
	v_mfma_f32_16x16x32_bf16 v[90:93], v[164:167], v[204:207], v[90:93]
	v_mfma_f32_16x16x32_bf16 v[78:81], v[156:159], v[212:215], v[78:81]
	v_mfma_f32_16x16x32_bf16 v[74:77], v[164:167], v[212:215], v[74:77]
	v_mfma_f32_16x16x32_bf16 v[118:121], v[168:171], v[184:187], v[118:121]
	v_mfma_f32_16x16x32_bf16 v[114:117], v[176:179], v[184:187], v[114:117]
	v_mfma_f32_16x16x32_bf16 v[102:105], v[168:171], v[192:195], v[102:105]
	v_mfma_f32_16x16x32_bf16 v[98:101], v[176:179], v[192:195], v[98:101]
	v_mfma_f32_16x16x32_bf16 v[86:89], v[168:171], v[200:203], v[86:89]
	v_mfma_f32_16x16x32_bf16 v[82:85], v[176:179], v[200:203], v[82:85]
	v_mfma_f32_16x16x32_bf16 v[70:73], v[168:171], v[208:211], v[70:73]
	v_mfma_f32_16x16x32_bf16 v[66:69], v[176:179], v[208:211], v[66:69]
	v_mfma_f32_16x16x32_bf16 v[118:121], v[172:175], v[188:191], v[118:121]
	v_mfma_f32_16x16x32_bf16 v[114:117], v[180:183], v[188:191], v[114:117]
	v_mfma_f32_16x16x32_bf16 v[102:105], v[172:175], v[196:199], v[102:105]
	v_mfma_f32_16x16x32_bf16 v[98:101], v[180:183], v[196:199], v[98:101]
	v_mfma_f32_16x16x32_bf16 v[86:89], v[172:175], v[204:207], v[86:89]
	v_mfma_f32_16x16x32_bf16 v[82:85], v[180:183], v[204:207], v[82:85]
	v_mfma_f32_16x16x32_bf16 v[70:73], v[172:175], v[212:215], v[70:73]
	v_mfma_f32_16x16x32_bf16 v[66:69], v[180:183], v[212:215], v[66:69]
	s_barrier
	s_add_i32 s2, s43, s28
	v_lshl_add_u64 v[216:217], s[24:25], 0, v[132:133]
	s_mov_b32 m0, s2
	global_load_lds_dwordx4 v[216:217], off
	s_add_i32 m0, s2, 0x2000
	s_add_u32 s2, s24, 0xb0000
	v_lshl_add_u64 v[218:219], s[24:25], 0, v[136:137]
	s_addc_u32 s3, s25, 0
	s_add_i32 s53, s44, s28
	global_load_lds_dwordx4 v[218:219], off
	v_lshl_add_u64 v[220:221], s[2:3], 0, v[132:133]
	s_mov_b32 m0, s53
	v_lshl_add_u64 v[222:223], s[26:27], 0, v[134:135]
	global_load_lds_dwordx4 v[220:221], off
	v_lshl_add_u64 v[220:221], s[2:3], 0, v[136:137]
	s_add_i32 m0, s53, 0x2000
	s_nop 0
	global_load_lds_dwordx4 v[220:221], off
	v_lshl_add_u64 v[220:221], s[26:27], 0, v[130:131]
	s_mov_b32 m0, s29
	s_nop 0
	global_load_lds_dwordx4 v[220:221], off
	s_mov_b32 m0, s30
	s_nop 0
	global_load_lds_dwordx4 v[222:223], off
	ds_read_b128 v[184:187], v155 offset:16384
	ds_read_b128 v[188:191], v155 offset:17408
	ds_read_b128 v[192:195], v155 offset:18432
	ds_read_b128 v[196:199], v155 offset:19456
	ds_read_b128 v[200:203], v155 offset:20480
	ds_read_b128 v[204:207], v155 offset:21504
	ds_read_b128 v[208:211], v155 offset:22528
	ds_read_b128 v[212:215], v155 offset:23552
	s_waitcnt vmcnt(8)
	s_waitcnt lgkmcnt(0)
	s_barrier
; #define GM_LDA(dst, b, h) do { _Pragma("unroll") for (int m = 0; m < 4; ++m) _Pragma("unroll") for (int k = 0; k < 2; ++k) dst[m][k] = *(const LAS s16x8*)(lds + GM_SA(b, h) + aoff + m * 2048 + k * 1024); } while (0)
; #define GM_LDB(dst, b, h) do { _Pragma("unroll") for (int n = 0; n < 2; ++n) _Pragma("unroll") for (int k = 0; k < 2; ++k) dst[n][k] = *(const LAS s16x8*)(lds + GM_SB(b, h) + boff + n * 2048 + k * 1024); } while (0)
; #define GM_MMA(ai, bj, At, Bt) do { __builtin_amdgcn_s_setprio(1); _Pragma("unroll") for (int m = 0; m < 4; ++m) _Pragma("unroll") for (int n = 0; n < 2; ++n) _Pragma("unroll") for (int k = 0; k < 2; ++k) \
;         acc[ai][bj][m][n] = mma16<BF>(Bt[n][k], At[m][k], acc[ai][bj][m][n]); __builtin_amdgcn_s_setprio(0); } while (0)
; #define GM_WAIT_V(n) asm volatile("s_waitcnt vmcnt(" #n ")" ::: "memory")
; #define GM_WAIT_L(n) asm volatile("s_waitcnt lgkmcnt(" #n ")" ::: "memory")
; #define GM_BAR __builtin_amdgcn_s_barrier()
; #define GM_SCHED __builtin_amdgcn_sched_barrier(0)
; #define GM_STA_H1(buf, p, o1) do { if constexpr (GATHER) GM_STAGE(buf, p, o1); else GM_STAGE(buf, (p) + hstepB, voffA); } while (0)
; template <bool BF, bool GATHER = false, class Epi, class Hook>
; __device__ __forceinline__ void gemm_phase(LAS unsigned char* lds, const Gemm g, const Order& S, const Epi& E, Hook& HK) {
;     ...
;             GM_WAIT_V(8); GM_WAIT_L(0); GM_BAR; GM_MMA(1, 0, At, B0); GM_MMA(1, 1, At, B1); GM_BAR; GM_SCHED;
;             GM_LDB(B0, 1, 0); GM_LDB(B1, 1, 1); GM_SCHED; GM_LDA(At, 1, 0); GM_STA_H1(GM_SA(0, 1), a2, s1);
;             GM_WAIT_V(8); GM_WAIT_L(0); GM_BAR; GM_MMA(0, 0, At, B0); GM_MMA(0, 1, At, B1); GM_BAR; GM_SCHED;
	s_waitcnt lgkmcnt(0)
	v_mfma_f32_16x16x32_bf16 v[62:65], v[146:149], v[184:187], v[62:65]
	v_mfma_f32_16x16x32_bf16 v[58:61], v[160:163], v[184:187], v[58:61]
	v_mfma_f32_16x16x32_bf16 v[46:49], v[146:149], v[192:195], v[46:49]
	v_mfma_f32_16x16x32_bf16 v[42:45], v[160:163], v[192:195], v[42:45]
	v_mfma_f32_16x16x32_bf16 v[30:33], v[146:149], v[200:203], v[30:33]
	v_mfma_f32_16x16x32_bf16 v[26:29], v[160:163], v[200:203], v[26:29]
	v_mfma_f32_16x16x32_bf16 v[14:17], v[146:149], v[208:211], v[14:17]
	v_mfma_f32_16x16x32_bf16 v[10:13], v[160:163], v[208:211], v[10:13]
	v_mfma_f32_16x16x32_bf16 v[62:65], v[156:159], v[188:191], v[62:65]
	v_mfma_f32_16x16x32_bf16 v[58:61], v[164:167], v[188:191], v[58:61]
	v_mfma_f32_16x16x32_bf16 v[46:49], v[156:159], v[196:199], v[46:49]
	v_mfma_f32_16x16x32_bf16 v[42:45], v[164:167], v[196:199], v[42:45]
	v_mfma_f32_16x16x32_bf16 v[30:33], v[156:159], v[204:207], v[30:33]
	v_mfma_f32_16x16x32_bf16 v[26:29], v[164:167], v[204:207], v[26:29]
	v_mfma_f32_16x16x32_bf16 v[14:17], v[156:159], v[212:215], v[14:17]
	v_mfma_f32_16x16x32_bf16 v[10:13], v[164:167], v[212:215], v[10:13]
	v_mfma_f32_16x16x32_bf16 v[54:57], v[168:171], v[184:187], v[54:57]
	v_mfma_f32_16x16x32_bf16 v[50:53], v[176:179], v[184:187], v[50:53]
	v_mfma_f32_16x16x32_bf16 v[38:41], v[168:171], v[192:195], v[38:41]
	v_mfma_f32_16x16x32_bf16 v[34:37], v[176:179], v[192:195], v[34:37]
	v_mfma_f32_16x16x32_bf16 v[22:25], v[168:171], v[200:203], v[22:25]
	v_mfma_f32_16x16x32_bf16 v[18:21], v[176:179], v[200:203], v[18:21]
	v_mfma_f32_16x16x32_bf16 v[6:9], v[168:171], v[208:211], v[6:9]
	v_mfma_f32_16x16x32_bf16 v[2:5], v[176:179], v[208:211], v[2:5]
	v_mfma_f32_16x16x32_bf16 v[54:57], v[172:175], v[188:191], v[54:57]
	v_mfma_f32_16x16x32_bf16 v[50:53], v[180:183], v[188:191], v[50:53]
	v_mfma_f32_16x16x32_bf16 v[38:41], v[172:175], v[196:199], v[38:41]
	v_mfma_f32_16x16x32_bf16 v[34:37], v[180:183], v[196:199], v[34:37]
	v_mfma_f32_16x16x32_bf16 v[22:25], v[172:175], v[204:207], v[22:25]
	v_mfma_f32_16x16x32_bf16 v[18:21], v[180:183], v[204:207], v[18:21]
	v_mfma_f32_16x16x32_bf16 v[6:9], v[172:175], v[212:215], v[6:9]
	v_mfma_f32_16x16x32_bf16 v[2:5], v[180:183], v[212:215], v[2:5]
	s_barrier
	s_add_u32 s2, s26, 0xb0000
	s_addc_u32 s3, s27, 0
	s_mov_b32 m0, s31
	v_lshl_add_u64 v[224:225], s[2:3], 0, v[130:131]
	global_load_lds_dwordx4 v[224:225], off
	v_lshl_add_u64 v[224:225], s[2:3], 0, v[134:135]
	s_mov_b32 m0, s33
	s_nop 0
	global_load_lds_dwordx4 v[224:225], off
	s_mov_b32 s54, 0x1c000
	s_mov_b32 s53, 0x18000
	v_add_u32_e32 v244, s53, v150
	v_add_u32_e32 v245, s54, v150
	ds_read_b128 v[146:149], v244
	ds_read_b128 v[156:159], v244 offset:1024
	ds_read_b128 v[160:163], v244 offset:2048
	ds_read_b128 v[164:167], v244 offset:3072
	ds_read_b128 v[168:171], v245
	ds_read_b128 v[172:175], v245 offset:1024
	ds_read_b128 v[176:179], v245 offset:2048
	ds_read_b128 v[180:183], v245 offset:3072
	ds_read_b128 v[184:187], v155 offset:32768
	ds_read_b128 v[188:191], v155 offset:33792
	ds_read_b128 v[192:195], v155 offset:34816
	ds_read_b128 v[196:199], v155 offset:35840
	ds_read_b128 v[200:203], v155 offset:36864
	ds_read_b128 v[204:207], v155 offset:37888
	ds_read_b128 v[208:211], v155 offset:38912
	ds_read_b128 v[212:215], v155 offset:39936
	s_waitcnt vmcnt(8)
	s_waitcnt lgkmcnt(0)
	s_barrier
	s_waitcnt lgkmcnt(0)
	v_mfma_f32_16x16x32_bf16 v[126:129], v[146:149], v[184:187], v[126:129]
	v_mfma_f32_16x16x32_bf16 v[122:125], v[160:163], v[184:187], v[122:125]
	v_mfma_f32_16x16x32_bf16 v[110:113], v[146:149], v[192:195], v[110:113]
	v_mfma_f32_16x16x32_bf16 v[106:109], v[160:163], v[192:195], v[106:109]
	v_mfma_f32_16x16x32_bf16 v[94:97], v[146:149], v[200:203], v[94:97]
	v_mfma_f32_16x16x32_bf16 v[90:93], v[160:163], v[200:203], v[90:93]
	v_mfma_f32_16x16x32_bf16 v[78:81], v[146:149], v[208:211], v[78:81]
	v_mfma_f32_16x16x32_bf16 v[74:77], v[160:163], v[208:211], v[74:77]
	v_mfma_f32_16x16x32_bf16 v[126:129], v[156:159], v[188:191], v[126:129]
	v_mfma_f32_16x16x32_bf16 v[122:125], v[164:167], v[188:191], v[122:125]
	v_mfma_f32_16x16x32_bf16 v[110:113], v[156:159], v[196:199], v[110:113]
	v_mfma_f32_16x16x32_bf16 v[106:109], v[164:167], v[196:199], v[106:109]
	v_mfma_f32_16x16x32_bf16 v[94:97], v[156:159], v[204:207], v[94:97]
	v_mfma_f32_16x16x32_bf16 v[90:93], v[164:167], v[204:207], v[90:93]
	v_mfma_f32_16x16x32_bf16 v[78:81], v[156:159], v[212:215], v[78:81]
	v_mfma_f32_16x16x32_bf16 v[74:77], v[164:167], v[212:215], v[74:77]
	v_mfma_f32_16x16x32_bf16 v[118:121], v[168:171], v[184:187], v[118:121]
	v_mfma_f32_16x16x32_bf16 v[114:117], v[176:179], v[184:187], v[114:117]
	v_mfma_f32_16x16x32_bf16 v[102:105], v[168:171], v[192:195], v[102:105]
	v_mfma_f32_16x16x32_bf16 v[98:101], v[176:179], v[192:195], v[98:101]
	v_mfma_f32_16x16x32_bf16 v[86:89], v[168:171], v[200:203], v[86:89]
	v_mfma_f32_16x16x32_bf16 v[82:85], v[176:179], v[200:203], v[82:85]
	v_mfma_f32_16x16x32_bf16 v[70:73], v[168:171], v[208:211], v[70:73]
	v_mfma_f32_16x16x32_bf16 v[66:69], v[176:179], v[208:211], v[66:69]
	v_mfma_f32_16x16x32_bf16 v[118:121], v[172:175], v[188:191], v[118:121]
	v_mfma_f32_16x16x32_bf16 v[114:117], v[180:183], v[188:191], v[114:117]
	v_mfma_f32_16x16x32_bf16 v[102:105], v[172:175], v[196:199], v[102:105]
	v_mfma_f32_16x16x32_bf16 v[98:101], v[180:183], v[196:199], v[98:101]
	v_mfma_f32_16x16x32_bf16 v[86:89], v[172:175], v[204:207], v[86:89]
	v_mfma_f32_16x16x32_bf16 v[82:85], v[180:183], v[204:207], v[82:85]
	v_mfma_f32_16x16x32_bf16 v[70:73], v[172:175], v[212:215], v[70:73]
	v_mfma_f32_16x16x32_bf16 v[66:69], v[180:183], v[212:215], v[66:69]
	s_barrier
; #define GM_STAGE(bufoff, gbase, voff) do { _Pragma("unroll") for (int _i = 0; _i < 2; ++_i) \
;         __builtin_amdgcn_global_load_lds((const unsigned*)((const char*)(gbase) + (voff)[_i]), (LAS unsigned*)(lds + (bufoff) + ldsw + _i * 8192), 16, 0, 0); } while (0)
; #define GM_LDA(dst, b, h) do { _Pragma("unroll") for (int m = 0; m < 4; ++m) _Pragma("unroll") for (int k = 0; k < 2; ++k) dst[m][k] = *(const LAS s16x8*)(lds + GM_SA(b, h) + aoff + m * 2048 + k * 1024); } while (0)
; #define GM_MMA(ai, bj, At, Bt) do { __builtin_amdgcn_s_setprio(1); _Pragma("unroll") for (int m = 0; m < 4; ++m) _Pragma("unroll") for (int n = 0; n < 2; ++n) _Pragma("unroll") for (int k = 0; k < 2; ++k) \
;         acc[ai][bj][m][n] = mma16<BF>(Bt[n][k], At[m][k], acc[ai][bj][m][n]); __builtin_amdgcn_s_setprio(0); } while (0)
; #define GM_WAIT_V(n) asm volatile("s_waitcnt vmcnt(" #n ")" ::: "memory")
; #define GM_WAIT_L(n) asm volatile("s_waitcnt lgkmcnt(" #n ")" ::: "memory")
; #define GM_BAR __builtin_amdgcn_s_barrier()
; #define GM_SCHED __builtin_amdgcn_sched_barrier(0)
; #define GM_STA_H0(buf, p, o0) do { if constexpr (GATHER) GM_STAGE(buf, p, o0); else GM_STAGE(buf, p, voffA); } while (0)
; template <bool BF, bool GATHER = false, class Epi, class Hook>
; __device__ __forceinline__ void gemm_phase(LAS unsigned char* lds, const Gemm g, const Order& S, const Epi& E, Hook& HK) {
;     ...
;         for (int t = 0; t < nt; t += 2) {
;     ...
;             GM_LDA(At, 1, 1); GM_STAGE(GM_SB(1, 0), b3, voffB); GM_STAGE(GM_SB(1, 1), b3 + hstepB, voffB); GM_STA_H0(GM_SA(1, 0), a3, s0);
;             GM_WAIT_V(8); GM_WAIT_L(0); GM_BAR; GM_MMA(1, 0, At, B0); GM_MMA(1, 1, At, B1); GM_BAR; GM_SCHED;
;     ...
;         if (wr == 0) GM_BAR;
	s_add_i32 s2, s53, s28
	v_lshl_add_u64 v[216:217], v[216:217], 0, s[12:13]
	s_mov_b32 m0, s2
	global_load_lds_dwordx4 v[216:217], off
	s_add_i32 m0, s2, 0x2000
	s_add_u32 s2, s24, 0xb0080
	v_lshl_add_u64 v[216:217], v[218:219], 0, s[12:13]
	s_addc_u32 s3, s25, 0
	s_add_i32 s24, s54, s28
	global_load_lds_dwordx4 v[216:217], off
	v_lshl_add_u64 v[216:217], s[2:3], 0, v[132:133]
	s_mov_b32 m0, s24
	s_nop 0
	global_load_lds_dwordx4 v[216:217], off
	v_lshl_add_u64 v[216:217], s[2:3], 0, v[136:137]
	s_add_i32 m0, s24, 0x2000
	s_nop 0
	global_load_lds_dwordx4 v[216:217], off
	v_lshl_add_u64 v[216:217], v[220:221], 0, s[12:13]
	s_mov_b32 m0, s36
	s_nop 0
	global_load_lds_dwordx4 v[216:217], off
	v_lshl_add_u64 v[216:217], v[222:223], 0, s[12:13]
	s_mov_b32 m0, s37
	s_nop 0
	global_load_lds_dwordx4 v[216:217], off
	ds_read_b128 v[184:187], v155 offset:49152
	ds_read_b128 v[188:191], v155 offset:50176
	ds_read_b128 v[192:195], v155 offset:51200
	ds_read_b128 v[196:199], v155 offset:52224
	ds_read_b128 v[200:203], v155 offset:53248
	ds_read_b128 v[204:207], v155 offset:54272
	ds_read_b128 v[208:211], v155 offset:55296
	ds_read_b128 v[212:215], v155 offset:56320
	s_waitcnt vmcnt(8)
	s_waitcnt lgkmcnt(0)
	s_barrier
	s_waitcnt lgkmcnt(0)
	v_mfma_f32_16x16x32_bf16 v[62:65], v[146:149], v[184:187], v[62:65]
	v_mfma_f32_16x16x32_bf16 v[58:61], v[160:163], v[184:187], v[58:61]
	v_mfma_f32_16x16x32_bf16 v[46:49], v[146:149], v[192:195], v[46:49]
	v_mfma_f32_16x16x32_bf16 v[42:45], v[160:163], v[192:195], v[42:45]
	v_mfma_f32_16x16x32_bf16 v[30:33], v[146:149], v[200:203], v[30:33]
	v_mfma_f32_16x16x32_bf16 v[26:29], v[160:163], v[200:203], v[26:29]
	v_mfma_f32_16x16x32_bf16 v[14:17], v[146:149], v[208:211], v[14:17]
	v_mfma_f32_16x16x32_bf16 v[10:13], v[160:163], v[208:211], v[10:13]
	v_mfma_f32_16x16x32_bf16 v[62:65], v[156:159], v[188:191], v[62:65]
	v_mfma_f32_16x16x32_bf16 v[58:61], v[164:167], v[188:191], v[58:61]
	v_mfma_f32_16x16x32_bf16 v[46:49], v[156:159], v[196:199], v[46:49]
	v_mfma_f32_16x16x32_bf16 v[42:45], v[164:167], v[196:199], v[42:45]
	v_mfma_f32_16x16x32_bf16 v[30:33], v[156:159], v[204:207], v[30:33]
	v_mfma_f32_16x16x32_bf16 v[26:29], v[164:167], v[204:207], v[26:29]
	v_mfma_f32_16x16x32_bf16 v[14:17], v[156:159], v[212:215], v[14:17]
	v_mfma_f32_16x16x32_bf16 v[10:13], v[164:167], v[212:215], v[10:13]
	v_mfma_f32_16x16x32_bf16 v[54:57], v[168:171], v[184:187], v[54:57]
	v_mfma_f32_16x16x32_bf16 v[50:53], v[176:179], v[184:187], v[50:53]
	v_mfma_f32_16x16x32_bf16 v[38:41], v[168:171], v[192:195], v[38:41]
	v_mfma_f32_16x16x32_bf16 v[34:37], v[176:179], v[192:195], v[34:37]
	v_mfma_f32_16x16x32_bf16 v[22:25], v[168:171], v[200:203], v[22:25]
	v_mfma_f32_16x16x32_bf16 v[18:21], v[176:179], v[200:203], v[18:21]
	v_mfma_f32_16x16x32_bf16 v[6:9], v[168:171], v[208:211], v[6:9]
	v_mfma_f32_16x16x32_bf16 v[2:5], v[176:179], v[208:211], v[2:5]
	v_mfma_f32_16x16x32_bf16 v[54:57], v[172:175], v[188:191], v[54:57]
	v_mfma_f32_16x16x32_bf16 v[50:53], v[180:183], v[188:191], v[50:53]
	v_mfma_f32_16x16x32_bf16 v[38:41], v[172:175], v[196:199], v[38:41]
	v_mfma_f32_16x16x32_bf16 v[34:37], v[180:183], v[196:199], v[34:37]
	v_mfma_f32_16x16x32_bf16 v[22:25], v[172:175], v[204:207], v[22:25]
	v_mfma_f32_16x16x32_bf16 v[18:21], v[180:183], v[204:207], v[18:21]
	v_mfma_f32_16x16x32_bf16 v[6:9], v[172:175], v[212:215], v[6:9]
	v_mfma_f32_16x16x32_bf16 v[2:5], v[180:183], v[212:215], v[2:5]
	s_barrier
	s_add_i32 s52, s52, 2
	s_add_u32 s50, s50, 0x100
	s_addc_u32 s51, s51, 0
	s_cmp_gt_u32 s52, 41
	s_mov_b64 s[2:3], s[22:23]
	s_cbranch_scc0 .LBB0_1867
	s_and_b64 vcc, exec, s[14:15]
	s_cbranch_vccz .LBB0_1870
	s_barrier
